# MoE GEMM1 gather tokens cached in VGPRs + saddr LDS-DMA, attention block loop rewritten branch-free, staging loads batched, C1/attn rebalance 4-2-5, GEMM1 acc zero-init folded into MFMA C=0
# speedup vs baseline: 1.0274x; 1.0274x over previous
; #define LAS __attribute__((address_space(3)))
; __device__ __forceinline__ int tid_hidden() { int t = threadIdx.x; asm volatile("" : "+v"(t)); return t; }
; #define lds lds_hidden(lds0)
; #define SSQ WSP(float, W_SSQ)
; __device__ __forceinline__ void attn_phase(LAS unsigned char* lds, const bf16_t* __restrict__ QA, const bf16_t* __restrict__ KA, const bf16_t* __restrict__ VTA, ...
;     const int tid = tid_hidden(), wid = __builtin_amdgcn_readfirstlane(tid >> 6), lane = tid & 63, l15 = lane & 15, g4 = lane >> 4;
;     for (int it = 0; it < count; ++it) {
;         const int item = first + it * stride;
;         const int b = item >> 5, qb = (item >> 1) & 15, kvh = item & 1;
;         const int kb0 = qb * 128 - 128;
;         unsigned z0 = 0u; asm volatile("" : "+v"(z0));
;         const u32x4 zz = (u32x4){z0, z0, z0, z0};
;         const int hg = wid >> 1, head = kvh * 4 + hg, half = wid & 1;
;         const int kc0 = ((g4 ^ (l15 & 7)) * 16);
;         const float sk = sink_l[head];
;         bf16x8 q0n, q1n;
;         { const size_t tokn = (size_t)b * SEQ + qb * 128 + half * 64 + l15;
;           q0n = *(const bf16x8*)(QA + tokn * 512 + head * 64 + 8 * g4); q1n = *(const bf16x8*)(QA + tokn * 512 + head * 64 + 32 + 8 * g4); }
; __global__ void __launch_bounds__(512, 2) fwd(Args a) {
;     ...
;                 const int af = c_ < 64 ? 0 : (c_ < 128 ? (c_ - 64) * 2 : 128 + (c_ - 128)), an = c_ < 64 ? 0 : (c_ < 128 ? 2 : 1);
;                 const int cf = c_ < 64 ? c_ * 5 : (c_ < 128 ? 320 + (c_ - 64) : 384 + (c_ - 128) * 5), cn = c_ < 64 ? 5 : (c_ < 128 ? 1 : 5);
.LBB0_734:
	s_cmpk_lt_i32 s36, 0x80
	s_cselect_b64 s[2:3], -1, 0
	s_cmpk_gt_i32 s36, 0x7f
	s_cselect_b64 s[0:1], -1, 0
	s_mov_b64 s[64:65], 0x4000
	s_mov_b64 s[68:69], 0x1000
	s_mov_b64 s[70:71], 0x1800
	s_mul_i32 s28, s36, 4
	s_cmpk_lt_u32 s36, 0x40
	s_cbranch_scc1 .Lcf_done
	s_mul_i32 s28, s36, 2
	s_addk_i32 s28, 128
	s_cmpk_lt_u32 s36, 0x80
	s_cbranch_scc1 .Lcf_done
	s_mul_i32 s28, s36, 5
	s_addk_i32 s28, -256
.Lcf_done:
.LBB0_741:
	s_mov_b32 s30, s91
	s_mov_b64 s[0:1], s[86:87]
	s_load_dwordx2 s[0:1], s[0:1], 0xa8
	s_mov_b64 s[6:7], s[86:87]
	s_mov_b64 s[8:9], s[86:87]
	s_mov_b64 s[10:11], s[86:87]
	v_mov_b32_e32 v2, v0
	s_waitcnt lgkmcnt(0)
	s_add_u32 s18, s0, 0xa008000
	s_addc_u32 s19, s1, 0
	s_load_dwordx2 s[0:1], s[6:7], 0xa8
	s_waitcnt lgkmcnt(0)
	s_add_u32 s6, s0, 0xb008000
	s_addc_u32 s7, s1, 0
	s_load_dwordx2 s[0:1], s[8:9], 0xa8
	s_mov_b64 s[8:9], s[86:87]
	s_waitcnt lgkmcnt(0)
	s_add_u32 s20, s0, 0xb408000
	s_addc_u32 s21, s1, 0
	s_load_dwordx2 s[0:1], s[10:11], 0xa8
	s_mov_b64 s[10:11], s[86:87]
	s_waitcnt lgkmcnt(0)
	s_add_u32 s0, s0, 0x12808000
	s_addc_u32 s1, s1, 0
	s_load_dwordx2 s[10:11], s[10:11], 0xa8
	s_waitcnt lgkmcnt(0)
	s_add_u32 s22, s10, 0x13808000
	s_addc_u32 s23, s11, 0
	s_andn2_b64 vcc, exec, s[4:5]
	v_readfirstlane_b32 s4, v2
	s_cbranch_vccnz .LBB0_943
	s_load_dwordx2 s[8:9], s[8:9], 0x38
	s_lshl_b32 s90, s40, 3
	s_lshl_b64 s[10:11], s[90:91], 2
	v_lshrrev_b32_e32 v3, 4, v2
	v_and_b32_e32 v4, 7, v2
	s_waitcnt lgkmcnt(0)
	s_add_u32 s31, s8, s10
	s_addc_u32 s34, s9, s11
	s_and_b64 s[2:3], s[2:3], exec
	v_bitop3_b32 v3, v3, v4, 3 bitop3:0x6c
	s_waitcnt vmcnt(0)
	v_lshlrev_b32_e32 v11, 4, v3
	v_lshlrev_b32_e32 v3, 4, v2
	s_movk_i32 s2, 0x80
	s_cselect_b32 s35, 2, 1
	s_ashr_i32 s37, s4, 7
	s_bfe_u32 s16, s4, 0x10006
	v_and_b32_e32 v4, 0x70, v3
	v_mov_b32_e32 v5, v35
	v_cmp_gt_i32_e64 s[4:5], s2, v2
	s_movk_i32 s2, 0xc0
	v_lshl_add_u64 v[90:91], s[6:7], 0, v[4:5]
	v_and_b32_e32 v3, 0xffffff80, v3
	v_cmp_gt_i32_e64 s[6:7], s2, v2
	s_mov_b32 s2, 0x55555556
	v_add_u32_e32 v5, s30, v3
	v_mul_hi_i32 v3, v2, s2
	v_lshrrev_b32_e32 v6, 31, v3
	v_add_u32_e32 v3, v3, v6
	s_mov_b32 s2, 0xffffffd
	s_movk_i32 s10, 0x330
	v_mul_lo_u32 v6, v3, s2
	v_mul_lo_u32 v3, v3, s10
	v_ashrrev_i32_e32 v114, 3, v2
	v_add_u32_e32 v13, s30, v3
	v_add_lshl_u32 v15, v6, v2, 4
	v_xor_b32_e32 v3, v114, v2
	v_add_u32_e32 v6, 0x200, v2
	v_lshlrev_b32_e32 v3, 4, v3
	v_ashrrev_i32_e32 v115, 3, v6
	v_and_b32_e32 v19, 0x70, v3
	v_xor_b32_e32 v3, v115, v2
	v_add_u32_e32 v8, 0x400, v2
	v_lshlrev_b32_e32 v3, 4, v3
	v_ashrrev_i32_e32 v116, 3, v8
	v_and_b32_e32 v21, 0x70, v3
	v_xor_b32_e32 v3, v116, v2
	v_add_u32_e32 v10, 0x600, v2
	v_lshlrev_b32_e32 v3, 4, v3
	v_ashrrev_i32_e32 v117, 3, v10
	v_and_b32_e32 v23, 0x70, v3
	v_xor_b32_e32 v3, v117, v2
	v_add_u32_e32 v12, 0x800, v2
	v_lshlrev_b32_e32 v3, 4, v3
	v_ashrrev_i32_e32 v118, 3, v12
	v_and_b32_e32 v25, 0x70, v3
	v_xor_b32_e32 v3, v118, v2
	v_add_u32_e32 v14, 0xa00, v2
	v_lshlrev_b32_e32 v3, 4, v3
	v_ashrrev_i32_e32 v119, 3, v14
	v_and_b32_e32 v27, 0x70, v3
	v_xor_b32_e32 v3, v119, v2
	v_lshlrev_b32_e32 v3, 4, v3
	s_mov_b32 s11, 0x2aaaaaab
	v_and_b32_e32 v29, 0x70, v3
	v_mul_hi_i32 v3, v2, s11
	v_lshrrev_b32_e32 v30, 31, v3
	v_ashrrev_i32_e32 v3, 3, v3
	v_add_u32_e32 v92, v3, v30
	s_movk_i32 s12, 0xffd0
	v_and_b32_e32 v7, 15, v2
	v_bfe_u32 v9, v2, 4, 2
	v_mad_u64_u32 v[2:3], s[2:3], v92, s12, v[2:3]
	v_lshlrev_b32_e32 v120, 3, v2
	v_mul_lo_u32 v3, v92, s10
	v_lshlrev_b32_e32 v31, 4, v2
	v_mul_hi_i32 v2, v6, s11
	v_add_u32_e32 v30, s30, v3
	v_lshrrev_b32_e32 v3, 31, v2
	v_ashrrev_i32_e32 v2, 3, v2
	v_add_u32_e32 v94, v2, v3
	v_mad_u64_u32 v[2:3], s[2:3], v94, s12, v[6:7]
	v_lshlrev_b32_e32 v121, 3, v2
	v_mul_lo_u32 v3, v94, s10
	v_lshlrev_b32_e32 v32, 4, v2
	v_mul_hi_i32 v2, v8, s11
	v_add_u32_e32 v6, s30, v3
	v_lshrrev_b32_e32 v3, 31, v2
	v_ashrrev_i32_e32 v2, 3, v2
	v_add_u32_e32 v96, v2, v3
	v_mad_u64_u32 v[2:3], s[2:3], v96, s12, v[8:9]
	v_lshlrev_b32_e32 v122, 3, v2
	v_mul_lo_u32 v3, v96, s10
	v_lshlrev_b32_e32 v33, 4, v2
	v_mul_hi_i32 v2, v10, s11
	v_add_u32_e32 v8, s30, v3
	v_lshrrev_b32_e32 v3, 31, v2
	v_ashrrev_i32_e32 v2, 3, v2
	v_add_u32_e32 v98, v2, v3
	v_mad_u64_u32 v[2:3], s[2:3], v98, s12, v[10:11]
	v_lshlrev_b32_e32 v123, 3, v2
	v_mul_lo_u32 v3, v98, s10
	v_lshlrev_b32_e32 v36, 4, v2
	v_mul_hi_i32 v2, v12, s11
	v_add_u32_e32 v10, s30, v3
	v_lshrrev_b32_e32 v3, 31, v2
	v_ashrrev_i32_e32 v2, 3, v2
	v_add_u32_e32 v100, v2, v3
	v_mad_u64_u32 v[2:3], s[2:3], v100, s12, v[12:13]
	v_lshlrev_b32_e32 v124, 3, v2
	v_mul_lo_u32 v3, v100, s10
	v_lshlrev_b32_e32 v37, 4, v2
	v_mul_hi_i32 v2, v14, s11
	v_add_u32_e32 v12, s30, v3
	v_lshrrev_b32_e32 v3, 31, v2
	v_ashrrev_i32_e32 v2, 3, v2
	v_add_u32_e32 v102, v2, v3
	v_mad_u64_u32 v[2:3], s[2:3], v102, s12, v[14:15]
	v_lshlrev_b32_e32 v17, 2, v9
	v_mul_lo_u32 v3, v102, s10
	v_lshlrev_b32_e32 v125, 3, v2
	v_add_u32_e32 v14, s30, v3
	v_lshlrev_b32_e32 v38, 4, v2
	v_sub_u32_e32 v2, v17, v7
	s_movk_i32 s2, 0x101
	v_or_b32_e32 v3, 0x100, v17
	v_cmp_gt_u32_e64 s[10:11], s2, v2
	v_sub_u32_e32 v3, v3, v7
	s_movk_i32 s2, 0xfe
	v_lshlrev_b32_e32 v34, 3, v9
	v_mul_u32_u24_e32 v2, 0x330, v7
	v_cmp_gt_u32_e64 s[14:15], s2, v3
	s_lshl_b32 s2, s16, 7
	v_add3_u32 v126, v2, s2, v34
	v_lshlrev_b32_e32 v2, 7, v7
	s_lshl_b32 s38, s16, 6
	v_xor_b32_e32 v16, 64, v11
	v_lshl_or_b32 v2, s16, 13, v2
	s_lshl_b32 s40, s29, 6
	v_lshl_add_u32 v18, v114, 7, s30
	v_lshl_add_u32 v20, v115, 7, s30
	v_lshl_add_u32 v22, v116, 7, s30
	v_lshl_add_u32 v24, v117, 7, s30
	v_lshl_add_u32 v26, v118, 7, s30
	v_lshl_add_u32 v28, v119, 7, s30
	v_cmp_gt_u32_e64 s[12:13], s33, v3
	v_or_b32_e32 v127, v2, v16
	v_or_b32_e32 v128, v2, v11
	s_bitcmp1_b32 s29, 0
	v_lshlrev_b32_e32 v2, 4, v9
	v_mov_b32_e32 v3, v35
	v_or_b32_e32 v88, s38, v7
	v_mov_b32_e32 v89, v35
	s_mov_b32 s39, 0
	v_cmp_eq_u32_e64 s[8:9], 0, v9
	v_ashrrev_i32_e32 v93, 31, v92
	v_ashrrev_i32_e32 v95, 31, v94
	v_ashrrev_i32_e32 v97, 31, v96
	v_ashrrev_i32_e32 v99, 31, v98
	v_ashrrev_i32_e32 v101, 31, v100
	v_ashrrev_i32_e32 v103, 31, v102
	v_or_b32_e32 v129, s38, v17
	s_cselect_b64 s[24:25], -1, 0
	s_lshl_b32 s41, s37, 6
	v_lshl_add_u64 v[104:105], s[18:19], 0, v[2:3]
	v_lshl_add_u64 v[106:107], s[0:1], 0, v[34:35]
	v_lshlrev_b32_e32 v34, 1, v34
	v_add_u32_e32 v130, v18, v19
	v_add_u32_e32 v131, v20, v21
	v_add_u32_e32 v132, v22, v23
	v_add_u32_e32 v133, v24, v25
	v_add_u32_e32 v134, v26, v27
	v_add_u32_e32 v135, v28, v29
	v_add_u32_e32 v136, v5, v4
	v_add_u32_e32 v137, v30, v31
	v_add_u32_e32 v138, v6, v32
	v_add_u32_e32 v139, v8, v33
	v_add_u32_e32 v140, v10, v36
	v_add_u32_e32 v141, v12, v37
	v_add_u32_e32 v142, v14, v38
	v_add_u32_e32 v143, v13, v15
	s_branch .LBB0_744

; #define LAS __attribute__((address_space(3)))
; #define lds lds_hidden(lds0)
; __device__ __forceinline__ void attn_phase(LAS unsigned char* lds, const bf16_t* __restrict__ QA, const bf16_t* __restrict__ KA, const bf16_t* __restrict__ VTA, ...
;     ...
;         { const size_t tokn = (size_t)b * SEQ + qb * 128 + half * 64 + l15;
;           q0n = *(const bf16x8*)(QA + tokn * 512 + head * 64 + 8 * g4); q1n = *(const bf16x8*)(QA + tokn * 512 + head * 64 + 32 + 8 * g4); }
;         __syncthreads();
; #pragma unroll
;         for (int i = 0; i < 6; ++i) {
;             const int ch = tid + i * 512, kap = ch >> 3, part = ch & 7, kpos = kb0 + kap;
;             u32x4 v = zz;
;             if (kpos >= 0 && kpos < SEQ) v = *(const u32x4*)(KA + (size_t)(b * SEQ + kpos) * 128 + kvh * 64 + part * 8);
;             *(LAS u32x4*)(lds + kap * KROW + ((part ^ (kap & 7)) * 16)) = v;
;         }
;         if (tid < 128) { const int kap = 384 + (tid >> 3), part = tid & 7; *(LAS u32x4*)(lds + kap * KROW + part * 16) = zz; }
; #pragma unroll
;         for (int i = 0; i < 6; ++i) {
;             const int ch = tid + i * 512, d = ch / 48, kc = ch - d * 48, kpos = kb0 + kc * 8;
;             u32x4 v = zz;
;             if (kpos >= 0 && kpos < SEQ) v = *(const u32x4*)(VTA + ((size_t)b * 128 + kvh * 64 + d) * SEQ + kpos);
;             *(LAS u32x4*)(lds + V_OFF + d * VROW + kc * 16) = v;
;         }
;         if (tid < 192) { const int d = tid / 3, kc = 48 + (tid - d * 3); *(LAS u32x4*)(lds + V_OFF + d * VROW + kc * 16) = zz; }
.LBB0_744:
	s_add_i32 s0, s39, s29
	s_ashr_i32 s2, s0, 5
	s_and_b32 s27, s0, 1
	s_lshl_b32 s0, s0, 6
	s_and_b32 s42, s0, 0x780
	s_lshl_b32 s0, s27, 2
	s_add_i32 s16, s0, s37
	s_ashr_i32 s17, s16, 31
	s_add_i32 s26, s42, 0xffffff80
	s_lshl_b64 s[0:1], s[16:17], 2
	s_add_u32 s0, s31, s0
	v_mov_b32_e32 v2, v35
	s_addc_u32 s1, s34, s1
	s_ashr_i32 s3, s2, 31
	global_load_dword v144, v35, s[0:1]
	s_lshl_b64 s[0:1], s[2:3], 11
	s_or_b32 s17, s0, s42
	v_mov_b32_e32 v5, s1
	v_or_b32_e32 v4, s17, v88
	v_lshlrev_b64 v[4:5], 10, v[4:5]
	s_lshl_b32 s16, s16, 6
	v_lshl_add_u64 v[4:5], s[18:19], 0, v[4:5]
	s_ashr_i32 s17, s16, 31
	v_lshl_add_u64 v[4:5], s[16:17], 1, v[4:5]
	v_lshl_add_u64 v[4:5], v[4:5], 0, v[34:35]
	global_load_dwordx4 v[14:17], v[4:5], off
	global_load_dwordx4 v[10:13], v[4:5], off offset:64
	s_lshl_b32 s90, s27, 7
	s_movk_i32 s43, 0x800
	s_lshl_b32 s42, s2, 11
	v_lshl_add_u64 v[18:19], v[90:91], 0, s[90:91]
	v_add_u32_e32 v3, s26, v114
	v_mov_b32_e32 v182, v35
	v_mov_b32_e32 v183, v35
	v_mov_b32_e32 v184, v35
	v_mov_b32_e32 v185, v35
	v_cmp_gt_u32_e32 vcc, s43, v3
	s_and_saveexec_b64 s[16:17], vcc
	v_or_b32_e32 v4, s42, v3
	v_ashrrev_i32_e32 v5, 31, v4
	v_lshlrev_b64 v[4:5], 8, v[4:5]
	v_lshl_add_u64 v[4:5], v[18:19], 0, v[4:5]
	global_load_dwordx4 v[182:185], v[4:5], off
	s_or_b64 exec, exec, s[16:17]
	v_add_u32_e32 v3, s26, v115
	v_mov_b32_e32 v186, v35
	v_mov_b32_e32 v187, v35
	v_mov_b32_e32 v188, v35
	v_mov_b32_e32 v189, v35
	v_cmp_gt_u32_e32 vcc, s43, v3
	s_and_saveexec_b64 s[16:17], vcc
	v_or_b32_e32 v4, s42, v3
	v_ashrrev_i32_e32 v5, 31, v4
	v_lshlrev_b64 v[4:5], 8, v[4:5]
	v_lshl_add_u64 v[4:5], v[18:19], 0, v[4:5]
	global_load_dwordx4 v[186:189], v[4:5], off
	s_or_b64 exec, exec, s[16:17]
	v_add_u32_e32 v3, s26, v116
	v_mov_b32_e32 v190, v35
	v_mov_b32_e32 v191, v35
	v_mov_b32_e32 v192, v35
	v_mov_b32_e32 v193, v35
	v_cmp_gt_u32_e32 vcc, s43, v3
	s_and_saveexec_b64 s[16:17], vcc
	v_or_b32_e32 v4, s42, v3
	v_ashrrev_i32_e32 v5, 31, v4
	v_lshlrev_b64 v[4:5], 8, v[4:5]
	v_lshl_add_u64 v[4:5], v[18:19], 0, v[4:5]
	global_load_dwordx4 v[190:193], v[4:5], off
	s_or_b64 exec, exec, s[16:17]
	v_add_u32_e32 v3, s26, v117
	v_mov_b32_e32 v194, v35
	v_mov_b32_e32 v195, v35
	v_mov_b32_e32 v196, v35
	v_mov_b32_e32 v197, v35
	v_cmp_gt_u32_e32 vcc, s43, v3
	s_and_saveexec_b64 s[16:17], vcc
	v_or_b32_e32 v4, s42, v3
	v_ashrrev_i32_e32 v5, 31, v4
	v_lshlrev_b64 v[4:5], 8, v[4:5]
	v_lshl_add_u64 v[4:5], v[18:19], 0, v[4:5]
	global_load_dwordx4 v[194:197], v[4:5], off
	s_or_b64 exec, exec, s[16:17]
	v_add_u32_e32 v3, s26, v118
	v_mov_b32_e32 v198, v35
	v_mov_b32_e32 v199, v35
	v_mov_b32_e32 v200, v35
	v_mov_b32_e32 v201, v35
	v_cmp_gt_u32_e32 vcc, s43, v3
	s_and_saveexec_b64 s[16:17], vcc
	v_or_b32_e32 v4, s42, v3
	v_ashrrev_i32_e32 v5, 31, v4
	v_lshlrev_b64 v[4:5], 8, v[4:5]
	v_lshl_add_u64 v[4:5], v[18:19], 0, v[4:5]
	global_load_dwordx4 v[198:201], v[4:5], off
	s_or_b64 exec, exec, s[16:17]
	v_add_u32_e32 v3, s26, v119
	v_mov_b32_e32 v202, v35
	v_mov_b32_e32 v203, v35
	v_mov_b32_e32 v204, v35
	v_mov_b32_e32 v205, v35
	v_cmp_gt_u32_e32 vcc, s43, v3
	s_and_saveexec_b64 s[16:17], vcc
	v_or_b32_e32 v4, s42, v3
	v_ashrrev_i32_e32 v5, 31, v4
	v_lshlrev_b64 v[4:5], 8, v[4:5]
	v_lshl_add_u64 v[4:5], v[18:19], 0, v[4:5]
	global_load_dwordx4 v[202:205], v[4:5], off
	s_or_b64 exec, exec, s[16:17]
	s_lshl_b32 s90, s27, 6
	s_lshl_b64 s[2:3], s[2:3], 7
	s_movk_i32 s27, 0x800
	s_or_b64 s[2:3], s[2:3], s[90:91]
	v_add_u32_e32 v6, s26, v120
	v_mov_b32_e32 v206, v35
	v_mov_b32_e32 v207, v35
	v_mov_b32_e32 v208, v35
	v_mov_b32_e32 v209, v35
	v_cmp_gt_u32_e32 vcc, s27, v6
	s_and_saveexec_b64 s[16:17], vcc
	v_lshl_add_u64 v[4:5], s[2:3], 0, v[92:93]
	v_lshlrev_b64 v[4:5], 12, v[4:5]
	v_lshl_add_u64 v[4:5], s[20:21], 0, v[4:5]
	v_mov_b32_e32 v7, v35
	v_lshl_add_u64 v[4:5], v[6:7], 1, v[4:5]
	global_load_dwordx4 v[206:209], v[4:5], off
	s_or_b64 exec, exec, s[16:17]
	v_add_u32_e32 v6, s26, v121
	v_mov_b32_e32 v210, v35
	v_mov_b32_e32 v211, v35
	v_mov_b32_e32 v212, v35
	v_mov_b32_e32 v213, v35
	v_cmp_gt_u32_e32 vcc, s27, v6
	s_and_saveexec_b64 s[16:17], vcc
	v_lshl_add_u64 v[4:5], s[2:3], 0, v[94:95]
	v_lshlrev_b64 v[4:5], 12, v[4:5]
	v_lshl_add_u64 v[4:5], s[20:21], 0, v[4:5]
	v_mov_b32_e32 v7, v35
	v_lshl_add_u64 v[4:5], v[6:7], 1, v[4:5]
	global_load_dwordx4 v[210:213], v[4:5], off
	s_or_b64 exec, exec, s[16:17]
	v_add_u32_e32 v6, s26, v122
	v_mov_b32_e32 v214, v35
	v_mov_b32_e32 v215, v35
	v_mov_b32_e32 v216, v35
	v_mov_b32_e32 v217, v35
	v_cmp_gt_u32_e32 vcc, s27, v6
	s_and_saveexec_b64 s[16:17], vcc
	v_lshl_add_u64 v[4:5], s[2:3], 0, v[96:97]
	v_lshlrev_b64 v[4:5], 12, v[4:5]
	v_lshl_add_u64 v[4:5], s[20:21], 0, v[4:5]
	v_mov_b32_e32 v7, v35
	v_lshl_add_u64 v[4:5], v[6:7], 1, v[4:5]
	global_load_dwordx4 v[214:217], v[4:5], off
	s_or_b64 exec, exec, s[16:17]
	v_add_u32_e32 v6, s26, v123
	v_mov_b32_e32 v218, v35
	v_mov_b32_e32 v219, v35
	v_mov_b32_e32 v220, v35
	v_mov_b32_e32 v221, v35
	v_cmp_gt_u32_e32 vcc, s27, v6
	s_and_saveexec_b64 s[16:17], vcc
	v_lshl_add_u64 v[4:5], s[2:3], 0, v[98:99]
	v_lshlrev_b64 v[4:5], 12, v[4:5]
	v_lshl_add_u64 v[4:5], s[20:21], 0, v[4:5]
	v_mov_b32_e32 v7, v35
	v_lshl_add_u64 v[4:5], v[6:7], 1, v[4:5]
	global_load_dwordx4 v[218:221], v[4:5], off
	s_or_b64 exec, exec, s[16:17]
	v_add_u32_e32 v6, s26, v124
	v_mov_b32_e32 v222, v35
	v_mov_b32_e32 v223, v35
	v_mov_b32_e32 v224, v35
	v_mov_b32_e32 v225, v35
	v_cmp_gt_u32_e32 vcc, s27, v6
	s_and_saveexec_b64 s[16:17], vcc
	v_lshl_add_u64 v[4:5], s[2:3], 0, v[100:101]
	v_lshlrev_b64 v[4:5], 12, v[4:5]
	v_lshl_add_u64 v[4:5], s[20:21], 0, v[4:5]
	v_mov_b32_e32 v7, v35
	v_lshl_add_u64 v[4:5], v[6:7], 1, v[4:5]
	global_load_dwordx4 v[222:225], v[4:5], off
	s_or_b64 exec, exec, s[16:17]
	v_add_u32_e32 v6, s26, v125
	v_mov_b32_e32 v226, v35
	v_mov_b32_e32 v227, v35
	v_mov_b32_e32 v228, v35
	v_mov_b32_e32 v229, v35
	v_cmp_gt_u32_e32 vcc, s27, v6
	s_and_saveexec_b64 s[16:17], vcc
	v_lshl_add_u64 v[4:5], s[2:3], 0, v[102:103]
	v_lshlrev_b64 v[4:5], 12, v[4:5]
	v_lshl_add_u64 v[4:5], s[20:21], 0, v[4:5]
	v_mov_b32_e32 v7, v35
	v_lshl_add_u64 v[4:5], v[6:7], 1, v[4:5]
	global_load_dwordx4 v[226:229], v[4:5], off
	s_or_b64 exec, exec, s[16:17]
	v_mov_b32_e32 v3, v35
	v_mov_b32_e32 v4, v35
	v_mov_b32_e32 v5, v35
	s_barrier
; #define LAS __attribute__((address_space(3)))
; #define lds lds_hidden(lds0)
; __device__ __forceinline__ void attn_phase(LAS unsigned char* lds, const bf16_t* __restrict__ QA, const bf16_t* __restrict__ KA, const bf16_t* __restrict__ VTA, ...
;     ...
;             *(LAS u32x4*)(lds + kap * KROW + ((part ^ (kap & 7)) * 16)) = v;
;         }
;         if (tid < 128) { const int kap = 384 + (tid >> 3), part = tid & 7; *(LAS u32x4*)(lds + kap * KROW + part * 16) = zz; }
; #pragma unroll
;         for (int i = 0; i < 6; ++i) {
;             const int ch = tid + i * 512, d = ch / 48, kc = ch - d * 48, kpos = kb0 + kc * 8;
;             u32x4 v = zz;
;             if (kpos >= 0 && kpos < SEQ) v = *(const u32x4*)(VTA + ((size_t)b * 128 + kvh * 64 + d) * SEQ + kpos);
;             *(LAS u32x4*)(lds + V_OFF + d * VROW + kc * 16) = v;
;         }
;         if (tid < 192) { const int d = tid / 3, kc = 48 + (tid - d * 3); *(LAS u32x4*)(lds + V_OFF + d * VROW + kc * 16) = zz; }
;         __syncthreads();
; #pragma unroll 1
;         for (int blk = 0; blk < 4; ++blk) {
;             const int t0 = half * 4 + blk, qr0 = t0 * 16, qo = qr0 + l15;
;             const size_t tok = (size_t)b * SEQ + qb * 128 + qo;
;             const bf16x8 q0 = q0n, q1 = q1n;
;             if (blk < 3) { const size_t tokn = tok + 16; q0n = *(const bf16x8*)(QA + tokn * 512 + head * 64 + 8 * g4); q1n = *(const bf16x8*)(QA + tokn * 512 + head * 64 + 32 + 8 * g4); }
	s_waitcnt vmcnt(0)
	ds_write_b128 v130, v[182:185]
	ds_write_b128 v131, v[186:189]
	ds_write_b128 v132, v[190:193]
	ds_write_b128 v133, v[194:197]
	ds_write_b128 v134, v[198:201]
	ds_write_b128 v135, v[202:205]
	s_and_saveexec_b64 s[16:17], s[4:5]
	ds_write_b128 v136, v[2:5] offset:49152
	s_or_b64 exec, exec, s[16:17]
	ds_write_b128 v137, v[206:209] offset:51200
	ds_write_b128 v138, v[210:213] offset:51200
	ds_write_b128 v139, v[214:217] offset:51200
	ds_write_b128 v140, v[218:221] offset:51200
	ds_write_b128 v141, v[222:225] offset:51200
	ds_write_b128 v142, v[226:229] offset:51200
	s_and_saveexec_b64 s[2:3], s[6:7]
	ds_write_b128 v143, v[2:5] offset:51968
	s_or_b64 exec, exec, s[2:3]
	v_cndmask_b32_e64 v2, 0, 1, s[24:25]
	s_and_b32 s43, s40, 0x780
	v_readfirstlane_b32 s16, v2
	s_lshl_b32 s2, s16, 2
	s_lshl_b32 s16, s16, 8
	s_add_i32 s2, s37, s2
	s_add_i32 s16, s41, s16
	s_ashr_i32 s3, s2, 31
	s_ashr_i32 s17, s16, 31
	s_or_b32 s42, s38, s43
	s_lshl_b64 s[2:3], s[2:3], 2
	s_lshl_b64 s[26:27], s[16:17], 1
	s_add_u32 s0, s43, s0
	s_addc_u32 s1, 0, s1
	v_lshl_add_u64 v[2:3], s[0:1], 0, v[88:89]
	s_add_u32 s0, s22, s2
	v_lshlrev_b64 v[4:5], 5, v[2:3]
	s_addc_u32 s1, s23, s3
	v_lshlrev_b64 v[2:3], 10, v[2:3]
	v_lshl_add_u64 v[108:109], s[0:1], 0, v[4:5]
	v_lshl_add_u64 v[110:111], v[104:105], 0, v[2:3]
	v_lshl_add_u64 v[112:113], v[106:107], 0, v[2:3]
	v_mov_b64_e32 v[2:3], v[10:11]
	v_mov_b64_e32 v[6:7], v[14:15]
	s_mov_b32 s43, 0
	v_mov_b32_e32 v145, v128
	v_mov_b32_e32 v146, v127
	v_mov_b32_e32 v147, v126
	v_mov_b64_e32 v[4:5], v[12:13]
	v_mov_b64_e32 v[8:9], v[16:17]
	s_waitcnt lgkmcnt(0)
	s_barrier
	s_branch .LBB0_774

; #define LAS __attribute__((address_space(3)))
; __device__ __forceinline__ float kf(float x) { asm volatile("" : "+s"(x)); return x; }
; #define lds lds_hidden(lds0)
; __device__ __forceinline__ void attn_phase(LAS unsigned char* lds, const bf16_t* __restrict__ QA, const bf16_t* __restrict__ KA, const bf16_t* __restrict__ VTA, ...
;     ...
;             const int t0 = half * 4 + blk, qr0 = t0 * 16, qo = qr0 + l15;
;             const size_t tok = (size_t)b * SEQ + qb * 128 + qo;
;             const bf16x8 q0 = q0n, q1 = q1n;
;             if (blk < 3) { const size_t tokn = tok + 16; q0n = *(const bf16x8*)(QA + tokn * 512 + head * 64 + 8 * g4); q1n = *(const bf16x8*)(QA + tokn * 512 + head * 64 + 32 + 8 * g4); }
;             f32x4 sc[18];
;             float mx = sk;
; #pragma unroll
;             for (int i = 0; i < 18; ++i) {
;                 const LAS unsigned char* kp = lds + ((t0 + i) * 16 + l15) * KROW;
;                 const bf16x8 k0 = *(const LAS bf16x8*)(kp + kc0), k1 = *(const LAS bf16x8*)(kp + (kc0 ^ 64));
;                 f32x4 a = (f32x4){0.f, 0.f, 0.f, 0.f};
;                 a = __builtin_amdgcn_mfma_f32_16x16x32_bf16(k0, q0, a, 0, 0, 0);
;                 a = __builtin_amdgcn_mfma_f32_16x16x32_bf16(k1, q1, a, 0, 0, 0);
; #pragma unroll
;                 for (int r = 0; r < 4; ++r) {
;                     const int kap = (t0 + i) * 16 + 4 * g4 + r, rel = kap - qo, kpos = kb0 + kap;
;                     const bool ok = (rel >= 0) && (rel <= 256) && (kpos >= 0) && (kpos < SEQ);
;                     a[r] = ok ? a[r] : kf(-1e30f);
;                     mx = fmaxf(mx, a[r]);
;                 }
;                 sc[i] = a;
;             }
.LBB0_776:
	v_add_u32_e32 v148, s30, v145
	v_add_u32_e32 v149, s30, v146
	ds_read_b128 v[36:39], v148
	ds_read_b128 v[40:43], v149
	ds_read_b128 v[44:47], v148 offset:2048
	ds_read_b128 v[48:51], v149 offset:2048
	ds_read_b128 v[52:55], v148 offset:4096
	ds_read_b128 v[56:59], v149 offset:4096
	v_sub_u32_e32 v150, v129, v88
	v_add_u32_e32 v160, s30, v147
	v_add_u32_e32 v151, 0xc800, v160
	v_add_u32_e32 v152, 0xfb00, v160
	v_add_u32_e32 v153, 0x12e00, v160
	v_add_u32_e32 v154, 0x16100, v160
	s_add_i32 s44, s42, s43
	s_mov_b32 s16, 0x3fb8aa3b
	v_mbcnt_lo_u32_b32 v161, -1, 0
	v_mbcnt_hi_u32_b32 v161, -1, v161
	v_lshlrev_b32_e32 v161, 2, v161
	v_xor_b32_e32 v158, 64, v161
	v_xor_b32_e32 v159, 0x80, v161
	v_mov_b32_e32 v155, v144
	v_mov_b32_e32 v180, 0xf149f2ca
	s_waitcnt lgkmcnt(4)
	v_mfma_f32_16x16x32_bf16 v[182:185], v[36:39], v[14:17], 0
	v_mfma_f32_16x16x32_bf16 v[182:185], v[40:43], v[10:13], v[182:185]
	ds_read_b128 v[60:63], v148 offset:6144
	ds_read_b128 v[64:67], v149 offset:6144
	s_waitcnt lgkmcnt(4)
	v_mfma_f32_16x16x32_bf16 v[186:189], v[44:47], v[14:17], 0
	v_mfma_f32_16x16x32_bf16 v[186:189], v[48:51], v[10:13], v[186:189]
	ds_read_b128 v[36:39], v148 offset:8192
	ds_read_b128 v[40:43], v149 offset:8192
	s_waitcnt lgkmcnt(4)
	v_mfma_f32_16x16x32_bf16 v[190:193], v[52:55], v[14:17], 0
	v_mfma_f32_16x16x32_bf16 v[190:193], v[56:59], v[10:13], v[190:193]
	ds_read_b128 v[44:47], v148 offset:10240
	ds_read_b128 v[48:51], v149 offset:10240
	s_add_i32 s17, s44, -128
	s_cmpk_lt_u32 s17, 0x800
	s_cselect_b64 s[0:1], -1, 0
	v_cmp_le_i32_e32 vcc, 0, v150
	s_and_b64 vcc, vcc, s[0:1]
	v_cndmask_b32_e32 v182, v180, v182, vcc
	v_cmp_le_i32_e32 vcc, -1, v150
	s_and_b64 vcc, vcc, s[0:1]
	v_cndmask_b32_e32 v183, v180, v183, vcc
	v_cmp_le_i32_e32 vcc, -2, v150
	s_and_b64 vcc, vcc, s[0:1]
	v_cndmask_b32_e32 v184, v180, v184, vcc
	v_cmp_le_i32_e32 vcc, -3, v150
	s_and_b64 vcc, vcc, s[0:1]
	v_cndmask_b32_e32 v185, v180, v185, vcc
	v_max3_f32 v155, v155, v182, v183
	v_max3_f32 v155, v155, v184, v185
	s_waitcnt lgkmcnt(4)
	v_mfma_f32_16x16x32_bf16 v[194:197], v[60:63], v[14:17], 0
	v_mfma_f32_16x16x32_bf16 v[194:197], v[64:67], v[10:13], v[194:197]
	ds_read_b128 v[52:55], v148 offset:12288
	ds_read_b128 v[56:59], v149 offset:12288
	s_add_i32 s17, s44, -112
	s_cmpk_lt_u32 s17, 0x800
	s_cselect_b64 vcc, -1, 0
	v_cndmask_b32_e32 v186, v180, v186, vcc
	v_cndmask_b32_e32 v187, v180, v187, vcc
	v_cndmask_b32_e32 v188, v180, v188, vcc
	v_cndmask_b32_e32 v189, v180, v189, vcc
	v_max3_f32 v155, v155, v186, v187
	v_max3_f32 v155, v155, v188, v189
	s_waitcnt lgkmcnt(4)
	v_mfma_f32_16x16x32_bf16 v[198:201], v[36:39], v[14:17], 0
	v_mfma_f32_16x16x32_bf16 v[198:201], v[40:43], v[10:13], v[198:201]
	ds_read_b128 v[60:63], v148 offset:14336
	ds_read_b128 v[64:67], v149 offset:14336
	s_add_i32 s17, s44, -96
	s_cmpk_lt_u32 s17, 0x800
	s_cselect_b64 vcc, -1, 0
	v_cndmask_b32_e32 v190, v180, v190, vcc
	v_cndmask_b32_e32 v191, v180, v191, vcc
	v_cndmask_b32_e32 v192, v180, v192, vcc
	v_cndmask_b32_e32 v193, v180, v193, vcc
	v_max3_f32 v155, v155, v190, v191
	v_max3_f32 v155, v155, v192, v193
	s_waitcnt lgkmcnt(4)
	v_mfma_f32_16x16x32_bf16 v[202:205], v[44:47], v[14:17], 0
	v_mfma_f32_16x16x32_bf16 v[202:205], v[48:51], v[10:13], v[202:205]
	ds_read_b128 v[36:39], v148 offset:16384
	ds_read_b128 v[40:43], v149 offset:16384
	s_add_i32 s17, s44, -80
	s_cmpk_lt_u32 s17, 0x800
	s_cselect_b64 vcc, -1, 0
	v_cndmask_b32_e32 v194, v180, v194, vcc
	v_cndmask_b32_e32 v195, v180, v195, vcc
	v_cndmask_b32_e32 v196, v180, v196, vcc
	v_cndmask_b32_e32 v197, v180, v197, vcc
	v_max3_f32 v155, v155, v194, v195
	v_max3_f32 v155, v155, v196, v197
	s_waitcnt lgkmcnt(4)
	v_mfma_f32_16x16x32_bf16 v[206:209], v[52:55], v[14:17], 0
	v_mfma_f32_16x16x32_bf16 v[206:209], v[56:59], v[10:13], v[206:209]
	ds_read_b128 v[44:47], v148 offset:18432
	ds_read_b128 v[48:51], v149 offset:18432
	s_add_i32 s17, s44, -64
	s_cmpk_lt_u32 s17, 0x800
	s_cselect_b64 vcc, -1, 0
	v_cndmask_b32_e32 v198, v180, v198, vcc
	v_cndmask_b32_e32 v199, v180, v199, vcc
	v_cndmask_b32_e32 v200, v180, v200, vcc
	v_cndmask_b32_e32 v201, v180, v201, vcc
	v_max3_f32 v155, v155, v198, v199
	v_max3_f32 v155, v155, v200, v201
	s_waitcnt lgkmcnt(4)
	v_mfma_f32_16x16x32_bf16 v[210:213], v[60:63], v[14:17], 0
	v_mfma_f32_16x16x32_bf16 v[210:213], v[64:67], v[10:13], v[210:213]
	ds_read_b128 v[52:55], v148 offset:20480
	ds_read_b128 v[56:59], v149 offset:20480
	s_add_i32 s17, s44, -48
	s_cmpk_lt_u32 s17, 0x800
	s_cselect_b64 vcc, -1, 0
	v_cndmask_b32_e32 v202, v180, v202, vcc
	v_cndmask_b32_e32 v203, v180, v203, vcc
	v_cndmask_b32_e32 v204, v180, v204, vcc
	v_cndmask_b32_e32 v205, v180, v205, vcc
	v_max3_f32 v155, v155, v202, v203
	v_max3_f32 v155, v155, v204, v205
	s_waitcnt lgkmcnt(4)
	v_mfma_f32_16x16x32_bf16 v[214:217], v[36:39], v[14:17], 0
	v_mfma_f32_16x16x32_bf16 v[214:217], v[40:43], v[10:13], v[214:217]
	ds_read_b128 v[60:63], v148 offset:22528
	ds_read_b128 v[64:67], v149 offset:22528
	s_add_i32 s17, s44, -32
	s_cmpk_lt_u32 s17, 0x800
	s_cselect_b64 vcc, -1, 0
	v_cndmask_b32_e32 v206, v180, v206, vcc
	v_cndmask_b32_e32 v207, v180, v207, vcc
	v_cndmask_b32_e32 v208, v180, v208, vcc
	v_cndmask_b32_e32 v209, v180, v209, vcc
	v_max3_f32 v155, v155, v206, v207
	v_max3_f32 v155, v155, v208, v209
	s_waitcnt lgkmcnt(4)
	v_mfma_f32_16x16x32_bf16 v[218:221], v[44:47], v[14:17], 0
	v_mfma_f32_16x16x32_bf16 v[218:221], v[48:51], v[10:13], v[218:221]
	ds_read_b128 v[36:39], v148 offset:24576
	ds_read_b128 v[40:43], v149 offset:24576
	s_add_i32 s17, s44, -16
	s_cmpk_lt_u32 s17, 0x800
	s_cselect_b64 vcc, -1, 0
	v_cndmask_b32_e32 v210, v180, v210, vcc
	v_cndmask_b32_e32 v211, v180, v211, vcc
	v_cndmask_b32_e32 v212, v180, v212, vcc
	v_cndmask_b32_e32 v213, v180, v213, vcc
	v_max3_f32 v155, v155, v210, v211
	v_max3_f32 v155, v155, v212, v213
	s_waitcnt lgkmcnt(4)
; #define LAS __attribute__((address_space(3)))
; __device__ __forceinline__ float kf(float x) { asm volatile("" : "+s"(x)); return x; }
; __device__ __forceinline__ float shx(float v, int m) { int ln; asm volatile("v_mbcnt_lo_u32_b32 %0, -1, 0\n\tv_mbcnt_hi_u32_b32 %0, -1, %0" : "=v"(ln)); return __builtin_bit_cast(float, __builtin_amdgcn_ds_bpermute((ln ^ m) << 2, __builtin_bit_cast(int, v))); }
; #define lds lds_hidden(lds0)
; __device__ __forceinline__ void attn_phase(LAS unsigned char* lds, const bf16_t* __restrict__ QA, const bf16_t* __restrict__ KA, const bf16_t* __restrict__ VTA, ...
;     ...
;             for (int i = 0; i < 18; ++i) {
;                 const LAS unsigned char* kp = lds + ((t0 + i) * 16 + l15) * KROW;
;                 const bf16x8 k0 = *(const LAS bf16x8*)(kp + kc0), k1 = *(const LAS bf16x8*)(kp + (kc0 ^ 64));
;                 f32x4 a = (f32x4){0.f, 0.f, 0.f, 0.f};
;                 a = __builtin_amdgcn_mfma_f32_16x16x32_bf16(k0, q0, a, 0, 0, 0);
;                 a = __builtin_amdgcn_mfma_f32_16x16x32_bf16(k1, q1, a, 0, 0, 0);
; #pragma unroll
;                 for (int r = 0; r < 4; ++r) {
;                     const int kap = (t0 + i) * 16 + 4 * g4 + r, rel = kap - qo, kpos = kb0 + kap;
;                     const bool ok = (rel >= 0) && (rel <= 256) && (kpos >= 0) && (kpos < SEQ);
;                     a[r] = ok ? a[r] : kf(-1e30f);
;                     mx = fmaxf(mx, a[r]);
;                 }
;                 sc[i] = a;
;             }
;             mx = fmaxf(mx, shx(mx, 16)); mx = fmaxf(mx, shx(mx, 32));
	v_mfma_f32_16x16x32_bf16 v[222:225], v[52:55], v[14:17], 0
	v_mfma_f32_16x16x32_bf16 v[222:225], v[56:59], v[10:13], v[222:225]
	ds_read_b128 v[44:47], v148 offset:26624
	ds_read_b128 v[48:51], v149 offset:26624
	s_add_i32 s17, s44, 0
	s_cmpk_lt_u32 s17, 0x800
	s_cselect_b64 vcc, -1, 0
	v_cndmask_b32_e32 v214, v180, v214, vcc
	v_cndmask_b32_e32 v215, v180, v215, vcc
	v_cndmask_b32_e32 v216, v180, v216, vcc
	v_cndmask_b32_e32 v217, v180, v217, vcc
	v_max3_f32 v155, v155, v214, v215
	v_max3_f32 v155, v155, v216, v217
	s_waitcnt lgkmcnt(4)
	v_mfma_f32_16x16x32_bf16 v[226:229], v[60:63], v[14:17], 0
	v_mfma_f32_16x16x32_bf16 v[226:229], v[64:67], v[10:13], v[226:229]
	ds_read_b128 v[52:55], v148 offset:28672
	ds_read_b128 v[56:59], v149 offset:28672
	s_add_i32 s17, s44, 16
	s_cmpk_lt_u32 s17, 0x800
	s_cselect_b64 vcc, -1, 0
	v_cndmask_b32_e32 v218, v180, v218, vcc
	v_cndmask_b32_e32 v219, v180, v219, vcc
	v_cndmask_b32_e32 v220, v180, v220, vcc
	v_cndmask_b32_e32 v221, v180, v221, vcc
	v_max3_f32 v155, v155, v218, v219
	v_max3_f32 v155, v155, v220, v221
	s_waitcnt lgkmcnt(4)
	v_mfma_f32_16x16x32_bf16 v[230:233], v[36:39], v[14:17], 0
	v_mfma_f32_16x16x32_bf16 v[230:233], v[40:43], v[10:13], v[230:233]
	ds_read_b128 v[60:63], v148 offset:30720
	ds_read_b128 v[64:67], v149 offset:30720
	s_add_i32 s17, s44, 32
	s_cmpk_lt_u32 s17, 0x800
	s_cselect_b64 vcc, -1, 0
	v_cndmask_b32_e32 v222, v180, v222, vcc
	v_cndmask_b32_e32 v223, v180, v223, vcc
	v_cndmask_b32_e32 v224, v180, v224, vcc
	v_cndmask_b32_e32 v225, v180, v225, vcc
	v_max3_f32 v155, v155, v222, v223
	v_max3_f32 v155, v155, v224, v225
	s_waitcnt lgkmcnt(4)
	v_mfma_f32_16x16x32_bf16 v[234:237], v[44:47], v[14:17], 0
	v_mfma_f32_16x16x32_bf16 v[234:237], v[48:51], v[10:13], v[234:237]
	ds_read_b128 v[36:39], v148 offset:32768
	ds_read_b128 v[40:43], v149 offset:32768
	s_add_i32 s17, s44, 48
	s_cmpk_lt_u32 s17, 0x800
	s_cselect_b64 vcc, -1, 0
	v_cndmask_b32_e32 v226, v180, v226, vcc
	v_cndmask_b32_e32 v227, v180, v227, vcc
	v_cndmask_b32_e32 v228, v180, v228, vcc
	v_cndmask_b32_e32 v229, v180, v229, vcc
	v_max3_f32 v155, v155, v226, v227
	v_max3_f32 v155, v155, v228, v229
	s_waitcnt lgkmcnt(4)
	v_mfma_f32_16x16x32_bf16 v[238:241], v[52:55], v[14:17], 0
	v_mfma_f32_16x16x32_bf16 v[238:241], v[56:59], v[10:13], v[238:241]
	s_add_i32 s17, s44, 64
	s_cmpk_lt_u32 s17, 0x800
	s_cselect_b64 vcc, -1, 0
	v_cndmask_b32_e32 v230, v180, v230, vcc
	v_cndmask_b32_e32 v231, v180, v231, vcc
	v_cndmask_b32_e32 v232, v180, v232, vcc
	v_cndmask_b32_e32 v233, v180, v233, vcc
	v_max3_f32 v155, v155, v230, v231
	v_max3_f32 v155, v155, v232, v233
	s_waitcnt lgkmcnt(2)
	v_mfma_f32_16x16x32_bf16 v[242:245], v[60:63], v[14:17], 0
	v_mfma_f32_16x16x32_bf16 v[242:245], v[64:67], v[10:13], v[242:245]
	s_add_i32 s17, s44, 80
	s_cmpk_lt_u32 s17, 0x800
	s_cselect_b64 vcc, -1, 0
	v_cndmask_b32_e32 v234, v180, v234, vcc
	v_cndmask_b32_e32 v235, v180, v235, vcc
	v_cndmask_b32_e32 v236, v180, v236, vcc
	v_cndmask_b32_e32 v237, v180, v237, vcc
	v_max3_f32 v155, v155, v234, v235
	v_max3_f32 v155, v155, v236, v237
	s_waitcnt lgkmcnt(0)
	v_mfma_f32_16x16x32_bf16 v[246:249], v[36:39], v[14:17], 0
	v_mfma_f32_16x16x32_bf16 v[246:249], v[40:43], v[10:13], v[246:249]
	s_add_i32 s17, s44, 96
	s_cmpk_lt_u32 s17, 0x800
	s_cselect_b64 vcc, -1, 0
	v_cndmask_b32_e32 v238, v180, v238, vcc
	v_cndmask_b32_e32 v239, v180, v239, vcc
	v_cndmask_b32_e32 v240, v180, v240, vcc
	v_cndmask_b32_e32 v241, v180, v241, vcc
	v_max3_f32 v155, v155, v238, v239
	v_max3_f32 v155, v155, v240, v241
	s_add_i32 s17, s44, 112
	s_cmpk_lt_u32 s17, 0x800
	s_cselect_b64 vcc, -1, 0
	v_cndmask_b32_e32 v242, v180, v242, vcc
	v_cndmask_b32_e32 v243, v180, v243, vcc
	v_cndmask_b32_e32 v244, v180, v244, vcc
	v_cndmask_b32_e32 v245, v180, v245, vcc
	v_max3_f32 v155, v155, v242, v243
	v_max3_f32 v155, v155, v244, v245
	s_add_i32 s17, s44, 128
	s_cmpk_lt_u32 s17, 0x800
	s_cselect_b64 s[0:1], -1, 0
	v_cmp_ge_i32_e32 vcc, 0, v150
	s_and_b64 vcc, vcc, s[0:1]
	v_cndmask_b32_e32 v246, v180, v246, vcc
	v_cmp_ge_i32_e32 vcc, -1, v150
	s_and_b64 vcc, vcc, s[0:1]
	v_cndmask_b32_e32 v247, v180, v247, vcc
	v_cmp_ge_i32_e32 vcc, -2, v150
	s_and_b64 vcc, vcc, s[0:1]
	v_cndmask_b32_e32 v248, v180, v248, vcc
	v_cmp_ge_i32_e32 vcc, -3, v150
	s_and_b64 vcc, vcc, s[0:1]
	v_cndmask_b32_e32 v249, v180, v249, vcc
	v_max3_f32 v155, v155, v246, v247
	v_max3_f32 v155, v155, v248, v249
	ds_bpermute_b32 v160, v158, v155
	s_waitcnt lgkmcnt(0)
	v_max_f32_e32 v155, v155, v160
	ds_bpermute_b32 v160, v159, v155
	ds_read2_b64 v[76:79], v151 offset0:0 offset1:4
	ds_read2_b64 v[80:83], v152 offset0:0 offset1:4
	ds_read2_b64 v[84:87], v153 offset0:0 offset1:4
	ds_read2_b64 v[162:165], v154 offset0:0 offset1:4
	ds_read2_b64 v[166:169], v151 offset0:8 offset1:12
	s_waitcnt lgkmcnt(5)
; __device__ __forceinline__ unsigned cvt_pk_bf16(float lo, float hi) { const bf16x2_t r = __builtin_convertvector((f32x2_t){lo, hi}, bf16x2_t); return __builtin_bit_cast(unsigned, r); }
; __device__ __forceinline__ float fexp(float x) { return __builtin_amdgcn_exp2f(x * 1.4426950408889634f); }
; __device__ __forceinline__ float shx(float v, int m) { int ln; asm volatile("v_mbcnt_lo_u32_b32 %0, -1, 0\n\tv_mbcnt_hi_u32_b32 %0, -1, %0" : "=v"(ln)); return __builtin_bit_cast(float, __builtin_amdgcn_ds_bpermute((ln ^ m) << 2, __builtin_bit_cast(int, v))); }
; __device__ __forceinline__ void attn_phase(LAS unsigned char* lds, const bf16_t* __restrict__ QA, const bf16_t* __restrict__ KA, const bf16_t* __restrict__ VTA, ...
;     ...
;             mx = fmaxf(mx, shx(mx, 16)); mx = fmaxf(mx, shx(mx, 32));
;             float sum = 0.f;
; #pragma unroll
;             for (int i = 0; i < 18; ++i)
; #pragma unroll
;                 for (int r = 0; r < 4; ++r) { const float p = fexp(sc[i][r] - mx); sc[i][r] = p; sum += p; }
;             sum += shx(sum, 16); sum += shx(sum, 32);
;             sum += fexp(sk - mx);
;             f32x4 o[4];
; #pragma unroll
;             for (int dt = 0; dt < 4; ++dt) o[dt] = (f32x4){0.f, 0.f, 0.f, 0.f};
; #pragma unroll
;             for (int u = 0; u < 9; ++u) {
;                 u32x4 pw; pw.x = cvt_pk_bf16(sc[2 * u][0], sc[2 * u][1]); pw.y = cvt_pk_bf16(sc[2 * u][2], sc[2 * u][3]);
;                 pw.z = cvt_pk_bf16(sc[2 * u + 1][0], sc[2 * u + 1][1]); pw.w = cvt_pk_bf16(sc[2 * u + 1][2], sc[2 * u + 1][3]);
	v_max_f32_e32 v155, v155, v160
	v_mul_f32_e64 v157, -v155, s16
	v_fma_f32 v182, v182, s16, v157
	v_fma_f32 v183, v183, s16, v157
	v_fma_f32 v184, v184, s16, v157
	v_fma_f32 v185, v185, s16, v157
	v_fma_f32 v186, v186, s16, v157
	v_fma_f32 v187, v187, s16, v157
	v_fma_f32 v188, v188, s16, v157
	v_fma_f32 v189, v189, s16, v157
	v_fma_f32 v190, v190, s16, v157
	v_fma_f32 v191, v191, s16, v157
	v_fma_f32 v192, v192, s16, v157
	v_fma_f32 v193, v193, s16, v157
	v_fma_f32 v194, v194, s16, v157
	v_fma_f32 v195, v195, s16, v157
	v_fma_f32 v196, v196, s16, v157
	v_fma_f32 v197, v197, s16, v157
	v_fma_f32 v198, v198, s16, v157
	v_fma_f32 v199, v199, s16, v157
	v_fma_f32 v200, v200, s16, v157
	v_fma_f32 v201, v201, s16, v157
	v_fma_f32 v202, v202, s16, v157
	v_fma_f32 v203, v203, s16, v157
	v_fma_f32 v204, v204, s16, v157
	v_fma_f32 v205, v205, s16, v157
	v_fma_f32 v206, v206, s16, v157
	v_fma_f32 v207, v207, s16, v157
	v_fma_f32 v208, v208, s16, v157
	v_fma_f32 v209, v209, s16, v157
	v_fma_f32 v210, v210, s16, v157
	v_fma_f32 v211, v211, s16, v157
	v_fma_f32 v212, v212, s16, v157
	v_fma_f32 v213, v213, s16, v157
	v_fma_f32 v214, v214, s16, v157
	v_fma_f32 v215, v215, s16, v157
	v_fma_f32 v216, v216, s16, v157
	v_fma_f32 v217, v217, s16, v157
	v_fma_f32 v218, v218, s16, v157
	v_fma_f32 v219, v219, s16, v157
	v_fma_f32 v220, v220, s16, v157
	v_fma_f32 v221, v221, s16, v157
	v_fma_f32 v222, v222, s16, v157
	v_fma_f32 v223, v223, s16, v157
	v_fma_f32 v224, v224, s16, v157
	v_fma_f32 v225, v225, s16, v157
	v_fma_f32 v226, v226, s16, v157
	v_fma_f32 v227, v227, s16, v157
	v_fma_f32 v228, v228, s16, v157
	v_fma_f32 v229, v229, s16, v157
	v_fma_f32 v230, v230, s16, v157
	v_fma_f32 v231, v231, s16, v157
	v_fma_f32 v232, v232, s16, v157
	v_fma_f32 v233, v233, s16, v157
	v_fma_f32 v234, v234, s16, v157
	v_fma_f32 v235, v235, s16, v157
	v_fma_f32 v236, v236, s16, v157
	v_fma_f32 v237, v237, s16, v157
	v_fma_f32 v238, v238, s16, v157
	v_fma_f32 v239, v239, s16, v157
	v_fma_f32 v240, v240, s16, v157
	v_fma_f32 v241, v241, s16, v157
	v_fma_f32 v242, v242, s16, v157
	v_fma_f32 v243, v243, s16, v157
	v_fma_f32 v244, v244, s16, v157
	v_fma_f32 v245, v245, s16, v157
	v_fma_f32 v246, v246, s16, v157
	v_fma_f32 v247, v247, s16, v157
	v_fma_f32 v248, v248, s16, v157
	v_fma_f32 v249, v249, s16, v157
	v_exp_f32_e32 v182, v182
	v_exp_f32_e32 v183, v183
	v_mov_b32_e32 v156, v182
	v_exp_f32_e32 v184, v184
	v_mov_b32_e32 v161, v183
	v_exp_f32_e32 v185, v185
	v_add_f32_e32 v156, v156, v184
	v_exp_f32_e32 v186, v186
	v_add_f32_e32 v161, v161, v185
	v_exp_f32_e32 v187, v187
	v_add_f32_e32 v156, v156, v186
	v_exp_f32_e32 v188, v188
	v_add_f32_e32 v161, v161, v187
	v_exp_f32_e32 v189, v189
	v_add_f32_e32 v156, v156, v188
	v_exp_f32_e32 v190, v190
	v_add_f32_e32 v161, v161, v189
	v_exp_f32_e32 v191, v191
	v_add_f32_e32 v156, v156, v190
	v_exp_f32_e32 v192, v192
	v_add_f32_e32 v161, v161, v191
	v_exp_f32_e32 v193, v193
	v_add_f32_e32 v156, v156, v192
	v_exp_f32_e32 v194, v194
	v_add_f32_e32 v161, v161, v193
	v_exp_f32_e32 v195, v195
	v_add_f32_e32 v156, v156, v194
	v_exp_f32_e32 v196, v196
	v_add_f32_e32 v161, v161, v195
	v_exp_f32_e32 v197, v197
	v_add_f32_e32 v156, v156, v196
	v_exp_f32_e32 v198, v198
	v_add_f32_e32 v161, v161, v197
	v_exp_f32_e32 v199, v199
	v_add_f32_e32 v156, v156, v198
	v_exp_f32_e32 v200, v200
	v_add_f32_e32 v161, v161, v199
	v_exp_f32_e32 v201, v201
	v_add_f32_e32 v156, v156, v200
	v_exp_f32_e32 v202, v202
	v_add_f32_e32 v161, v161, v201
	v_exp_f32_e32 v203, v203
	v_add_f32_e32 v156, v156, v202
	v_exp_f32_e32 v204, v204
	v_add_f32_e32 v161, v161, v203
	v_exp_f32_e32 v205, v205
	v_add_f32_e32 v156, v156, v204
	v_exp_f32_e32 v206, v206
	v_add_f32_e32 v161, v161, v205
	v_exp_f32_e32 v207, v207
	v_add_f32_e32 v156, v156, v206
	v_exp_f32_e32 v208, v208
	v_add_f32_e32 v161, v161, v207
	v_exp_f32_e32 v209, v209
	v_add_f32_e32 v156, v156, v208
	v_exp_f32_e32 v210, v210
	v_add_f32_e32 v161, v161, v209
	v_exp_f32_e32 v211, v211
	v_add_f32_e32 v156, v156, v210
	v_exp_f32_e32 v212, v212
	v_add_f32_e32 v161, v161, v211
	v_exp_f32_e32 v213, v213
	v_add_f32_e32 v156, v156, v212
	v_exp_f32_e32 v214, v214
	v_add_f32_e32 v161, v161, v213
	v_exp_f32_e32 v215, v215
	v_add_f32_e32 v156, v156, v214
	v_exp_f32_e32 v216, v216
	v_add_f32_e32 v161, v161, v215
	v_exp_f32_e32 v217, v217
	v_add_f32_e32 v156, v156, v216
	v_exp_f32_e32 v218, v218
	v_add_f32_e32 v161, v161, v217
	v_exp_f32_e32 v219, v219
	v_add_f32_e32 v156, v156, v218
	v_exp_f32_e32 v220, v220
	v_add_f32_e32 v161, v161, v219
	v_exp_f32_e32 v221, v221
	v_add_f32_e32 v156, v156, v220
	v_exp_f32_e32 v222, v222
	v_add_f32_e32 v161, v161, v221
	v_exp_f32_e32 v223, v223
	v_add_f32_e32 v156, v156, v222
	v_exp_f32_e32 v224, v224
	v_add_f32_e32 v161, v161, v223
	v_exp_f32_e32 v225, v225
	v_add_f32_e32 v156, v156, v224
	v_exp_f32_e32 v226, v226
	v_add_f32_e32 v161, v161, v225
	v_exp_f32_e32 v227, v227
	v_add_f32_e32 v156, v156, v226
	v_exp_f32_e32 v228, v228
	v_add_f32_e32 v161, v161, v227
	v_exp_f32_e32 v229, v229
	v_add_f32_e32 v156, v156, v228
	v_exp_f32_e32 v230, v230
	v_add_f32_e32 v161, v161, v229
	v_exp_f32_e32 v231, v231
	v_add_f32_e32 v156, v156, v230
	v_exp_f32_e32 v232, v232
	v_add_f32_e32 v161, v161, v231
	v_exp_f32_e32 v233, v233
	v_add_f32_e32 v156, v156, v232
	v_exp_f32_e32 v234, v234
	v_add_f32_e32 v161, v161, v233
	v_exp_f32_e32 v235, v235
	v_add_f32_e32 v156, v156, v234
	v_exp_f32_e32 v236, v236
	v_add_f32_e32 v161, v161, v235
	v_exp_f32_e32 v237, v237
	v_add_f32_e32 v156, v156, v236
	v_exp_f32_e32 v238, v238
	v_add_f32_e32 v161, v161, v237
	v_exp_f32_e32 v239, v239
	v_add_f32_e32 v156, v156, v238
	v_exp_f32_e32 v240, v240
	v_add_f32_e32 v161, v161, v239
	v_exp_f32_e32 v241, v241
	v_add_f32_e32 v156, v156, v240
	v_exp_f32_e32 v242, v242
	v_add_f32_e32 v161, v161, v241
	v_exp_f32_e32 v243, v243
	v_add_f32_e32 v156, v156, v242
	v_exp_f32_e32 v244, v244
	v_add_f32_e32 v161, v161, v243
	v_exp_f32_e32 v245, v245
	v_add_f32_e32 v156, v156, v244
	v_exp_f32_e32 v246, v246
	v_add_f32_e32 v161, v161, v245
	v_exp_f32_e32 v247, v247
	v_add_f32_e32 v156, v156, v246
	v_exp_f32_e32 v248, v248
	v_add_f32_e32 v161, v161, v247
	v_exp_f32_e32 v249, v249
	v_add_f32_e32 v156, v156, v248
	s_nop 0
	v_add_f32_e32 v161, v161, v249
	v_add_f32_e32 v156, v156, v161
	v_fma_f32 v161, v144, s16, v157
	v_exp_f32_e32 v161, v161
	ds_bpermute_b32 v160, v158, v156
	v_cvt_pk_bf16_f32 v68, v182, v183
	v_cvt_pk_bf16_f32 v69, v184, v185
	v_cvt_pk_bf16_f32 v70, v186, v187
	v_cvt_pk_bf16_f32 v71, v188, v189
	s_waitcnt lgkmcnt(0)
; #define LAS __attribute__((address_space(3)))
; __device__ __forceinline__ unsigned cvt_pk_bf16(float lo, float hi) { const bf16x2_t r = __builtin_convertvector((f32x2_t){lo, hi}, bf16x2_t); return __builtin_bit_cast(unsigned, r); }
; #define lds lds_hidden(lds0)
; __device__ __forceinline__ void attn_phase(LAS unsigned char* lds, const bf16_t* __restrict__ QA, const bf16_t* __restrict__ KA, const bf16_t* __restrict__ VTA, ...
;     ...
; #pragma unroll
;             for (int u = 0; u < 9; ++u) {
;                 u32x4 pw; pw.x = cvt_pk_bf16(sc[2 * u][0], sc[2 * u][1]); pw.y = cvt_pk_bf16(sc[2 * u][2], sc[2 * u][3]);
;                 pw.z = cvt_pk_bf16(sc[2 * u + 1][0], sc[2 * u + 1][1]); pw.w = cvt_pk_bf16(sc[2 * u + 1][2], sc[2 * u + 1][3]);
;                 const bf16x8 pf = __builtin_bit_cast(bf16x8, pw);
; #pragma unroll
;                 for (int dt = 0; dt < 4; ++dt) {
;                     const LAS unsigned char* vp = lds + V_OFF + (dt * 16 + l15) * VROW + ((t0 + 2 * u) * 16 + 4 * g4) * 2;
;                     const u32x2 va = *(const LAS u32x2*)vp, vb = *(const LAS u32x2*)(vp + 32);
;                     const bf16x8 vf = __builtin_bit_cast(bf16x8, (u32x4){va.x, va.y, vb.x, vb.y});
;                     o[dt] = __builtin_amdgcn_mfma_f32_16x16x32_bf16(vf, pf, o[dt], 0, 0, 0);
;                 }
;             }
	v_add_f32_e32 v156, v156, v160
	ds_bpermute_b32 v160, v159, v156
	v_cvt_pk_bf16_f32 v72, v190, v191
	v_cvt_pk_bf16_f32 v73, v192, v193
	v_cvt_pk_bf16_f32 v74, v194, v195
	v_cvt_pk_bf16_f32 v75, v196, v197
	v_mfma_f32_16x16x32_bf16 v[18:21], v[76:79], v[68:71], 0
	ds_read2_b64 v[170:173], v152 offset0:8 offset1:12
	v_mfma_f32_16x16x32_bf16 v[22:25], v[80:83], v[68:71], 0
	ds_read2_b64 v[76:79], v153 offset0:8 offset1:12
	v_mfma_f32_16x16x32_bf16 v[26:29], v[84:87], v[68:71], 0
	ds_read2_b64 v[80:83], v154 offset0:8 offset1:12
	v_mfma_f32_16x16x32_bf16 v[30:33], v[162:165], v[68:71], 0
	ds_read2_b64 v[84:87], v151 offset0:16 offset1:20
	v_cvt_pk_bf16_f32 v68, v198, v199
	v_cvt_pk_bf16_f32 v69, v200, v201
	v_cvt_pk_bf16_f32 v70, v202, v203
	v_cvt_pk_bf16_f32 v71, v204, v205
	v_mfma_f32_16x16x32_bf16 v[18:21], v[166:169], v[72:75], v[18:21]
	ds_read2_b64 v[162:165], v152 offset0:16 offset1:20
	s_waitcnt lgkmcnt(4)
	v_add_f32_e32 v156, v156, v160
	v_add_f32_e32 v156, v156, v161
	v_mfma_f32_16x16x32_bf16 v[22:25], v[170:173], v[72:75], v[22:25]
	ds_read2_b64 v[166:169], v153 offset0:16 offset1:20
	s_waitcnt lgkmcnt(4)
	v_mfma_f32_16x16x32_bf16 v[26:29], v[76:79], v[72:75], v[26:29]
	ds_read2_b64 v[170:173], v154 offset0:16 offset1:20
	s_waitcnt lgkmcnt(4)
	v_mfma_f32_16x16x32_bf16 v[30:33], v[80:83], v[72:75], v[30:33]
	ds_read2_b64 v[76:79], v151 offset0:24 offset1:28
	v_cvt_pk_bf16_f32 v72, v206, v207
	v_cvt_pk_bf16_f32 v73, v208, v209
	v_cvt_pk_bf16_f32 v74, v210, v211
	v_cvt_pk_bf16_f32 v75, v212, v213
	s_waitcnt lgkmcnt(4)
	v_mfma_f32_16x16x32_bf16 v[18:21], v[84:87], v[68:71], v[18:21]
	ds_read2_b64 v[80:83], v152 offset0:24 offset1:28
	s_waitcnt lgkmcnt(4)
	v_mfma_f32_16x16x32_bf16 v[22:25], v[162:165], v[68:71], v[22:25]
	ds_read2_b64 v[84:87], v153 offset0:24 offset1:28
	s_waitcnt lgkmcnt(4)
	v_mfma_f32_16x16x32_bf16 v[26:29], v[166:169], v[68:71], v[26:29]
	ds_read2_b64 v[162:165], v154 offset0:24 offset1:28
	s_waitcnt lgkmcnt(4)
	v_mfma_f32_16x16x32_bf16 v[30:33], v[170:173], v[68:71], v[30:33]
	ds_read2_b64 v[166:169], v151 offset0:32 offset1:36
	v_cvt_pk_bf16_f32 v68, v214, v215
	v_cvt_pk_bf16_f32 v69, v216, v217
	v_cvt_pk_bf16_f32 v70, v218, v219
	v_cvt_pk_bf16_f32 v71, v220, v221
	s_waitcnt lgkmcnt(4)
	v_mfma_f32_16x16x32_bf16 v[18:21], v[76:79], v[72:75], v[18:21]
	ds_read2_b64 v[170:173], v152 offset0:32 offset1:36
	s_waitcnt lgkmcnt(4)
	v_mfma_f32_16x16x32_bf16 v[22:25], v[80:83], v[72:75], v[22:25]
	ds_read2_b64 v[76:79], v153 offset0:32 offset1:36
	s_waitcnt lgkmcnt(4)
	v_mfma_f32_16x16x32_bf16 v[26:29], v[84:87], v[72:75], v[26:29]
	ds_read2_b64 v[80:83], v154 offset0:32 offset1:36
	s_waitcnt lgkmcnt(4)
	v_mfma_f32_16x16x32_bf16 v[30:33], v[162:165], v[72:75], v[30:33]
	ds_read2_b64 v[84:87], v151 offset0:40 offset1:44
	v_cvt_pk_bf16_f32 v72, v222, v223
	v_cvt_pk_bf16_f32 v73, v224, v225
	v_cvt_pk_bf16_f32 v74, v226, v227
	v_cvt_pk_bf16_f32 v75, v228, v229
	s_waitcnt lgkmcnt(4)
	v_mfma_f32_16x16x32_bf16 v[18:21], v[166:169], v[68:71], v[18:21]
	ds_read2_b64 v[162:165], v152 offset0:40 offset1:44
	s_waitcnt lgkmcnt(4)
	v_mfma_f32_16x16x32_bf16 v[22:25], v[170:173], v[68:71], v[22:25]
	ds_read2_b64 v[166:169], v153 offset0:40 offset1:44
	s_waitcnt lgkmcnt(4)
	v_mfma_f32_16x16x32_bf16 v[26:29], v[76:79], v[68:71], v[26:29]
	ds_read2_b64 v[170:173], v154 offset0:40 offset1:44
	s_waitcnt lgkmcnt(4)
	v_mfma_f32_16x16x32_bf16 v[30:33], v[80:83], v[68:71], v[30:33]
	ds_read2_b64 v[76:79], v151 offset0:48 offset1:52
	v_cvt_pk_bf16_f32 v68, v230, v231
	v_cvt_pk_bf16_f32 v69, v232, v233
	v_cvt_pk_bf16_f32 v70, v234, v235
	v_cvt_pk_bf16_f32 v71, v236, v237
	s_waitcnt lgkmcnt(4)
	v_mfma_f32_16x16x32_bf16 v[18:21], v[84:87], v[72:75], v[18:21]
	ds_read2_b64 v[80:83], v152 offset0:48 offset1:52
	s_waitcnt lgkmcnt(4)
	v_mfma_f32_16x16x32_bf16 v[22:25], v[162:165], v[72:75], v[22:25]
	ds_read2_b64 v[84:87], v153 offset0:48 offset1:52
	s_waitcnt lgkmcnt(4)
	v_mfma_f32_16x16x32_bf16 v[26:29], v[166:169], v[72:75], v[26:29]
	ds_read2_b64 v[162:165], v154 offset0:48 offset1:52
	s_waitcnt lgkmcnt(4)
; #define LAS __attribute__((address_space(3)))
; __device__ __forceinline__ unsigned cvt_pk_bf16(float lo, float hi) { const bf16x2_t r = __builtin_convertvector((f32x2_t){lo, hi}, bf16x2_t); return __builtin_bit_cast(unsigned, r); }
; __device__ __forceinline__ float shx(float v, int m) { int ln; asm volatile("v_mbcnt_lo_u32_b32 %0, -1, 0\n\tv_mbcnt_hi_u32_b32 %0, -1, %0" : "=v"(ln)); return __builtin_bit_cast(float, __builtin_amdgcn_ds_bpermute((ln ^ m) << 2, __builtin_bit_cast(int, v))); }
; #define lds lds_hidden(lds0)
; #define SSQ WSP(float, W_SSQ)
; __device__ __forceinline__ void attn_phase(LAS unsigned char* lds, const bf16_t* __restrict__ QA, const bf16_t* __restrict__ KA, const bf16_t* __restrict__ VTA, ...
;     ...
;             for (int u = 0; u < 9; ++u) {
;                 u32x4 pw; pw.x = cvt_pk_bf16(sc[2 * u][0], sc[2 * u][1]); pw.y = cvt_pk_bf16(sc[2 * u][2], sc[2 * u][3]);
;                 pw.z = cvt_pk_bf16(sc[2 * u + 1][0], sc[2 * u + 1][1]); pw.w = cvt_pk_bf16(sc[2 * u + 1][2], sc[2 * u + 1][3]);
;                 const bf16x8 pf = __builtin_bit_cast(bf16x8, pw);
; #pragma unroll
;                 for (int dt = 0; dt < 4; ++dt) {
;                     const LAS unsigned char* vp = lds + V_OFF + (dt * 16 + l15) * VROW + ((t0 + 2 * u) * 16 + 4 * g4) * 2;
;                     const u32x2 va = *(const LAS u32x2*)vp, vb = *(const LAS u32x2*)(vp + 32);
;                     const bf16x8 vf = __builtin_bit_cast(bf16x8, (u32x4){va.x, va.y, vb.x, vb.y});
;                     o[dt] = __builtin_amdgcn_mfma_f32_16x16x32_bf16(vf, pf, o[dt], 0, 0, 0);
;                 }
;             }
;             const float inv = 1.f / sum;
;             float ss = 0.f;
; #pragma unroll
;             for (int dt = 0; dt < 4; ++dt) {
;                 const f32x4 v = o[dt] * inv;
;                 ss += v[0] * v[0] + v[1] * v[1] + v[2] * v[2] + v[3] * v[3];
;                 u32x2 w; w.x = cvt_pk_bf16(v[0], v[1]); w.y = cvt_pk_bf16(v[2], v[3]);
;                 *(u32x2*)(AO + tok * 512 + head * 64 + dt * 16 + 4 * g4) = w;
;             }
;             ss += shx(ss, 16); ss += shx(ss, 32);
;             if (g4 == 0) SSQ[tok * 8 + head] = ss;
	v_mfma_f32_16x16x32_bf16 v[30:33], v[170:173], v[72:75], v[30:33]
	ds_read2_b64 v[166:169], v151 offset0:56 offset1:60
	v_cvt_pk_bf16_f32 v72, v238, v239
	v_cvt_pk_bf16_f32 v73, v240, v241
	v_cvt_pk_bf16_f32 v74, v242, v243
	v_cvt_pk_bf16_f32 v75, v244, v245
	s_waitcnt lgkmcnt(4)
	v_mfma_f32_16x16x32_bf16 v[18:21], v[76:79], v[68:71], v[18:21]
	ds_read2_b64 v[170:173], v152 offset0:56 offset1:60
	s_waitcnt lgkmcnt(4)
	v_mfma_f32_16x16x32_bf16 v[22:25], v[80:83], v[68:71], v[22:25]
	ds_read2_b64 v[76:79], v153 offset0:56 offset1:60
	s_waitcnt lgkmcnt(4)
	v_mfma_f32_16x16x32_bf16 v[26:29], v[84:87], v[68:71], v[26:29]
	ds_read2_b64 v[80:83], v154 offset0:56 offset1:60
	s_waitcnt lgkmcnt(4)
	v_mfma_f32_16x16x32_bf16 v[30:33], v[162:165], v[68:71], v[30:33]
	ds_read2_b64 v[84:87], v151 offset0:64 offset1:68
	v_cvt_pk_bf16_f32 v68, v246, v247
	v_cvt_pk_bf16_f32 v69, v248, v249
	v_mov_b32_e32 v70, 0
	v_mov_b32_e32 v71, 0
	s_waitcnt lgkmcnt(4)
	v_mfma_f32_16x16x32_bf16 v[18:21], v[166:169], v[72:75], v[18:21]
	ds_read2_b64 v[162:165], v152 offset0:64 offset1:68
	s_waitcnt lgkmcnt(4)
	v_mfma_f32_16x16x32_bf16 v[22:25], v[170:173], v[72:75], v[22:25]
	ds_read2_b64 v[166:169], v153 offset0:64 offset1:68
	s_waitcnt lgkmcnt(4)
	v_mfma_f32_16x16x32_bf16 v[26:29], v[76:79], v[72:75], v[26:29]
	ds_read2_b64 v[170:173], v154 offset0:64 offset1:68
	s_waitcnt lgkmcnt(4)
	v_mfma_f32_16x16x32_bf16 v[30:33], v[80:83], v[72:75], v[30:33]
	s_waitcnt lgkmcnt(3)
	v_mfma_f32_16x16x32_bf16 v[18:21], v[84:87], v[68:71], v[18:21]
	s_waitcnt lgkmcnt(2)
	v_mfma_f32_16x16x32_bf16 v[22:25], v[162:165], v[68:71], v[22:25]
	s_waitcnt lgkmcnt(1)
	v_mfma_f32_16x16x32_bf16 v[26:29], v[166:169], v[68:71], v[26:29]
	s_waitcnt lgkmcnt(0)
	v_mfma_f32_16x16x32_bf16 v[30:33], v[170:173], v[68:71], v[30:33]
	v_div_scale_f32 v174, s[0:1], v156, v156, 1.0
	v_rcp_f32_e32 v175, v174
	s_nop 0
	v_fma_f32 v176, -v174, v175, 1.0
	v_fmac_f32_e32 v175, v176, v175
	v_div_scale_f32 v176, vcc, 1.0, v156, 1.0
	v_mul_f32_e32 v177, v176, v175
	v_fma_f32 v178, -v174, v177, v176
	v_fmac_f32_e32 v177, v178, v175
	v_fma_f32 v174, -v174, v177, v176
	v_div_fmas_f32 v174, v174, v175, v177
	v_div_fixup_f32 v179, v174, v156, 1.0
	v_lshl_add_u64 v[176:177], v[112:113], 0, s[26:27]
	v_mul_f32_e32 v18, v179, v18
	v_mul_f32_e32 v19, v179, v19
	v_mul_f32_e32 v20, v179, v20
	v_mul_f32_e32 v21, v179, v21
	v_mul_f32_e32 v178, v18, v18
	v_fmac_f32_e32 v178, v19, v19
	v_fmac_f32_e32 v178, v20, v20
	v_fmac_f32_e32 v178, v21, v21
	v_cvt_pk_bf16_f32 v36, v18, v19
	v_cvt_pk_bf16_f32 v37, v20, v21
	global_store_dwordx2 v[176:177], v[36:37], off
	v_mul_f32_e32 v22, v179, v22
	v_mul_f32_e32 v23, v179, v23
	v_mul_f32_e32 v24, v179, v24
	v_mul_f32_e32 v25, v179, v25
	v_fmac_f32_e32 v178, v22, v22
	v_fmac_f32_e32 v178, v23, v23
	v_fmac_f32_e32 v178, v24, v24
	v_fmac_f32_e32 v178, v25, v25
	v_cvt_pk_bf16_f32 v38, v22, v23
	v_cvt_pk_bf16_f32 v39, v24, v25
	global_store_dwordx2 v[176:177], v[38:39], off offset:32
	v_mul_f32_e32 v26, v179, v26
	v_mul_f32_e32 v27, v179, v27
	v_mul_f32_e32 v28, v179, v28
	v_mul_f32_e32 v29, v179, v29
	v_fmac_f32_e32 v178, v26, v26
	v_fmac_f32_e32 v178, v27, v27
	v_fmac_f32_e32 v178, v28, v28
	v_fmac_f32_e32 v178, v29, v29
	v_cvt_pk_bf16_f32 v40, v26, v27
	v_cvt_pk_bf16_f32 v41, v28, v29
	global_store_dwordx2 v[176:177], v[40:41], off offset:64
	v_mul_f32_e32 v30, v179, v30
	v_mul_f32_e32 v31, v179, v31
	v_mul_f32_e32 v32, v179, v32
	v_mul_f32_e32 v33, v179, v33
	v_fmac_f32_e32 v178, v30, v30
	v_fmac_f32_e32 v178, v31, v31
	v_fmac_f32_e32 v178, v32, v32
	v_fmac_f32_e32 v178, v33, v33
	v_cvt_pk_bf16_f32 v42, v30, v31
	v_cvt_pk_bf16_f32 v43, v32, v33
	global_store_dwordx2 v[176:177], v[42:43], off offset:96
	ds_bpermute_b32 v160, v158, v178
	s_waitcnt lgkmcnt(0)
	v_add_f32_e32 v10, v178, v160
	ds_bpermute_b32 v11, v159, v10
	s_and_saveexec_b64 s[0:1], s[8:9]
	s_cbranch_execz .LBB0_773
	s_waitcnt lgkmcnt(0)
	v_add_f32_e32 v10, v10, v11
	global_store_dword v[108:109], v10, off
	s_branch .LBB0_773

; #define LAS __attribute__((address_space(3)))
; __device__ __forceinline__ int tid_hidden() { int t = threadIdx.x; asm volatile("" : "+v"(t)); return t; }
; #define C1_PF_LF(ITEM, DIR) do { const int b_ = (ITEM) >> 7, h_ = ((ITEM) >> 5) & 3, j_ = (ITEM) & 31; const size_t tk_ = (size_t)b_ * SEQ + j_ * 64; \
;         _Pragma("unroll") for (int i = 0; i < 16; ++i) lfn[i] = (unsigned)((const unsigned short*)LF)[(tk_ + tq * 16 + i) * 1024 + (DIR) * 512 + h_ * 128 + d]; } while (0)
; #define C1_PF_VT(ITEM) do { const int b_ = (ITEM) >> 7, h_ = ((ITEM) >> 5) & 3, j_ = (ITEM) & 31; \
;         _Pragma("unroll") for (int i = 0; i < 2; ++i) { const int ch = tid + i * 512, e = ch >> 3, part = ch & 7; vtn[i] = *(const u32x4*)(VTH + ((size_t)b_ * 512 + h_ * 128 + e) * SEQ + j_ * 64 + part * 8); } } while (0)
; #define lds lds_hidden(lds0)
; __device__ __forceinline__ void c1_phase(LAS unsigned char* lds, const bf16_t* __restrict__ LF, const bf16_t* __restrict__ VTH, bf16_t* __restrict__ UT, float* __restrict__ DEC, int first, int count, int stride) {
;     const int tid = tid_hidden(), wid = __builtin_amdgcn_readfirstlane(tid >> 6), lane = tid & 63, l15 = lane & 15, g4 = lane >> 4;
;     const int d = tid & 127, tq = tid >> 7;
;     LAS float* qtot = (LAS float*)(lds + C1_QT);
;     unsigned lfn[16]; u32x4 vtn[2];
;     ...
;     if (count > 0) { C1_PF_VT(first); C1_PF_LF(first, 0); }
; __global__ void __launch_bounds__(512, 2) fwd(Args a) {
;     ...
;                 const int af = c_ < 64 ? 0 : (c_ < 128 ? (c_ - 64) * 2 : 128 + (c_ - 128)), an = c_ < 64 ? 0 : (c_ < 128 ? 2 : 1);
;                 const int cf = c_ < 64 ? c_ * 5 : (c_ < 128 ? 320 + (c_ - 64) : 384 + (c_ - 128) * 5), cn = c_ < 64 ? 5 : (c_ < 128 ? 1 : 5);
.LBB0_943:
	s_mov_b32 s14, s91
	s_mov_b64 s[0:1], s[86:87]
	s_load_dwordx2 s[0:1], s[0:1], 0xa8
	s_mov_b32 s18, 4
	s_cmpk_lt_u32 s36, 0x40
	s_cbranch_scc1 .Lcn_done
	s_mov_b32 s18, 2
	s_cmpk_lt_u32 s36, 0x80
	s_cbranch_scc1 .Lcn_done
	s_mov_b32 s18, 5
.Lcn_done:
	s_andn2_b32 s36, s36, 63
	s_mov_b64 s[2:3], s[86:87]
	s_waitcnt lgkmcnt(0)
	s_add_u32 s0, s0, 0xc808000
	s_addc_u32 s1, s1, 0
	s_load_dwordx2 s[2:3], s[2:3], 0xa8
	s_mov_b64 s[6:7], s[86:87]
	s_waitcnt vmcnt(0)
	v_mov_b32_e32 v10, v0
	v_mov_b32_e32 v15, v35
	v_mov_b32_e32 v11, v35
	s_waitcnt lgkmcnt(0)
	s_add_u32 s4, s2, 0x10808000
	s_addc_u32 s5, s3, 0
	s_load_dwordx2 s[2:3], s[6:7], 0xa8
	s_mov_b64 s[6:7], s[86:87]
	s_mov_b32 s19, 0
	s_waitcnt lgkmcnt(0)
	s_add_u32 s2, s2, 0x13888000
	s_addc_u32 s3, s3, 0
	s_load_dwordx2 s[6:7], s[6:7], 0xa8
	s_waitcnt lgkmcnt(0)
	s_add_u32 s12, s6, 0x1b888000
	s_addc_u32 s13, s7, 0
	s_ashr_i32 s6, s28, 7
	s_lshl_b32 s10, s28, 2
	s_ashr_i32 s7, s6, 31
	s_and_b32 s15, s10, 0x180
	s_lshl_b32 s10, s28, 6
	s_lshl_b64 s[8:9], s[6:7], 9
	s_and_b32 s16, s10, 0x7c0
	s_or_b32 s8, s8, s15
	s_lshl_b32 s10, s16, 1
	s_add_u32 s10, s4, s10
	v_ashrrev_i32_e32 v36, 7, v10
	s_addc_u32 s11, s5, 0
	s_lshl_b64 s[6:7], s[6:7], 11
	v_lshlrev_b32_e32 v22, 4, v36
	s_or_b32 s6, s6, s16
	v_ashrrev_i32_e32 v23, 31, v22
	v_lshl_add_u64 v[12:13], s[6:7], 0, v[22:23]
	s_lshl_b32 s6, s15, 1
	v_and_b32_e32 v37, 0x7f, v10
	s_add_u32 s6, s0, s6
	s_addc_u32 s7, s1, 0
	v_lshlrev_b32_e32 v14, 1, v37
	v_lshl_add_u64 v[16:17], s[6:7], 0, v[14:15]
	v_lshlrev_b64 v[12:13], 11, v[12:13]
	v_lshl_add_u64 v[12:13], v[16:17], 0, v[12:13]
	s_movk_i32 s6, 0x1000
	v_add_co_u32_e32 v16, vcc, s6, v12
	s_movk_i32 s6, 0x3000
	s_nop 0
	v_addc_co_u32_e32 v17, vcc, 0, v13, vcc
	v_add_co_u32_e32 v24, vcc, s83, v12
	v_add_u32_e32 v6, 0x200, v10
	s_nop 0
	v_addc_co_u32_e32 v25, vcc, 0, v13, vcc
	v_add_co_u32_e32 v26, vcc, s6, v12
	v_ashrrev_i32_e32 v18, 3, v10
	s_nop 0
	v_addc_co_u32_e32 v27, vcc, 0, v13, vcc
	v_add_co_u32_e32 v28, vcc, s92, v12
	v_ashrrev_i32_e32 v20, 3, v6
	s_nop 0
	v_addc_co_u32_e32 v29, vcc, 0, v13, vcc
	s_movk_i32 s6, 0x5000
	v_lshlrev_b32_e32 v2, 4, v10
	v_ashrrev_i32_e32 v19, 31, v18
	v_ashrrev_i32_e32 v21, 31, v20
	v_add_co_u32_e32 v30, vcc, s6, v12
	v_and_b32_e32 v34, 0x70, v2
	v_lshl_add_u64 v[4:5], s[8:9], 0, v[18:19]
	v_lshl_add_u64 v[6:7], s[8:9], 0, v[20:21]
	v_addc_co_u32_e32 v31, vcc, 0, v13, vcc
	v_lshl_add_u64 v[2:3], s[10:11], 0, v[34:35]
	v_lshlrev_b64 v[4:5], 12, v[4:5]
	v_lshlrev_b64 v[6:7], 12, v[6:7]
	v_add_co_u32_e32 v32, vcc, s93, v12
	v_lshl_add_u64 v[4:5], v[2:3], 0, v[4:5]
	v_lshl_add_u64 v[6:7], v[2:3], 0, v[6:7]
	v_addc_co_u32_e32 v33, vcc, 0, v13, vcc
	s_movk_i32 s6, 0x7000
	global_load_dwordx4 v[2:5], v[4:5], off
	s_nop 0
	global_load_dwordx4 v[6:9], v[6:7], off
	s_nop 0
	global_load_ushort v109, v[24:25], off
	global_load_ushort v108, v[24:25], off offset:2048
	global_load_ushort v107, v[28:29], off offset:-4096
	global_load_ushort v105, v[28:29], off
	global_load_ushort v104, v[28:29], off offset:2048
	global_load_ushort v106, v[32:33], off offset:-4096
	global_load_ushort v103, v[32:33], off
	global_load_ushort v102, v[32:33], off offset:2048
	v_add_co_u32_e32 v28, vcc, s6, v12
	v_readfirstlane_b32 s15, v10
	s_nop 0
	v_addc_co_u32_e32 v29, vcc, 0, v13, vcc
	global_load_ushort v117, v[12:13], off
	global_load_ushort v116, v[12:13], off offset:2048
	global_load_ushort v115, v[24:25], off offset:-4096
	global_load_ushort v114, v[16:17], off offset:2048
	global_load_ushort v113, v[26:27], off offset:2048
	global_load_ushort v112, v[30:31], off offset:2048
	global_load_ushort v111, v[28:29], off
	global_load_ushort v110, v[28:29], off offset:2048
	v_lshl_add_u64 v[26:27], v[10:11], 2, s[12:13]
	s_ashr_i32 s13, s15, 2
	s_movk_i32 s10, 0x80
	s_and_b32 s12, s13, -16
	v_bfe_u32 v12, v10, 4, 2
	v_and_b32_e32 v13, 15, v10
	v_lshl_add_u32 v96, v10, 2, s14
	v_cmp_gt_u32_e64 s[10:11], s10, v10
	v_bfi_b32 v10, -16, s13, v10
	s_ashr_i32 s13, s12, 31
	s_lshl_b64 s[12:13], s[12:13], 1
	s_movk_i32 s16, 0x90
	s_add_u32 s2, s2, s12
	v_add_u32_e32 v16, s14, v34
	v_lshl_add_u64 v[24:25], s[4:5], 0, v[34:35]
	v_mov_b32_e32 v17, s14
	v_cmp_lt_i32_e64 s[4:5], 0, v36
	v_cmp_lt_i32_e64 s[6:7], 1, v36
	v_cmp_lt_i32_e64 s[8:9], 2, v36
	v_lshlrev_b32_e32 v32, 5, v36
	v_mul_lo_u32 v10, v10, s16
	v_lshlrev_b32_e32 v36, 4, v12
	s_addc_u32 s3, s3, s13
	v_lshlrev_b32_e32 v34, 3, v12
	v_lshl_add_u32 v97, v37, 2, s14
	v_mad_u32_u24 v17, v37, s16, v17
	v_add_u32_e32 v33, s14, v10
	v_add_u32_e32 v37, s14, v36
	v_lshl_add_u64 v[10:11], s[2:3], 0, v[34:35]
	v_lshl_add_u64 v[28:29], s[0:1], 0, v[14:15]
	v_mul_lo_u32 v12, v18, s16
	v_mul_lo_u32 v14, v20, s16
	v_mul_u32_u24_e32 v15, 0x90, v13
	v_lshlrev_b32_e32 v34, 8, v13
	v_lshl_add_u64 v[30:31], v[10:11], 0, v[34:35]
	v_add_u32_e32 v34, v16, v12
	v_add_u32_e32 v98, v16, v14
	v_add_u32_e32 v99, v17, v32
	v_add_u32_e32 v100, v33, v36
	v_add_u32_e32 v101, v37, v15
	s_branch .LBB0_945

;     __device__ __forceinline__ const char* bptr(const Unit& u) const { return (const char*)Bt + ((size_t)u.e * NTN * BM + (size_t)u.pn * BM) * RB; }
; #define G8_STAGE_U(bufoff, gbase) do { const char* _g = (const char*)(gbase); const char* _g1 = _g + (size_t)(64 * RB); asm volatile("" : "+s"(_g), "+s"(_g1));   \
;         G8_GLDS(_g + vo0, bufoff, 0); G8_GLDS(_g1 + vo0, bufoff, 1); } while (0)
; #define G8_TABRD(par, h) do { if constexpr (Src::GATHER) { LAS const int* _t = (LAS const int*)(lds + TAB_OFF + (par) * 1024 + (h) * 512 + tabA); tv0 = (unsigned)_t[0]; tv1 = (unsigned)_t[64]; } } while (0)
; #define G8_STAGE_A(bufoff, up, par, h, kb) do { if constexpr (Src::GATHER) G8_STAGE_G(bufoff, kb); else G8_STAGE_U(bufoff, (up) + (h) * hstep + (kb)); } while (0)
; #define G8_WAIT_V(n) asm volatile("s_waitcnt vmcnt(" #n ")" ::: "memory")
; #define G8_BAR __builtin_amdgcn_s_barrier()
;     __device__ __forceinline__ const char* bptr(const Unit& u) const { return (const char*)Bt + (size_t)u.pn * BM * KD * 2; }
; #define lds lds_hidden(lds0)
; template <class Epi, class Src>
; __device__ __forceinline__ void gemm_phase(LAS unsigned char* lds, const Src S, const Epi E) {
;     ...
;     const char* Ab = (const char*)S.A;
;     const char* cB = S.bptr(cur);
;     const char* cA = Ab + (size_t)(cur.rowbase + cur.rt * BM) * RB;
;     int par = 0;
;     if (Src::GATHER) { tab_fill(S, cur, tid, wid, lds, 0); G8_WAIT_V(0); __syncthreads(); }
;     G8_STAGE_U(G8_SB(0, 0), cB); G8_TABRD(0, 0); G8_STAGE_A(G8_SA(0, 0), cA, 0, 0, 0); G8_STAGE_U(G8_SB(0, 1), cB + hstep); G8_TABRD(0, 1); G8_STAGE_A(G8_SA(0, 1), cA, 0, 1, 0);
;     if (wr == 1) G8_BAR;
;     G8_WAIT_V(4); G8_BAR;
;     G8_STAGE_U(G8_SB(1, 0), cB + kstep); G8_TABRD(0, 0); G8_STAGE_A(G8_SA(1, 0), cA, 0, 0, kstep); G8_STAGE_U(G8_SB(1, 1), cB + hstep + kstep);
;     G8_WAIT_V(6); G8_BAR;
.LBB0_1351:
	v_bfe_i32 v5, v2, 27, 1
	v_lshlrev_b32_e32 v3, 4, v2
	v_lshrrev_b32_e32 v5, 22, v5
	v_add_u32_e32 v5, v3, v5
	s_lshl_b32 s90, s40, 16
	v_and_b32_e32 v5, 0xfffffc00, v5
	s_lshl_b64 s[20:21], s[90:91], 10
	v_ashrrev_i32_e32 v4, 31, v2
	v_sub_u32_e32 v3, v3, v5
	s_add_u32 s40, s0, s20
	v_lshrrev_b32_e32 v4, 26, v4
	v_lshrrev_b32_e32 v5, 4, v3
	s_addc_u32 s41, s1, s21
	s_ashr_i32 s19, s18, 31
	v_add_u32_e32 v4, v2, v4
	v_bitop3_b32 v5, v5, v3, 32 bitop3:0x6c
	v_ashrrev_i32_e32 v3, 31, v3
	s_lshl_b64 s[0:1], s[18:19], 18
	s_lshl_b64 s[20:21], s[16:17], 21
	v_ashrrev_i32_e32 v4, 6, v4
	v_lshrrev_b32_e32 v3, 26, v3
	s_add_u32 s17, s40, s20
	v_lshlrev_b32_e32 v6, 3, v4
	v_add_u32_e32 v3, v5, v3
	s_addc_u32 s19, s41, s21
	v_and_b32_e32 v6, -16, v6
	v_ashrrev_i32_e32 v3, 6, v3
	s_add_u32 s20, s17, s0
	v_add_u32_e32 v6, v3, v6
	v_mul_i32_i24_e32 v3, 64, v3
	s_addc_u32 s21, s19, s1
	s_ashr_i32 s1, s37, 8
	v_sub_u32_e32 v3, v5, v3
	s_lshl_b32 s0, s3, 10
	v_lshlrev_b32_e32 v4, 5, v4
	v_ashrrev_i16_sdwa v3, v1, sext(v3) dst_sel:DWORD dst_unused:UNUSED_PAD src0_sel:DWORD src1_sel:BYTE_0
	s_add_u32 s24, s20, 0x10000
	v_and_b32_e32 v4, 32, v4
	v_bfe_i32 v3, v3, 0, 16
	s_addc_u32 s25, s21, 0
	s_add_i32 s43, s13, 0x10000
	v_add_lshl_u32 v155, v4, v3, 1
	s_add_i32 s44, s43, s0
	v_lshl_add_u32 v252, v6, 10, v155
	s_mov_b64 s[26:27], s[20:21]
	s_mov_b32 m0, s44
	s_add_i32 s45, s44, 0x2000
	v_lshlrev_b32_e32 v3, 2, v6
	s_waitcnt vmcnt(0)
	s_waitcnt vmcnt(0) lgkmcnt(0)
	s_barrier
	s_add_i32 s46, s13, 0x20000
	global_load_lds_dwordx4 v252, s[26:27]
	s_mov_b32 m0, s45
	v_add_u32_e32 v156, s46, v3
	global_load_lds_dwordx4 v252, s[24:25]
	ds_read2st64_b32 v[4:5], v156 offset1:1
	s_add_i32 s47, s13, s0
	s_add_i32 s48, s47, 0x2000
	s_add_u32 s24, s20, 0x20000
	s_addc_u32 s25, s21, 0
	s_add_u32 s26, s20, 0x30000
	s_waitcnt lgkmcnt(0)
	v_lshl_or_b32 v159, v5, 16, v4
	v_lshl_add_u32 v4, v4, 10, v155
	s_mov_b32 m0, s47
	s_addc_u32 s27, s21, 0
	s_add_i32 s49, s13, 0x14000
	global_load_lds_dwordx4 v4, s[8:9]
	v_lshl_add_u32 v4, v5, 10, v155
	s_mov_b32 m0, s48
	s_add_i32 s50, s49, s0
	global_load_lds_dwordx4 v4, s[8:9]
	s_mov_b32 m0, s50
	s_add_i32 s51, s50, 0x2000
	v_add_u32_e32 v3, s13, v3
	global_load_lds_dwordx4 v252, s[24:25]
	s_mov_b32 m0, s51
	v_add_u32_e32 v3, 0x20200, v3
	global_load_lds_dwordx4 v252, s[26:27]
	ds_read2st64_b32 v[4:5], v3 offset1:1
	s_add_i32 s52, s47, 0x4000
	s_mov_b32 m0, s52
	s_add_i32 s53, s47, 0x6000
	s_cmp_lg_u32 s1, 1
	s_waitcnt lgkmcnt(0)
	v_lshl_or_b32 v255, v5, 16, v4
	v_lshl_add_u32 v3, v4, 10, v155
	global_load_lds_dwordx4 v3, s[8:9]
	v_lshl_add_u32 v3, v5, 10, v155
	s_mov_b32 m0, s53
	s_nop 0
	global_load_lds_dwordx4 v3, s[8:9]
	s_cbranch_scc1 .LBB0_1353
	s_barrier
.LBB0_1353:
	s_lshl_b64 s[24:25], s[6:7], 2
	s_add_u32 s19, s4, s24
	s_addc_u32 s42, s5, s25
	s_lshl_b64 s[4:5], s[90:91], 2
	s_add_u32 s54, s22, s4
	s_addc_u32 s56, s23, s5
	s_lshl_b32 s3, s3, 12
	s_lshl_b32 s1, s1, 13
	s_and_b32 s3, s3, 0x3000
	s_add_u32 s4, s20, 0x80
	s_addc_u32 s5, s21, 0
	s_add_u32 s22, s20, 0x10080
	s_addc_u32 s23, s21, 0
	s_add_i32 s58, s13, 0x18000
	v_mov_b32_e32 v253, v35
	v_and_b32_e32 v3, 15, v2
	s_add_i32 s59, s58, s0
	v_and_b32_e32 v4, 48, v2
	v_lshlrev_b32_e32 v5, 6, v3
	v_lshlrev_b32_e32 v7, 2, v2
	s_waitcnt vmcnt(4)
	s_barrier
	s_mov_b32 m0, s59
	v_lshl_add_u64 v[2:3], s[4:5], 0, v[252:253]
	s_add_i32 s60, s59, 0x2000
	global_load_lds_dwordx4 v[2:3], off
	v_lshl_add_u64 v[2:3], s[22:23], 0, v[252:253]
	s_mov_b32 m0, s60
	v_and_b32_e32 v7, 32, v7
	global_load_lds_dwordx4 v[2:3], off
	ds_read2st64_b32 v[2:3], v156 offset1:1
	v_or_b32_e32 v6, v5, v4
	v_bitop3_b32 v4, v5, v7, v4 bitop3:0x36
	v_or_b32_e32 v157, s3, v4
	s_mov_b64 s[4:5], 0x80
	s_waitcnt lgkmcnt(0)
	v_lshl_add_u32 v34, v2, 10, v155
	v_lshl_add_u64 v[4:5], s[8:9], 0, v[34:35]
	v_lshl_add_u32 v34, v3, 10, v155
	s_add_i32 s61, s47, 0x8000
	v_lshl_add_u64 v[2:3], s[8:9], 0, v[34:35]
	s_add_i32 s62, s47, 0xa000
	v_lshl_add_u64 v[4:5], v[4:5], 0, s[4:5]
	v_lshl_add_u64 v[2:3], v[2:3], 0, s[4:5]
	s_add_u32 s4, s20, 0x20080
	s_addc_u32 s5, s21, 0
	s_add_u32 s22, s20, 0x30080
	s_mov_b32 m0, s61
	s_addc_u32 s23, s21, 0
	s_add_i32 s63, s13, 0x1c000
	global_load_lds_dwordx4 v[4:5], off
	s_mov_b32 m0, s62
	s_add_i32 s64, s63, s0
	global_load_lds_dwordx4 v[2:3], off
	s_mov_b32 m0, s64
	v_lshl_add_u64 v[2:3], s[4:5], 0, v[252:253]
	s_add_i32 s65, s64, 0x2000
	global_load_lds_dwordx4 v[2:3], off
	v_lshl_add_u64 v[2:3], s[22:23], 0, v[252:253]
	s_mov_b32 m0, s65
	v_bitop3_b32 v6, v6, s1, v7 bitop3:0xde
	global_load_lds_dwordx4 v[2:3], off
	s_waitcnt vmcnt(6)
	s_add_i32 s55, s55, s2
	s_add_i32 s66, s66, 0x20840
	v_add_u32_e32 v158, s13, v6
	s_add_i32 s67, s13, 0x20a00
	s_mov_b32 s68, 0
	s_mov_b32 s57, 0
	s_barrier
	s_add_i32 s72, s57, 1
	s_cmp_gt_i32 s57, 14
	s_mov_b64 s[0:1], -1
	s_cbranch_scc0 .LBB0_1356

.LBB0_1369:
	s_ashr_i32 s27, s26, 31
	s_lshl_b64 s[0:1], s[26:27], 18
	s_lshl_b64 s[2:3], s[22:23], 21
	s_add_u32 s2, s40, s2
	s_addc_u32 s3, s41, s3
	s_add_u32 s28, s2, s0
	v_lshl_add_u32 v134, s68, 10, v156
	s_addc_u32 s29, s3, s1
	s_and_b64 s[0:1], s[24:25], exec
	s_cselect_b32 s1, s29, s21
	s_cselect_b32 s0, s28, s20
	s_add_u32 s2, s20, 0x100
	s_addc_u32 s3, s21, 0
	v_add_u32_e32 v132, s43, v157
	s_mov_b64 s[94:95], 0x80
	s_add_i32 s23, s47, 0xc000
	s_add_i32 s17, s47, 0xe000
	ds_read_b128 v[136:139], v132
	ds_read_b128 v[140:143], v132 offset:1024
	ds_read_b128 v[160:163], v132 offset:2048
	ds_read_b128 v[164:167], v132 offset:3072
	ds_read_b128 v[168:171], v158
	ds_read_b128 v[172:175], v158 offset:1024
	ds_read_b128 v[176:179], v158 offset:2048
	ds_read_b128 v[180:183], v158 offset:3072
	ds_read_b128 v[184:187], v158 offset:4096
	ds_read_b128 v[188:191], v158 offset:5120
	ds_read_b128 v[192:195], v158 offset:6144
	ds_read_b128 v[196:199], v158 offset:7168
	s_add_u32 s94, s8, 0x80
	s_addc_u32 s95, s9, 0
	v_and_b32_e32 v34, 0xffff, v255
	v_lshl_add_u32 v34, v34, 10, v155
	s_mov_b32 m0, s23
	s_nop 0
	global_load_lds_dwordx4 v34, s[94:95]
	v_lshrrev_b32_e32 v34, 16, v255
	v_lshl_add_u32 v34, v34, 10, v155
	s_mov_b32 m0, s17
	s_nop 0
	global_load_lds_dwordx4 v34, s[94:95]
	s_waitcnt lgkmcnt(8)
	s_barrier
	s_waitcnt lgkmcnt(0)
	s_setprio 1
	s_waitcnt lgkmcnt(0)
	v_mfma_scale_f32_16x16x128_f8f6f4 v[150:153], v[136:143], v[168:175], 0, v154, v154 op_sel_hi:[0,0,0]
	v_mfma_scale_f32_16x16x128_f8f6f4 v[208:211], v[160:167], v[168:175], 0, v154, v154 op_sel_hi:[0,0,0]
	v_mfma_scale_f32_16x16x128_f8f6f4 v[212:215], v[136:143], v[176:183], 0, v154, v154 op_sel_hi:[0,0,0]
	v_mfma_scale_f32_16x16x128_f8f6f4 v[216:219], v[160:167], v[176:183], 0, v154, v154 op_sel_hi:[0,0,0]
	v_mfma_scale_f32_16x16x128_f8f6f4 v[220:223], v[136:143], v[184:191], 0, v154, v154 op_sel_hi:[0,0,0]
	v_mfma_scale_f32_16x16x128_f8f6f4 v[224:227], v[160:167], v[184:191], 0, v154, v154 op_sel_hi:[0,0,0]
	v_mfma_scale_f32_16x16x128_f8f6f4 v[228:231], v[136:143], v[192:199], 0, v154, v154 op_sel_hi:[0,0,0]
	v_mfma_scale_f32_16x16x128_f8f6f4 v[232:235], v[160:167], v[192:199], 0, v154, v154 op_sel_hi:[0,0,0]
	s_setprio 0
	s_barrier
	s_add_u32 s74, s20, 0x10100
	v_add_u32_e32 v133, s49, v157
	s_addc_u32 s75, s21, 0
	s_mov_b32 m0, s44
	ds_read_b128 v[124:127], v133
	ds_read_b128 v[128:131], v133 offset:1024
	ds_read_b128 v[200:203], v133 offset:2048
	ds_read_b128 v[204:207], v133 offset:3072
	s_nop 0
	v_lshl_add_u64 v[68:69], s[2:3], 0, v[252:253]
	global_load_lds_dwordx4 v[68:69], off
	v_lshl_add_u64 v[68:69], s[74:75], 0, v[252:253]
	s_mov_b32 m0, s45
	s_nop 0
	global_load_lds_dwordx4 v[68:69], off
	s_barrier
	s_waitcnt lgkmcnt(0)
	s_setprio 1
	s_waitcnt lgkmcnt(0)
	v_mfma_scale_f32_16x16x128_f8f6f4 v[96:99], v[124:131], v[168:175], 0, v154, v154 op_sel_hi:[0,0,0]
	v_mfma_scale_f32_16x16x128_f8f6f4 v[92:95], v[200:207], v[168:175], 0, v154, v154 op_sel_hi:[0,0,0]
	v_mfma_scale_f32_16x16x128_f8f6f4 v[88:91], v[124:131], v[176:183], 0, v154, v154 op_sel_hi:[0,0,0]
	v_mfma_scale_f32_16x16x128_f8f6f4 v[84:87], v[200:207], v[176:183], 0, v154, v154 op_sel_hi:[0,0,0]
	v_mfma_scale_f32_16x16x128_f8f6f4 v[80:83], v[124:131], v[184:191], 0, v154, v154 op_sel_hi:[0,0,0]
	v_mfma_scale_f32_16x16x128_f8f6f4 v[76:79], v[200:207], v[184:191], 0, v154, v154 op_sel_hi:[0,0,0]
	v_mfma_scale_f32_16x16x128_f8f6f4 v[72:75], v[124:131], v[192:199], 0, v154, v154 op_sel_hi:[0,0,0]
	v_mfma_scale_f32_16x16x128_f8f6f4 v[68:71], v[200:207], v[192:199], 0, v154, v154 op_sel_hi:[0,0,0]
	s_setprio 0
	s_barrier
	s_nop 0
	s_mov_b64 s[76:77], 0x100
	ds_read_b128 v[104:107], v158 offset:16384
	ds_read_b128 v[108:111], v158 offset:17408
	ds_read_b128 v[112:115], v158 offset:18432
	ds_read_b128 v[116:119], v158 offset:19456
	ds_read_b128 v[168:171], v158 offset:20480
	ds_read_b128 v[172:175], v158 offset:21504
	ds_read_b128 v[176:179], v158 offset:22528
	ds_read_b128 v[180:183], v158 offset:23552
	s_add_u32 s94, s8, 0x100
	s_addc_u32 s95, s9, 0
	v_and_b32_e32 v34, 0xffff, v159
	v_lshl_add_u32 v34, v34, 10, v155
	s_mov_b32 m0, s47
	s_nop 0
	global_load_lds_dwordx4 v34, s[94:95]
	v_lshrrev_b32_e32 v34, 16, v159
	v_lshl_add_u32 v34, v34, 10, v155
	s_mov_b32 m0, s48
	s_nop 0
	global_load_lds_dwordx4 v34, s[94:95]
	s_barrier
	s_waitcnt lgkmcnt(0)
	s_setprio 1
	s_waitcnt lgkmcnt(0)
	v_mfma_scale_f32_16x16x128_f8f6f4 v[64:67], v[136:143], v[104:111], 0, v154, v154 op_sel_hi:[0,0,0]
	v_mfma_scale_f32_16x16x128_f8f6f4 v[60:63], v[160:167], v[104:111], 0, v154, v154 op_sel_hi:[0,0,0]
	v_mfma_scale_f32_16x16x128_f8f6f4 v[56:59], v[136:143], v[112:119], 0, v154, v154 op_sel_hi:[0,0,0]
	v_mfma_scale_f32_16x16x128_f8f6f4 v[52:55], v[160:167], v[112:119], 0, v154, v154 op_sel_hi:[0,0,0]
	v_mfma_scale_f32_16x16x128_f8f6f4 v[48:51], v[136:143], v[168:175], 0, v154, v154 op_sel_hi:[0,0,0]
	v_mfma_scale_f32_16x16x128_f8f6f4 v[44:47], v[160:167], v[168:175], 0, v154, v154 op_sel_hi:[0,0,0]
	v_mfma_scale_f32_16x16x128_f8f6f4 v[40:43], v[136:143], v[176:183], 0, v154, v154 op_sel_hi:[0,0,0]
	v_mfma_scale_f32_16x16x128_f8f6f4 v[36:39], v[160:167], v[176:183], 0, v154, v154 op_sel_hi:[0,0,0]
	s_setprio 0
	s_barrier
	s_add_u32 s2, s20, 0x20100
	s_addc_u32 s3, s21, 0
	s_add_u32 s74, s20, 0x30100
	s_addc_u32 s75, s21, 0
	s_mov_b32 m0, s50
	s_nop 0
	v_lshl_add_u64 v[6:7], s[2:3], 0, v[252:253]
	global_load_lds_dwordx4 v[6:7], off
	v_lshl_add_u64 v[6:7], s[74:75], 0, v[252:253]
	s_mov_b32 m0, s51
	s_nop 0
	global_load_lds_dwordx4 v[6:7], off
	s_waitcnt vmcnt(6)
	s_barrier
; __device__ __forceinline__ int tid_hidden() { int t = threadIdx.x; asm volatile("" : "+v"(t)); return t; }
; #define lds lds_hidden(lds0)
; template <class Epi, class Src>
; __device__ __forceinline__ void gemm_phase(LAS unsigned char* lds, const Src S, const Epi E) {
;     ...
;         { const int tp = tid_hidden(); E.prefetch(cur, lds, par, tp, __builtin_amdgcn_readfirstlane(tp >> 6)); }
;         if (Src::GATHER && has_next) { const int tp = tid_hidden(); tab_fill(S, nxt, tp, __builtin_amdgcn_readfirstlane(tp >> 6), lds, par ^ 1); }
;         for (int t = 0; t < NKTR - 2; t += 2) {
;             const size_t k1 = (size_t)(t + 1) * kstep, k2 = (size_t)(t + 2) * kstep;
;             const char* b2 = cB + k2; const char* b3 = b2 + kstep;
;             G8_ITER(cA, par, k1, cA, par, k2, b2, b3);
	s_setprio 1
	v_mfma_scale_f32_16x16x128_f8f6f4 v[100:103], v[124:131], v[104:111], 0, v154, v154 op_sel_hi:[0,0,0]
	v_mfma_scale_f32_16x16x128_f8f6f4 v[104:107], v[200:207], v[104:111], 0, v154, v154 op_sel_hi:[0,0,0]
	v_mfma_scale_f32_16x16x128_f8f6f4 v[108:111], v[124:131], v[112:119], 0, v154, v154 op_sel_hi:[0,0,0]
	v_mfma_scale_f32_16x16x128_f8f6f4 v[112:115], v[200:207], v[112:119], 0, v154, v154 op_sel_hi:[0,0,0]
	v_mfma_scale_f32_16x16x128_f8f6f4 v[116:119], v[124:131], v[168:175], 0, v154, v154 op_sel_hi:[0,0,0]
	v_mfma_scale_f32_16x16x128_f8f6f4 v[120:123], v[200:207], v[168:175], 0, v154, v154 op_sel_hi:[0,0,0]
	v_mfma_scale_f32_16x16x128_f8f6f4 v[124:127], v[124:131], v[176:183], 0, v154, v154 op_sel_hi:[0,0,0]
	v_mfma_scale_f32_16x16x128_f8f6f4 v[128:131], v[200:207], v[176:183], 0, v154, v154 op_sel_hi:[0,0,0]
	s_setprio 0
	s_barrier
	s_nop 4
	v_add_u32_e32 v135, s58, v157
	ds_read_b128 v[138:141], v135
	ds_read_b128 v[142:145], v135 offset:1024
	ds_read_b128 v[160:163], v135 offset:2048
	ds_read_b128 v[164:167], v135 offset:3072
	ds_read_b128 v[168:171], v158 offset:32768
	ds_read_b128 v[172:175], v158 offset:33792
	ds_read_b128 v[176:179], v158 offset:34816
	ds_read_b128 v[180:183], v158 offset:35840
	ds_read_b128 v[184:187], v158 offset:36864
	ds_read_b128 v[188:191], v158 offset:37888
	ds_read_b128 v[192:195], v158 offset:38912
	ds_read_b128 v[196:199], v158 offset:39936
	s_add_u32 s94, s8, 0x100
	s_addc_u32 s95, s9, 0
	v_and_b32_e32 v34, 0xffff, v255
	v_lshl_add_u32 v34, v34, 10, v155
	s_mov_b32 m0, s52
	s_nop 0
	global_load_lds_dwordx4 v34, s[94:95]
	v_lshrrev_b32_e32 v34, 16, v255
	v_lshl_add_u32 v34, v34, 10, v155
	s_mov_b32 m0, s53
	s_nop 0
	global_load_lds_dwordx4 v34, s[94:95]
	s_waitcnt lgkmcnt(8)
	s_barrier
	s_waitcnt lgkmcnt(0)
	s_setprio 1
	s_waitcnt lgkmcnt(0)
	v_mfma_scale_f32_16x16x128_f8f6f4 v[2:5], v[138:145], v[168:175], v[150:153], v154, v154 op_sel_hi:[0,0,0]
	v_mfma_scale_f32_16x16x128_f8f6f4 v[6:9], v[160:167], v[168:175], v[208:211], v154, v154 op_sel_hi:[0,0,0]
	v_mfma_scale_f32_16x16x128_f8f6f4 v[10:13], v[138:145], v[176:183], v[212:215], v154, v154 op_sel_hi:[0,0,0]
	v_mfma_scale_f32_16x16x128_f8f6f4 v[14:17], v[160:167], v[176:183], v[216:219], v154, v154 op_sel_hi:[0,0,0]
	v_mfma_scale_f32_16x16x128_f8f6f4 v[18:21], v[138:145], v[184:191], v[220:223], v154, v154 op_sel_hi:[0,0,0]
	v_mfma_scale_f32_16x16x128_f8f6f4 v[22:25], v[160:167], v[184:191], v[224:227], v154, v154 op_sel_hi:[0,0,0]
	v_mfma_scale_f32_16x16x128_f8f6f4 v[26:29], v[138:145], v[192:199], v[228:231], v154, v154 op_sel_hi:[0,0,0]
	v_mfma_scale_f32_16x16x128_f8f6f4 v[30:33], v[160:167], v[192:199], v[232:235], v154, v154 op_sel_hi:[0,0,0]
	s_setprio 0
	s_barrier
	s_add_u32 s2, s20, 0x180
	s_addc_u32 s3, s21, 0
	s_add_u32 s74, s20, 0x10180
	v_add_u32_e32 v136, s63, v157
	s_addc_u32 s75, s21, 0
	s_mov_b32 m0, s59
	ds_read_b128 v[200:203], v136
	ds_read_b128 v[204:207], v136 offset:1024
	ds_read_b128 v[208:211], v136 offset:2048
	ds_read_b128 v[212:215], v136 offset:3072
	s_nop 0
	v_lshl_add_u64 v[146:147], s[2:3], 0, v[252:253]
	global_load_lds_dwordx4 v[146:147], off
	v_lshl_add_u64 v[146:147], s[74:75], 0, v[252:253]
	s_mov_b32 m0, s60
	s_nop 0
	global_load_lds_dwordx4 v[146:147], off
	s_barrier
	s_waitcnt lgkmcnt(0)
	s_setprio 1
	s_waitcnt lgkmcnt(0)
	v_mfma_scale_f32_16x16x128_f8f6f4 v[96:99], v[200:207], v[168:175], v[96:99], v154, v154 op_sel_hi:[0,0,0]
	v_mfma_scale_f32_16x16x128_f8f6f4 v[92:95], v[208:215], v[168:175], v[92:95], v154, v154 op_sel_hi:[0,0,0]
	v_mfma_scale_f32_16x16x128_f8f6f4 v[88:91], v[200:207], v[176:183], v[88:91], v154, v154 op_sel_hi:[0,0,0]
	v_mfma_scale_f32_16x16x128_f8f6f4 v[84:87], v[208:215], v[176:183], v[84:87], v154, v154 op_sel_hi:[0,0,0]
	v_mfma_scale_f32_16x16x128_f8f6f4 v[80:83], v[200:207], v[184:191], v[80:83], v154, v154 op_sel_hi:[0,0,0]
	v_mfma_scale_f32_16x16x128_f8f6f4 v[76:79], v[208:215], v[184:191], v[76:79], v154, v154 op_sel_hi:[0,0,0]
	v_mfma_scale_f32_16x16x128_f8f6f4 v[72:75], v[200:207], v[192:199], v[72:75], v154, v154 op_sel_hi:[0,0,0]
	v_mfma_scale_f32_16x16x128_f8f6f4 v[68:71], v[208:215], v[192:199], v[68:71], v154, v154 op_sel_hi:[0,0,0]
	s_setprio 0
	s_barrier
	s_mov_b64 s[76:77], 0x180
	ds_read_b128 v[168:171], v158 offset:49152
	ds_read_b128 v[172:175], v158 offset:50176
	ds_read_b128 v[176:179], v158 offset:51200
	ds_read_b128 v[180:183], v158 offset:52224
	ds_read_b128 v[184:187], v158 offset:53248
	ds_read_b128 v[188:191], v158 offset:54272
	ds_read_b128 v[192:195], v158 offset:55296
	ds_read_b128 v[196:199], v158 offset:56320
	s_add_u32 s94, s8, 0x180
	s_addc_u32 s95, s9, 0
	v_and_b32_e32 v34, 0xffff, v159
	v_lshl_add_u32 v34, v34, 10, v155
	s_mov_b32 m0, s61
	s_nop 0
	global_load_lds_dwordx4 v34, s[94:95]
	v_lshrrev_b32_e32 v34, 16, v159
	v_lshl_add_u32 v34, v34, 10, v155
	s_mov_b32 m0, s62
	s_nop 0
	global_load_lds_dwordx4 v34, s[94:95]
	s_barrier
	s_waitcnt lgkmcnt(0)
	s_setprio 1
	s_waitcnt lgkmcnt(0)
	v_mfma_scale_f32_16x16x128_f8f6f4 v[64:67], v[138:145], v[168:175], v[64:67], v154, v154 op_sel_hi:[0,0,0]
	v_mfma_scale_f32_16x16x128_f8f6f4 v[60:63], v[160:167], v[168:175], v[60:63], v154, v154 op_sel_hi:[0,0,0]
	v_mfma_scale_f32_16x16x128_f8f6f4 v[56:59], v[138:145], v[176:183], v[56:59], v154, v154 op_sel_hi:[0,0,0]
	v_mfma_scale_f32_16x16x128_f8f6f4 v[52:55], v[160:167], v[176:183], v[52:55], v154, v154 op_sel_hi:[0,0,0]
	v_mfma_scale_f32_16x16x128_f8f6f4 v[48:51], v[138:145], v[184:191], v[48:51], v154, v154 op_sel_hi:[0,0,0]
	v_mfma_scale_f32_16x16x128_f8f6f4 v[44:47], v[160:167], v[184:191], v[44:47], v154, v154 op_sel_hi:[0,0,0]
	v_mfma_scale_f32_16x16x128_f8f6f4 v[40:43], v[138:145], v[192:199], v[40:43], v154, v154 op_sel_hi:[0,0,0]
	v_mfma_scale_f32_16x16x128_f8f6f4 v[36:39], v[160:167], v[192:199], v[36:39], v154, v154 op_sel_hi:[0,0,0]
	s_setprio 0
	s_barrier
; __device__ __forceinline__ int tid_hidden() { int t = threadIdx.x; asm volatile("" : "+v"(t)); return t; }
; #define lds lds_hidden(lds0)
; template <class Epi, class Src>
; __device__ __forceinline__ void gemm_phase(LAS unsigned char* lds, const Src S, const Epi E) {
;     ...
;         { const int tp = tid_hidden(); E.prefetch(cur, lds, par, tp, __builtin_amdgcn_readfirstlane(tp >> 6)); }
;         if (Src::GATHER && has_next) { const int tp = tid_hidden(); tab_fill(S, nxt, tp, __builtin_amdgcn_readfirstlane(tp >> 6), lds, par ^ 1); }
;         for (int t = 0; t < NKTR - 2; t += 2) {
;             const size_t k1 = (size_t)(t + 1) * kstep, k2 = (size_t)(t + 2) * kstep;
;             const char* b2 = cB + k2; const char* b3 = b2 + kstep;
;             G8_ITER(cA, par, k1, cA, par, k2, b2, b3);
	s_add_u32 s2, s20, 0x20180
	s_addc_u32 s3, s21, 0
	s_add_u32 s74, s20, 0x30180
	s_addc_u32 s75, s21, 0
	s_mov_b32 m0, s64
	s_nop 0
	v_lshl_add_u64 v[138:139], s[2:3], 0, v[252:253]
	global_load_lds_dwordx4 v[138:139], off
	v_lshl_add_u64 v[138:139], s[74:75], 0, v[252:253]
	s_mov_b32 m0, s65
	s_nop 0
	global_load_lds_dwordx4 v[138:139], off
	s_waitcnt vmcnt(6)
	s_barrier
	s_setprio 1
	v_mfma_scale_f32_16x16x128_f8f6f4 v[108:111], v[200:207], v[176:183], v[108:111], v154, v154 op_sel_hi:[0,0,0]
	v_mfma_scale_f32_16x16x128_f8f6f4 v[112:115], v[208:215], v[176:183], v[112:115], v154, v154 op_sel_hi:[0,0,0]
	v_mfma_scale_f32_16x16x128_f8f6f4 v[116:119], v[200:207], v[184:191], v[116:119], v154, v154 op_sel_hi:[0,0,0]
	v_mfma_scale_f32_16x16x128_f8f6f4 v[120:123], v[208:215], v[184:191], v[120:123], v154, v154 op_sel_hi:[0,0,0]
	v_mfma_scale_f32_16x16x128_f8f6f4 v[124:127], v[200:207], v[192:199], v[124:127], v154, v154 op_sel_hi:[0,0,0]
	v_mfma_scale_f32_16x16x128_f8f6f4 v[128:131], v[208:215], v[192:199], v[128:131], v154, v154 op_sel_hi:[0,0,0]
	v_mfma_scale_f32_16x16x128_f8f6f4 v[100:103], v[200:207], v[168:175], v[100:103], v154, v154 op_sel_hi:[0,0,0]
	v_mfma_scale_f32_16x16x128_f8f6f4 v[104:107], v[208:215], v[168:175], v[104:107], v154, v154 op_sel_hi:[0,0,0]
	s_setprio 0
	s_barrier
	s_add_u32 s2, s20, 0x200
	s_addc_u32 s3, s21, 0
	ds_read_b128 v[138:141], v132
	ds_read_b128 v[142:145], v132 offset:1024
	ds_read_b128 v[160:163], v132 offset:2048
	ds_read_b128 v[164:167], v132 offset:3072
	ds_read_b128 v[168:171], v158
	ds_read_b128 v[172:175], v158 offset:1024
	ds_read_b128 v[176:179], v158 offset:2048
	ds_read_b128 v[180:183], v158 offset:3072
	ds_read_b128 v[184:187], v158 offset:4096
	ds_read_b128 v[188:191], v158 offset:5120
	ds_read_b128 v[192:195], v158 offset:6144
	ds_read_b128 v[196:199], v158 offset:7168
	s_add_u32 s94, s8, 0x180
	s_addc_u32 s95, s9, 0
	v_and_b32_e32 v34, 0xffff, v255
	v_lshl_add_u32 v34, v34, 10, v155
	s_mov_b32 m0, s23
	s_nop 0
	global_load_lds_dwordx4 v34, s[94:95]
	v_lshrrev_b32_e32 v34, 16, v255
	v_lshl_add_u32 v34, v34, 10, v155
	s_mov_b32 m0, s17
	s_nop 0
	global_load_lds_dwordx4 v34, s[94:95]
	s_waitcnt lgkmcnt(8)
	s_barrier
	s_waitcnt lgkmcnt(0)
	s_setprio 1
	s_waitcnt lgkmcnt(0)
	v_mfma_scale_f32_16x16x128_f8f6f4 v[204:207], v[138:145], v[176:183], v[10:13], v154, v154 op_sel_hi:[0,0,0]
	v_mfma_scale_f32_16x16x128_f8f6f4 v[150:153], v[138:145], v[168:175], v[2:5], v154, v154 op_sel_hi:[0,0,0]
	v_mfma_scale_f32_16x16x128_f8f6f4 v[200:203], v[160:167], v[168:175], v[6:9], v154, v154 op_sel_hi:[0,0,0]
	v_mfma_scale_f32_16x16x128_f8f6f4 v[208:211], v[160:167], v[176:183], v[14:17], v154, v154 op_sel_hi:[0,0,0]
	v_mfma_scale_f32_16x16x128_f8f6f4 v[212:215], v[138:145], v[184:191], v[18:21], v154, v154 op_sel_hi:[0,0,0]
	v_mfma_scale_f32_16x16x128_f8f6f4 v[216:219], v[160:167], v[184:191], v[22:25], v154, v154 op_sel_hi:[0,0,0]
	v_mfma_scale_f32_16x16x128_f8f6f4 v[220:223], v[138:145], v[192:199], v[26:29], v154, v154 op_sel_hi:[0,0,0]
	v_mfma_scale_f32_16x16x128_f8f6f4 v[224:227], v[160:167], v[192:199], v[30:33], v154, v154 op_sel_hi:[0,0,0]
	s_setprio 0
	s_barrier
	s_add_u32 s74, s20, 0x10200
	s_addc_u32 s75, s21, 0
	s_mov_b32 m0, s44
	ds_read_b128 v[2:5], v133
	ds_read_b128 v[6:9], v133 offset:1024
	ds_read_b128 v[10:13], v133 offset:2048
	ds_read_b128 v[14:17], v133 offset:3072
	s_nop 0
	v_lshl_add_u64 v[18:19], s[2:3], 0, v[252:253]
	global_load_lds_dwordx4 v[18:19], off
	v_lshl_add_u64 v[18:19], s[74:75], 0, v[252:253]
	s_mov_b32 m0, s45
	s_nop 0
	global_load_lds_dwordx4 v[18:19], off
	s_barrier
	s_waitcnt lgkmcnt(0)
	s_setprio 1
	s_waitcnt lgkmcnt(0)
	v_mfma_scale_f32_16x16x128_f8f6f4 v[88:91], v[2:9], v[176:183], v[88:91], v154, v154 op_sel_hi:[0,0,0]
	v_mfma_scale_f32_16x16x128_f8f6f4 v[84:87], v[10:17], v[176:183], v[84:87], v154, v154 op_sel_hi:[0,0,0]
	v_mfma_scale_f32_16x16x128_f8f6f4 v[228:231], v[2:9], v[168:175], v[96:99], v154, v154 op_sel_hi:[0,0,0]
	v_mfma_scale_f32_16x16x128_f8f6f4 v[168:171], v[10:17], v[168:175], v[92:95], v154, v154 op_sel_hi:[0,0,0]
	v_mfma_scale_f32_16x16x128_f8f6f4 v[172:175], v[2:9], v[184:191], v[80:83], v154, v154 op_sel_hi:[0,0,0]
	v_mfma_scale_f32_16x16x128_f8f6f4 v[176:179], v[10:17], v[184:191], v[76:79], v154, v154 op_sel_hi:[0,0,0]
	v_mfma_scale_f32_16x16x128_f8f6f4 v[180:183], v[2:9], v[192:199], v[72:75], v154, v154 op_sel_hi:[0,0,0]
	v_mfma_scale_f32_16x16x128_f8f6f4 v[184:187], v[10:17], v[192:199], v[68:71], v154, v154 op_sel_hi:[0,0,0]
	s_setprio 0
	s_barrier
	s_nop 0
	s_mov_b64 s[76:77], 0x200
	ds_read_b128 v[18:21], v158 offset:16384
	ds_read_b128 v[22:25], v158 offset:17408
	ds_read_b128 v[26:29], v158 offset:18432
	ds_read_b128 v[30:33], v158 offset:19456
	ds_read_b128 v[68:71], v158 offset:20480
	ds_read_b128 v[72:75], v158 offset:21504
	ds_read_b128 v[76:79], v158 offset:22528
	ds_read_b128 v[80:83], v158 offset:23552
	s_add_u32 s94, s8, 0x200
	s_addc_u32 s95, s9, 0
	v_and_b32_e32 v34, 0xffff, v159
	v_lshl_add_u32 v34, v34, 10, v155
	s_mov_b32 m0, s47
	s_nop 0
	global_load_lds_dwordx4 v34, s[94:95]
	v_lshrrev_b32_e32 v34, 16, v159
	v_lshl_add_u32 v34, v34, 10, v155
	s_mov_b32 m0, s48
	s_nop 0
	global_load_lds_dwordx4 v34, s[94:95]
	s_barrier
; __device__ __forceinline__ int tid_hidden() { int t = threadIdx.x; asm volatile("" : "+v"(t)); return t; }
; #define lds lds_hidden(lds0)
; template <class Epi, class Src>
; __device__ __forceinline__ void gemm_phase(LAS unsigned char* lds, const Src S, const Epi E) {
;     ...
;         { const int tp = tid_hidden(); E.prefetch(cur, lds, par, tp, __builtin_amdgcn_readfirstlane(tp >> 6)); }
;         if (Src::GATHER && has_next) { const int tp = tid_hidden(); tab_fill(S, nxt, tp, __builtin_amdgcn_readfirstlane(tp >> 6), lds, par ^ 1); }
;         for (int t = 0; t < NKTR - 2; t += 2) {
;             const size_t k1 = (size_t)(t + 1) * kstep, k2 = (size_t)(t + 2) * kstep;
;             const char* b2 = cB + k2; const char* b3 = b2 + kstep;
;             G8_ITER(cA, par, k1, cA, par, k2, b2, b3);
	s_waitcnt lgkmcnt(0)
	s_setprio 1
	s_waitcnt lgkmcnt(0)
	v_mfma_scale_f32_16x16x128_f8f6f4 v[236:239], v[138:145], v[68:75], v[48:51], v154, v154 op_sel_hi:[0,0,0]
	v_mfma_scale_f32_16x16x128_f8f6f4 v[240:243], v[160:167], v[68:75], v[44:47], v154, v154 op_sel_hi:[0,0,0]
	v_mfma_scale_f32_16x16x128_f8f6f4 v[244:247], v[138:145], v[76:83], v[40:43], v154, v154 op_sel_hi:[0,0,0]
	v_mfma_scale_f32_16x16x128_f8f6f4 v[248:251], v[160:167], v[76:83], v[36:39], v154, v154 op_sel_hi:[0,0,0]
	v_mfma_scale_f32_16x16x128_f8f6f4 v[188:191], v[138:145], v[18:25], v[64:67], v154, v154 op_sel_hi:[0,0,0]
	v_mfma_scale_f32_16x16x128_f8f6f4 v[192:195], v[160:167], v[18:25], v[60:63], v154, v154 op_sel_hi:[0,0,0]
	v_mfma_scale_f32_16x16x128_f8f6f4 v[196:199], v[138:145], v[26:33], v[56:59], v154, v154 op_sel_hi:[0,0,0]
	v_mfma_scale_f32_16x16x128_f8f6f4 v[232:235], v[160:167], v[26:33], v[52:55], v154, v154 op_sel_hi:[0,0,0]
	s_setprio 0
	s_barrier
	s_add_u32 s2, s20, 0x20200
	s_addc_u32 s3, s21, 0
	s_add_u32 s74, s20, 0x30200
	s_addc_u32 s75, s21, 0
	s_mov_b32 m0, s50
	s_nop 0
	v_lshl_add_u64 v[36:37], s[2:3], 0, v[252:253]
	global_load_lds_dwordx4 v[36:37], off
	v_lshl_add_u64 v[36:37], s[74:75], 0, v[252:253]
	s_mov_b32 m0, s51
	s_nop 0
	global_load_lds_dwordx4 v[36:37], off
	s_waitcnt vmcnt(6)
	s_barrier
	s_setprio 1
	v_mfma_scale_f32_16x16x128_f8f6f4 v[146:149], v[2:9], v[18:25], v[100:103], v154, v154 op_sel_hi:[0,0,0]
	v_mfma_scale_f32_16x16x128_f8f6f4 v[18:21], v[10:17], v[18:25], v[104:107], v154, v154 op_sel_hi:[0,0,0]
	v_mfma_scale_f32_16x16x128_f8f6f4 v[22:25], v[2:9], v[26:33], v[108:111], v154, v154 op_sel_hi:[0,0,0]
	v_mfma_scale_f32_16x16x128_f8f6f4 v[26:29], v[10:17], v[26:33], v[112:115], v154, v154 op_sel_hi:[0,0,0]
	v_mfma_scale_f32_16x16x128_f8f6f4 v[30:33], v[2:9], v[68:75], v[116:119], v154, v154 op_sel_hi:[0,0,0]
	v_mfma_scale_f32_16x16x128_f8f6f4 v[36:39], v[10:17], v[68:75], v[120:123], v154, v154 op_sel_hi:[0,0,0]
	v_mfma_scale_f32_16x16x128_f8f6f4 v[72:75], v[2:9], v[76:83], v[124:127], v154, v154 op_sel_hi:[0,0,0]
	v_mfma_scale_f32_16x16x128_f8f6f4 v[76:79], v[10:17], v[76:83], v[128:131], v154, v154 op_sel_hi:[0,0,0]
	s_setprio 0
	s_barrier
	ds_read_b128 v[92:95], v135
	ds_read_b128 v[96:99], v135 offset:1024
	ds_read_b128 v[100:103], v135 offset:2048
	ds_read_b128 v[104:107], v135 offset:3072
	ds_read_b128 v[40:43], v158 offset:32768
	ds_read_b128 v[44:47], v158 offset:33792
	ds_read_b128 v[48:51], v158 offset:34816
	ds_read_b128 v[52:55], v158 offset:35840
	ds_read_b128 v[56:59], v158 offset:36864
	ds_read_b128 v[60:63], v158 offset:37888
	ds_read_b128 v[64:67], v158 offset:38912
	ds_read_b128 v[68:71], v158 offset:39936
	s_add_u32 s94, s8, 0x200
	s_addc_u32 s95, s9, 0
	v_and_b32_e32 v34, 0xffff, v255
	v_lshl_add_u32 v34, v34, 10, v155
	s_mov_b32 m0, s52
	s_nop 0
	global_load_lds_dwordx4 v34, s[94:95]
	v_lshrrev_b32_e32 v34, 16, v255
	v_lshl_add_u32 v34, v34, 10, v155
	s_mov_b32 m0, s53
	s_nop 0
	global_load_lds_dwordx4 v34, s[94:95]
	s_waitcnt lgkmcnt(8)
	s_barrier
	s_waitcnt lgkmcnt(0)
	s_setprio 1
	s_waitcnt lgkmcnt(0)
	v_mfma_scale_f32_16x16x128_f8f6f4 v[2:5], v[92:99], v[40:47], v[150:153], v154, v154 op_sel_hi:[0,0,0]
	v_mfma_scale_f32_16x16x128_f8f6f4 v[6:9], v[100:107], v[40:47], v[200:203], v154, v154 op_sel_hi:[0,0,0]
	v_mfma_scale_f32_16x16x128_f8f6f4 v[10:13], v[92:99], v[48:55], v[204:207], v154, v154 op_sel_hi:[0,0,0]
	v_mfma_scale_f32_16x16x128_f8f6f4 v[14:17], v[100:107], v[48:55], v[208:211], v154, v154 op_sel_hi:[0,0,0]
	v_mfma_scale_f32_16x16x128_f8f6f4 v[204:207], v[92:99], v[64:71], v[220:223], v154, v154 op_sel_hi:[0,0,0]
	v_mfma_scale_f32_16x16x128_f8f6f4 v[150:153], v[92:99], v[56:63], v[212:215], v154, v154 op_sel_hi:[0,0,0]
	v_mfma_scale_f32_16x16x128_f8f6f4 v[200:203], v[100:107], v[56:63], v[216:219], v154, v154 op_sel_hi:[0,0,0]
	v_mfma_scale_f32_16x16x128_f8f6f4 v[208:211], v[100:107], v[64:71], v[224:227], v154, v154 op_sel_hi:[0,0,0]
	s_setprio 0
	s_barrier
	s_add_u32 s2, s20, 0x280
	s_addc_u32 s3, s21, 0
	s_add_u32 s74, s20, 0x10280
	s_addc_u32 s75, s21, 0
	s_mov_b32 m0, s59
	ds_read_b128 v[124:127], v136
	ds_read_b128 v[128:131], v136 offset:1024
	ds_read_b128 v[138:141], v136 offset:2048
	ds_read_b128 v[142:145], v136 offset:3072
	s_nop 0
	v_lshl_add_u64 v[80:81], s[2:3], 0, v[252:253]
	global_load_lds_dwordx4 v[80:81], off
	v_lshl_add_u64 v[80:81], s[74:75], 0, v[252:253]
	s_mov_b32 m0, s60
	s_nop 0
	global_load_lds_dwordx4 v[80:81], off
	s_barrier
	s_waitcnt lgkmcnt(0)
	s_setprio 1
	s_waitcnt lgkmcnt(0)
	v_mfma_scale_f32_16x16x128_f8f6f4 v[212:215], v[124:131], v[40:47], v[228:231], v154, v154 op_sel_hi:[0,0,0]
	v_mfma_scale_f32_16x16x128_f8f6f4 v[40:43], v[138:145], v[40:47], v[168:171], v154, v154 op_sel_hi:[0,0,0]
	v_mfma_scale_f32_16x16x128_f8f6f4 v[44:47], v[124:131], v[48:55], v[88:91], v154, v154 op_sel_hi:[0,0,0]
	v_mfma_scale_f32_16x16x128_f8f6f4 v[48:51], v[138:145], v[48:55], v[84:87], v154, v154 op_sel_hi:[0,0,0]
	v_mfma_scale_f32_16x16x128_f8f6f4 v[52:55], v[124:131], v[56:63], v[172:175], v154, v154 op_sel_hi:[0,0,0]
	v_mfma_scale_f32_16x16x128_f8f6f4 v[56:59], v[138:145], v[56:63], v[176:179], v154, v154 op_sel_hi:[0,0,0]
	v_mfma_scale_f32_16x16x128_f8f6f4 v[60:63], v[124:131], v[64:71], v[180:183], v154, v154 op_sel_hi:[0,0,0]
	v_mfma_scale_f32_16x16x128_f8f6f4 v[64:67], v[138:145], v[64:71], v[184:187], v154, v154 op_sel_hi:[0,0,0]
	s_setprio 0
	s_barrier
; __device__ __forceinline__ int tid_hidden() { int t = threadIdx.x; asm volatile("" : "+v"(t)); return t; }
; #define lds lds_hidden(lds0)
; template <class Epi, class Src>
; __device__ __forceinline__ void gemm_phase(LAS unsigned char* lds, const Src S, const Epi E) {
;     ...
;         { const int tp = tid_hidden(); E.prefetch(cur, lds, par, tp, __builtin_amdgcn_readfirstlane(tp >> 6)); }
;         if (Src::GATHER && has_next) { const int tp = tid_hidden(); tab_fill(S, nxt, tp, __builtin_amdgcn_readfirstlane(tp >> 6), lds, par ^ 1); }
;         for (int t = 0; t < NKTR - 2; t += 2) {
;             const size_t k1 = (size_t)(t + 1) * kstep, k2 = (size_t)(t + 2) * kstep;
;             const char* b2 = cB + k2; const char* b3 = b2 + kstep;
;             G8_ITER(cA, par, k1, cA, par, k2, b2, b3);
	s_mov_b64 s[76:77], 0x280
	ds_read_b128 v[108:111], v158 offset:49152
	ds_read_b128 v[112:115], v158 offset:50176
	ds_read_b128 v[116:119], v158 offset:51200
	ds_read_b128 v[120:123], v158 offset:52224
	ds_read_b128 v[160:163], v158 offset:53248
	ds_read_b128 v[164:167], v158 offset:54272
	ds_read_b128 v[168:171], v158 offset:55296
	ds_read_b128 v[172:175], v158 offset:56320
	s_add_u32 s94, s8, 0x280
	s_addc_u32 s95, s9, 0
	v_and_b32_e32 v34, 0xffff, v159
	v_lshl_add_u32 v34, v34, 10, v155
	s_mov_b32 m0, s61
	s_nop 0
	global_load_lds_dwordx4 v34, s[94:95]
	v_lshrrev_b32_e32 v34, 16, v159
	v_lshl_add_u32 v34, v34, 10, v155
	s_mov_b32 m0, s62
	s_nop 0
	global_load_lds_dwordx4 v34, s[94:95]
	s_barrier
	s_waitcnt lgkmcnt(0)
	s_setprio 1
	s_waitcnt lgkmcnt(0)
	v_mfma_scale_f32_16x16x128_f8f6f4 v[68:71], v[92:99], v[108:115], v[188:191], v154, v154 op_sel_hi:[0,0,0]
	v_mfma_scale_f32_16x16x128_f8f6f4 v[220:223], v[92:99], v[116:123], v[196:199], v154, v154 op_sel_hi:[0,0,0]
	v_mfma_scale_f32_16x16x128_f8f6f4 v[80:83], v[100:107], v[116:123], v[232:235], v154, v154 op_sel_hi:[0,0,0]
	v_mfma_scale_f32_16x16x128_f8f6f4 v[84:87], v[92:99], v[160:167], v[236:239], v154, v154 op_sel_hi:[0,0,0]
	v_mfma_scale_f32_16x16x128_f8f6f4 v[88:91], v[100:107], v[160:167], v[240:243], v154, v154 op_sel_hi:[0,0,0]
	v_mfma_scale_f32_16x16x128_f8f6f4 v[92:95], v[92:99], v[168:175], v[244:247], v154, v154 op_sel_hi:[0,0,0]
	v_mfma_scale_f32_16x16x128_f8f6f4 v[96:99], v[100:107], v[168:175], v[248:251], v154, v154 op_sel_hi:[0,0,0]
	v_mfma_scale_f32_16x16x128_f8f6f4 v[216:219], v[100:107], v[108:115], v[192:195], v154, v154 op_sel_hi:[0,0,0]
	s_setprio 0
	s_barrier
	s_add_u32 s2, s20, 0x20280
	s_addc_u32 s3, s21, 0
	s_add_u32 s74, s20, 0x30280
	s_addc_u32 s75, s21, 0
	s_mov_b32 m0, s64
	s_nop 0
	v_lshl_add_u64 v[100:101], s[2:3], 0, v[252:253]
	global_load_lds_dwordx4 v[100:101], off
	v_lshl_add_u64 v[100:101], s[74:75], 0, v[252:253]
	s_mov_b32 m0, s65
	s_nop 0
	global_load_lds_dwordx4 v[100:101], off
	s_waitcnt vmcnt(6)
	s_barrier
	s_setprio 1
	v_mfma_scale_f32_16x16x128_f8f6f4 v[100:103], v[124:131], v[108:115], v[146:149], v154, v154 op_sel_hi:[0,0,0]
	v_mfma_scale_f32_16x16x128_f8f6f4 v[104:107], v[138:145], v[108:115], v[18:21], v154, v154 op_sel_hi:[0,0,0]
	v_mfma_scale_f32_16x16x128_f8f6f4 v[108:111], v[124:131], v[116:123], v[22:25], v154, v154 op_sel_hi:[0,0,0]
	v_mfma_scale_f32_16x16x128_f8f6f4 v[112:115], v[138:145], v[116:123], v[26:29], v154, v154 op_sel_hi:[0,0,0]
	v_mfma_scale_f32_16x16x128_f8f6f4 v[116:119], v[124:131], v[160:167], v[30:33], v154, v154 op_sel_hi:[0,0,0]
	v_mfma_scale_f32_16x16x128_f8f6f4 v[120:123], v[138:145], v[160:167], v[36:39], v154, v154 op_sel_hi:[0,0,0]
	v_mfma_scale_f32_16x16x128_f8f6f4 v[124:127], v[124:131], v[168:175], v[72:75], v154, v154 op_sel_hi:[0,0,0]
	v_mfma_scale_f32_16x16x128_f8f6f4 v[128:131], v[138:145], v[168:175], v[76:79], v154, v154 op_sel_hi:[0,0,0]
	s_setprio 0
	s_barrier
	s_add_u32 s2, s20, 0x300
	s_addc_u32 s3, s21, 0
	ds_read_b128 v[138:141], v132
	ds_read_b128 v[142:145], v132 offset:1024
	ds_read_b128 v[160:163], v132 offset:2048
	ds_read_b128 v[164:167], v132 offset:3072
	ds_read_b128 v[168:171], v158
	ds_read_b128 v[172:175], v158 offset:1024
	ds_read_b128 v[176:179], v158 offset:2048
	ds_read_b128 v[180:183], v158 offset:3072
	ds_read_b128 v[184:187], v158 offset:4096
	ds_read_b128 v[188:191], v158 offset:5120
	ds_read_b128 v[192:195], v158 offset:6144
	ds_read_b128 v[196:199], v158 offset:7168
	s_add_u32 s94, s8, 0x280
	s_addc_u32 s95, s9, 0
	v_and_b32_e32 v34, 0xffff, v255
	v_lshl_add_u32 v34, v34, 10, v155
	s_mov_b32 m0, s23
	s_nop 0
	global_load_lds_dwordx4 v34, s[94:95]
	v_lshrrev_b32_e32 v34, 16, v255
	v_lshl_add_u32 v34, v34, 10, v155
	s_mov_b32 m0, s17
	s_nop 0
	global_load_lds_dwordx4 v34, s[94:95]
	s_waitcnt lgkmcnt(8)
	s_barrier
	s_waitcnt lgkmcnt(0)
	s_setprio 1
	s_waitcnt lgkmcnt(0)
	v_mfma_scale_f32_16x16x128_f8f6f4 v[204:207], v[138:145], v[192:199], v[204:207], v154, v154 op_sel_hi:[0,0,0]
	v_mfma_scale_f32_16x16x128_f8f6f4 v[146:149], v[138:145], v[168:175], v[2:5], v154, v154 op_sel_hi:[0,0,0]
	v_mfma_scale_f32_16x16x128_f8f6f4 v[224:227], v[160:167], v[168:175], v[6:9], v154, v154 op_sel_hi:[0,0,0]
	v_mfma_scale_f32_16x16x128_f8f6f4 v[228:231], v[138:145], v[176:183], v[10:13], v154, v154 op_sel_hi:[0,0,0]
	v_mfma_scale_f32_16x16x128_f8f6f4 v[232:235], v[160:167], v[176:183], v[14:17], v154, v154 op_sel_hi:[0,0,0]
	v_mfma_scale_f32_16x16x128_f8f6f4 v[150:153], v[138:145], v[184:191], v[150:153], v154, v154 op_sel_hi:[0,0,0]
	v_mfma_scale_f32_16x16x128_f8f6f4 v[200:203], v[160:167], v[184:191], v[200:203], v154, v154 op_sel_hi:[0,0,0]
	v_mfma_scale_f32_16x16x128_f8f6f4 v[208:211], v[160:167], v[192:199], v[208:211], v154, v154 op_sel_hi:[0,0,0]
	s_setprio 0
	s_barrier
	s_add_u32 s74, s20, 0x10300
	s_addc_u32 s75, s21, 0
	s_mov_b32 m0, s44
	ds_read_b128 v[2:5], v133
	ds_read_b128 v[6:9], v133 offset:1024
	ds_read_b128 v[10:13], v133 offset:2048
	ds_read_b128 v[14:17], v133 offset:3072
	s_nop 0
	v_lshl_add_u64 v[18:19], s[2:3], 0, v[252:253]
	global_load_lds_dwordx4 v[18:19], off
	v_lshl_add_u64 v[18:19], s[74:75], 0, v[252:253]
	s_mov_b32 m0, s45
	s_nop 0
	global_load_lds_dwordx4 v[18:19], off
	s_barrier
; __device__ __forceinline__ int tid_hidden() { int t = threadIdx.x; asm volatile("" : "+v"(t)); return t; }
; #define lds lds_hidden(lds0)
; template <class Epi, class Src>
; __device__ __forceinline__ void gemm_phase(LAS unsigned char* lds, const Src S, const Epi E) {
;     ...
;         { const int tp = tid_hidden(); E.prefetch(cur, lds, par, tp, __builtin_amdgcn_readfirstlane(tp >> 6)); }
;         if (Src::GATHER && has_next) { const int tp = tid_hidden(); tab_fill(S, nxt, tp, __builtin_amdgcn_readfirstlane(tp >> 6), lds, par ^ 1); }
;         for (int t = 0; t < NKTR - 2; t += 2) {
;             const size_t k1 = (size_t)(t + 1) * kstep, k2 = (size_t)(t + 2) * kstep;
;             const char* b2 = cB + k2; const char* b3 = b2 + kstep;
;             G8_ITER(cA, par, k1, cA, par, k2, b2, b3);
	s_waitcnt lgkmcnt(0)
	s_setprio 1
	s_waitcnt lgkmcnt(0)
	v_mfma_scale_f32_16x16x128_f8f6f4 v[64:67], v[10:17], v[192:199], v[64:67], v154, v154 op_sel_hi:[0,0,0]
	v_mfma_scale_f32_16x16x128_f8f6f4 v[212:215], v[2:9], v[168:175], v[212:215], v154, v154 op_sel_hi:[0,0,0]
	v_mfma_scale_f32_16x16x128_f8f6f4 v[168:171], v[10:17], v[168:175], v[40:43], v154, v154 op_sel_hi:[0,0,0]
	v_mfma_scale_f32_16x16x128_f8f6f4 v[172:175], v[2:9], v[176:183], v[44:47], v154, v154 op_sel_hi:[0,0,0]
	v_mfma_scale_f32_16x16x128_f8f6f4 v[176:179], v[10:17], v[176:183], v[48:51], v154, v154 op_sel_hi:[0,0,0]
	v_mfma_scale_f32_16x16x128_f8f6f4 v[180:183], v[2:9], v[184:191], v[52:55], v154, v154 op_sel_hi:[0,0,0]
	v_mfma_scale_f32_16x16x128_f8f6f4 v[184:187], v[10:17], v[184:191], v[56:59], v154, v154 op_sel_hi:[0,0,0]
	v_mfma_scale_f32_16x16x128_f8f6f4 v[188:191], v[2:9], v[192:199], v[60:63], v154, v154 op_sel_hi:[0,0,0]
	s_setprio 0
	s_barrier
	s_nop 2
	s_mov_b64 s[76:77], 0x300
	ds_read_b128 v[18:21], v158 offset:16384
	ds_read_b128 v[22:25], v158 offset:17408
	ds_read_b128 v[26:29], v158 offset:18432
	ds_read_b128 v[30:33], v158 offset:19456
	ds_read_b128 v[36:39], v158 offset:20480
	ds_read_b128 v[40:43], v158 offset:21504
	ds_read_b128 v[44:47], v158 offset:22528
	ds_read_b128 v[48:51], v158 offset:23552
	s_add_u32 s94, s8, 0x300
	s_addc_u32 s95, s9, 0
	v_and_b32_e32 v34, 0xffff, v159
	v_lshl_add_u32 v34, v34, 10, v155
	s_mov_b32 m0, s47
	s_nop 0
	global_load_lds_dwordx4 v34, s[94:95]
	v_lshrrev_b32_e32 v34, 16, v159
	v_lshl_add_u32 v34, v34, 10, v155
	s_mov_b32 m0, s48
	s_nop 0
	global_load_lds_dwordx4 v34, s[94:95]
	s_barrier
	s_waitcnt lgkmcnt(0)
	s_setprio 1
	s_waitcnt lgkmcnt(0)
	v_mfma_scale_f32_16x16x128_f8f6f4 v[236:239], v[138:145], v[36:43], v[84:87], v154, v154 op_sel_hi:[0,0,0]
	v_mfma_scale_f32_16x16x128_f8f6f4 v[240:243], v[160:167], v[36:43], v[88:91], v154, v154 op_sel_hi:[0,0,0]
	v_mfma_scale_f32_16x16x128_f8f6f4 v[192:195], v[138:145], v[18:25], v[68:71], v154, v154 op_sel_hi:[0,0,0]
	v_mfma_scale_f32_16x16x128_f8f6f4 v[196:199], v[160:167], v[18:25], v[216:219], v154, v154 op_sel_hi:[0,0,0]
	v_mfma_scale_f32_16x16x128_f8f6f4 v[216:219], v[138:145], v[26:33], v[220:223], v154, v154 op_sel_hi:[0,0,0]
	v_mfma_scale_f32_16x16x128_f8f6f4 v[220:223], v[160:167], v[26:33], v[80:83], v154, v154 op_sel_hi:[0,0,0]
	v_mfma_scale_f32_16x16x128_f8f6f4 v[138:141], v[138:145], v[44:51], v[92:95], v154, v154 op_sel_hi:[0,0,0]
	v_mfma_scale_f32_16x16x128_f8f6f4 v[142:145], v[160:167], v[44:51], v[96:99], v154, v154 op_sel_hi:[0,0,0]
	s_setprio 0
	s_barrier
	s_add_u32 s2, s20, 0x20300
	s_addc_u32 s3, s21, 0
	s_add_u32 s74, s20, 0x30300
	s_addc_u32 s75, s21, 0
	s_mov_b32 m0, s50
	s_nop 0
	v_lshl_add_u64 v[52:53], s[2:3], 0, v[252:253]
	global_load_lds_dwordx4 v[52:53], off
	v_lshl_add_u64 v[52:53], s[74:75], 0, v[252:253]
	s_mov_b32 m0, s51
	s_nop 0
	global_load_lds_dwordx4 v[52:53], off
	s_waitcnt vmcnt(6)
	s_barrier
	s_setprio 1
	v_mfma_scale_f32_16x16x128_f8f6f4 v[160:163], v[2:9], v[18:25], v[100:103], v154, v154 op_sel_hi:[0,0,0]
	v_mfma_scale_f32_16x16x128_f8f6f4 v[164:167], v[10:17], v[18:25], v[104:107], v154, v154 op_sel_hi:[0,0,0]
	v_mfma_scale_f32_16x16x128_f8f6f4 v[244:247], v[2:9], v[26:33], v[108:111], v154, v154 op_sel_hi:[0,0,0]
	v_mfma_scale_f32_16x16x128_f8f6f4 v[248:251], v[10:17], v[26:33], v[112:115], v154, v154 op_sel_hi:[0,0,0]
	v_mfma_scale_f32_16x16x128_f8f6f4 v[18:21], v[2:9], v[36:43], v[116:119], v154, v154 op_sel_hi:[0,0,0]
	v_mfma_scale_f32_16x16x128_f8f6f4 v[22:25], v[10:17], v[36:43], v[120:123], v154, v154 op_sel_hi:[0,0,0]
	v_mfma_scale_f32_16x16x128_f8f6f4 v[6:9], v[2:9], v[44:51], v[124:127], v154, v154 op_sel_hi:[0,0,0]
	v_mfma_scale_f32_16x16x128_f8f6f4 v[10:13], v[10:17], v[44:51], v[128:131], v154, v154 op_sel_hi:[0,0,0]
	s_setprio 0
	s_barrier
	ds_read_b128 v[68:71], v135
	ds_read_b128 v[72:75], v135 offset:1024
	ds_read_b128 v[76:79], v135 offset:2048
	ds_read_b128 v[80:83], v135 offset:3072
	ds_read_b128 v[40:43], v158 offset:32768
	ds_read_b128 v[44:47], v158 offset:33792
	ds_read_b128 v[48:51], v158 offset:34816
	ds_read_b128 v[52:55], v158 offset:35840
	ds_read_b128 v[56:59], v158 offset:36864
	ds_read_b128 v[60:63], v158 offset:37888
	ds_read_b128 v[84:87], v158 offset:38912
	ds_read_b128 v[88:91], v158 offset:39936
	s_add_u32 s94, s8, 0x300
	s_addc_u32 s95, s9, 0
	v_and_b32_e32 v34, 0xffff, v255
	v_lshl_add_u32 v34, v34, 10, v155
	s_mov_b32 m0, s52
	s_nop 0
	global_load_lds_dwordx4 v34, s[94:95]
	v_lshrrev_b32_e32 v34, 16, v255
	v_lshl_add_u32 v34, v34, 10, v155
	s_mov_b32 m0, s53
	s_nop 0
	global_load_lds_dwordx4 v34, s[94:95]
	s_waitcnt lgkmcnt(8)
	s_barrier
	s_waitcnt lgkmcnt(0)
	s_setprio 1
	s_waitcnt lgkmcnt(0)
	v_mfma_scale_f32_16x16x128_f8f6f4 v[2:5], v[68:75], v[40:47], v[146:149], v154, v154 op_sel_hi:[0,0,0]
	v_mfma_scale_f32_16x16x128_f8f6f4 v[14:17], v[76:83], v[48:55], v[232:235], v154, v154 op_sel_hi:[0,0,0]
	v_mfma_scale_f32_16x16x128_f8f6f4 v[26:29], v[68:75], v[84:91], v[204:207], v154, v154 op_sel_hi:[0,0,0]
	v_mfma_scale_f32_16x16x128_f8f6f4 v[30:33], v[76:83], v[84:91], v[208:211], v154, v154 op_sel_hi:[0,0,0]
	v_mfma_scale_f32_16x16x128_f8f6f4 v[224:227], v[76:83], v[40:47], v[224:227], v154, v154 op_sel_hi:[0,0,0]
	v_mfma_scale_f32_16x16x128_f8f6f4 v[228:231], v[68:75], v[48:55], v[228:231], v154, v154 op_sel_hi:[0,0,0]
	v_mfma_scale_f32_16x16x128_f8f6f4 v[146:149], v[68:75], v[56:63], v[150:153], v154, v154 op_sel_hi:[0,0,0]
	v_mfma_scale_f32_16x16x128_f8f6f4 v[150:153], v[76:83], v[56:63], v[200:203], v154, v154 op_sel_hi:[0,0,0]
	s_setprio 0
	s_barrier
; __device__ __forceinline__ int tid_hidden() { int t = threadIdx.x; asm volatile("" : "+v"(t)); return t; }
; #define lds lds_hidden(lds0)
; template <class Epi, class Src>
; __device__ __forceinline__ void gemm_phase(LAS unsigned char* lds, const Src S, const Epi E) {
;     ...
;         { const int tp = tid_hidden(); E.prefetch(cur, lds, par, tp, __builtin_amdgcn_readfirstlane(tp >> 6)); }
;         if (Src::GATHER && has_next) { const int tp = tid_hidden(); tab_fill(S, nxt, tp, __builtin_amdgcn_readfirstlane(tp >> 6), lds, par ^ 1); }
;         for (int t = 0; t < NKTR - 2; t += 2) {
;             const size_t k1 = (size_t)(t + 1) * kstep, k2 = (size_t)(t + 2) * kstep;
;             const char* b2 = cB + k2; const char* b3 = b2 + kstep;
;             G8_ITER(cA, par, k1, cA, par, k2, b2, b3);
	s_add_u32 s2, s20, 0x380
	s_addc_u32 s3, s21, 0
	s_add_u32 s74, s20, 0x10380
	s_addc_u32 s75, s21, 0
	s_mov_b32 m0, s59
	ds_read_b128 v[92:95], v136
	ds_read_b128 v[96:99], v136 offset:1024
	ds_read_b128 v[100:103], v136 offset:2048
	ds_read_b128 v[104:107], v136 offset:3072
	s_nop 0
	v_lshl_add_u64 v[36:37], s[2:3], 0, v[252:253]
	global_load_lds_dwordx4 v[36:37], off
	v_lshl_add_u64 v[36:37], s[74:75], 0, v[252:253]
	s_mov_b32 m0, s60
	s_nop 0
	global_load_lds_dwordx4 v[36:37], off
	s_barrier
	s_waitcnt lgkmcnt(0)
	s_setprio 1
	s_waitcnt lgkmcnt(0)
	v_mfma_scale_f32_16x16x128_f8f6f4 v[36:39], v[92:99], v[40:47], v[212:215], v154, v154 op_sel_hi:[0,0,0]
	v_mfma_scale_f32_16x16x128_f8f6f4 v[40:43], v[100:107], v[40:47], v[168:171], v154, v154 op_sel_hi:[0,0,0]
	v_mfma_scale_f32_16x16x128_f8f6f4 v[44:47], v[92:99], v[48:55], v[172:175], v154, v154 op_sel_hi:[0,0,0]
	v_mfma_scale_f32_16x16x128_f8f6f4 v[48:51], v[100:107], v[48:55], v[176:179], v154, v154 op_sel_hi:[0,0,0]
	v_mfma_scale_f32_16x16x128_f8f6f4 v[52:55], v[92:99], v[56:63], v[180:183], v154, v154 op_sel_hi:[0,0,0]
	v_mfma_scale_f32_16x16x128_f8f6f4 v[56:59], v[100:107], v[56:63], v[184:187], v154, v154 op_sel_hi:[0,0,0]
	v_mfma_scale_f32_16x16x128_f8f6f4 v[60:63], v[92:99], v[84:91], v[188:191], v154, v154 op_sel_hi:[0,0,0]
	v_mfma_scale_f32_16x16x128_f8f6f4 v[64:67], v[100:107], v[84:91], v[64:67], v154, v154 op_sel_hi:[0,0,0]
	s_setprio 0
	s_barrier
	s_mov_b64 s[76:77], 0x380
	ds_read_b128 v[84:87], v158 offset:49152
	ds_read_b128 v[88:91], v158 offset:50176
	ds_read_b128 v[108:111], v158 offset:51200
	ds_read_b128 v[112:115], v158 offset:52224
	ds_read_b128 v[116:119], v158 offset:53248
	ds_read_b128 v[120:123], v158 offset:54272
	ds_read_b128 v[124:127], v158 offset:55296
	ds_read_b128 v[128:131], v158 offset:56320
	s_add_u32 s94, s8, 0x380
	s_addc_u32 s95, s9, 0
	v_and_b32_e32 v34, 0xffff, v159
	v_lshl_add_u32 v34, v34, 10, v155
	s_mov_b32 m0, s61
	s_nop 0
	global_load_lds_dwordx4 v34, s[94:95]
	v_lshrrev_b32_e32 v34, 16, v159
	v_lshl_add_u32 v34, v34, 10, v155
	s_mov_b32 m0, s62
	s_nop 0
	global_load_lds_dwordx4 v34, s[94:95]
	s_barrier
	s_waitcnt lgkmcnt(0)
	s_setprio 1
	s_waitcnt lgkmcnt(0)
	v_mfma_scale_f32_16x16x128_f8f6f4 v[168:171], v[68:75], v[84:91], v[192:195], v154, v154 op_sel_hi:[0,0,0]
	v_mfma_scale_f32_16x16x128_f8f6f4 v[172:175], v[76:83], v[84:91], v[196:199], v154, v154 op_sel_hi:[0,0,0]
	v_mfma_scale_f32_16x16x128_f8f6f4 v[176:179], v[68:75], v[108:115], v[216:219], v154, v154 op_sel_hi:[0,0,0]
	v_mfma_scale_f32_16x16x128_f8f6f4 v[180:183], v[76:83], v[108:115], v[220:223], v154, v154 op_sel_hi:[0,0,0]
	v_mfma_scale_f32_16x16x128_f8f6f4 v[184:187], v[68:75], v[116:123], v[236:239], v154, v154 op_sel_hi:[0,0,0]
	v_mfma_scale_f32_16x16x128_f8f6f4 v[188:191], v[76:83], v[116:123], v[240:243], v154, v154 op_sel_hi:[0,0,0]
	v_mfma_scale_f32_16x16x128_f8f6f4 v[138:141], v[68:75], v[124:131], v[138:141], v154, v154 op_sel_hi:[0,0,0]
	v_mfma_scale_f32_16x16x128_f8f6f4 v[142:145], v[76:83], v[124:131], v[142:145], v154, v154 op_sel_hi:[0,0,0]
	s_setprio 0
	s_barrier
	s_add_u32 s2, s20, 0x20380
	s_addc_u32 s3, s21, 0
	s_add_u32 s74, s20, 0x30380
	s_addc_u32 s75, s21, 0
	s_mov_b32 m0, s64
	s_nop 0
	v_lshl_add_u64 v[68:69], s[2:3], 0, v[252:253]
	global_load_lds_dwordx4 v[68:69], off
	v_lshl_add_u64 v[68:69], s[74:75], 0, v[252:253]
	s_mov_b32 m0, s65
	s_nop 0
	global_load_lds_dwordx4 v[68:69], off
	s_waitcnt vmcnt(6)
	s_barrier
	s_setprio 1
	v_mfma_scale_f32_16x16x128_f8f6f4 v[200:203], v[92:99], v[116:123], v[18:21], v154, v154 op_sel_hi:[0,0,0]
	v_mfma_scale_f32_16x16x128_f8f6f4 v[116:119], v[100:107], v[116:123], v[22:25], v154, v154 op_sel_hi:[0,0,0]
	v_mfma_scale_f32_16x16x128_f8f6f4 v[120:123], v[92:99], v[124:131], v[6:9], v154, v154 op_sel_hi:[0,0,0]
	v_mfma_scale_f32_16x16x128_f8f6f4 v[124:127], v[100:107], v[124:131], v[10:13], v154, v154 op_sel_hi:[0,0,0]
	v_mfma_scale_f32_16x16x128_f8f6f4 v[160:163], v[92:99], v[84:91], v[160:163], v154, v154 op_sel_hi:[0,0,0]
	v_mfma_scale_f32_16x16x128_f8f6f4 v[164:167], v[100:107], v[84:91], v[164:167], v154, v154 op_sel_hi:[0,0,0]
	v_mfma_scale_f32_16x16x128_f8f6f4 v[192:195], v[92:99], v[108:115], v[244:247], v154, v154 op_sel_hi:[0,0,0]
	v_mfma_scale_f32_16x16x128_f8f6f4 v[196:199], v[100:107], v[108:115], v[248:251], v154, v154 op_sel_hi:[0,0,0]
	s_setprio 0
	s_barrier
	s_xor_b32 s3, s68, 1
	s_and_b64 s[74:75], s[24:25], exec
	s_cselect_b32 s2, s3, s68
	ds_read_b128 v[68:71], v132
	ds_read_b128 v[72:75], v132 offset:1024
	ds_read_b128 v[76:79], v132 offset:2048
	ds_read_b128 v[80:83], v132 offset:3072
	ds_read_b128 v[84:87], v158
	ds_read_b128 v[88:91], v158 offset:1024
	ds_read_b128 v[92:95], v158 offset:2048
	ds_read_b128 v[96:99], v158 offset:3072
	ds_read_b128 v[100:103], v158 offset:4096
	ds_read_b128 v[104:107], v158 offset:5120
	ds_read_b128 v[108:111], v158 offset:6144
	ds_read_b128 v[112:115], v158 offset:7168
	s_add_u32 s94, s8, 0x380
	s_addc_u32 s95, s9, 0
	v_and_b32_e32 v34, 0xffff, v255
	v_lshl_add_u32 v34, v34, 10, v155
	s_mov_b32 m0, s23
	s_nop 0
	global_load_lds_dwordx4 v34, s[94:95]
	v_lshrrev_b32_e32 v34, 16, v255
	v_lshl_add_u32 v34, v34, 10, v155
	s_mov_b32 m0, s17
	s_nop 0
	global_load_lds_dwordx4 v34, s[94:95]
	s_waitcnt lgkmcnt(8)
	s_barrier
; __device__ __forceinline__ int tid_hidden() { int t = threadIdx.x; asm volatile("" : "+v"(t)); return t; }
; #define lds lds_hidden(lds0)
; template <class Epi, class Src>
; __device__ __forceinline__ void gemm_phase(LAS unsigned char* lds, const Src S, const Epi E) {
;     ...
;         { const int tp = tid_hidden(); E.prefetch(cur, lds, par, tp, __builtin_amdgcn_readfirstlane(tp >> 6)); }
;         if (Src::GATHER && has_next) { const int tp = tid_hidden(); tab_fill(S, nxt, tp, __builtin_amdgcn_readfirstlane(tp >> 6), lds, par ^ 1); }
;         for (int t = 0; t < NKTR - 2; t += 2) {
;             const size_t k1 = (size_t)(t + 1) * kstep, k2 = (size_t)(t + 2) * kstep;
;             const char* b2 = cB + k2; const char* b3 = b2 + kstep;
;             G8_ITER(cA, par, k1, cA, par, k2, b2, b3);
;         }
;         {
;             const int par2 = has_next ? (par ^ 1) : par;
;             const char* b3 = nB + kstep;
;             G8_ITER(cA, par, (size_t)(NKTR - 1) * kstep, nA, par2, (size_t)0, nB, b3);
;         }
	s_waitcnt lgkmcnt(0)
	s_setprio 1
	s_waitcnt lgkmcnt(0)
	v_mfma_scale_f32_16x16x128_f8f6f4 v[128:131], v[68:75], v[84:91], v[2:5], v154, v154 op_sel_hi:[0,0,0]
	v_mfma_scale_f32_16x16x128_f8f6f4 v[204:207], v[76:83], v[84:91], v[224:227], v154, v154 op_sel_hi:[0,0,0]
	v_mfma_scale_f32_16x16x128_f8f6f4 v[208:211], v[68:75], v[92:99], v[228:231], v154, v154 op_sel_hi:[0,0,0]
	v_mfma_scale_f32_16x16x128_f8f6f4 v[212:215], v[76:83], v[92:99], v[14:17], v154, v154 op_sel_hi:[0,0,0]
	v_mfma_scale_f32_16x16x128_f8f6f4 v[146:149], v[68:75], v[100:107], v[146:149], v154, v154 op_sel_hi:[0,0,0]
	v_mfma_scale_f32_16x16x128_f8f6f4 v[150:153], v[76:83], v[100:107], v[150:153], v154, v154 op_sel_hi:[0,0,0]
	v_mfma_scale_f32_16x16x128_f8f6f4 v[216:219], v[68:75], v[108:115], v[26:29], v154, v154 op_sel_hi:[0,0,0]
	v_mfma_scale_f32_16x16x128_f8f6f4 v[220:223], v[76:83], v[108:115], v[30:33], v154, v154 op_sel_hi:[0,0,0]
	s_setprio 0
	s_barrier
	s_add_u32 s74, s0, 0x10000
	s_addc_u32 s75, s1, 0
	s_mov_b64 s[76:77], s[0:1]
	s_mov_b32 m0, s44
	ds_read_b128 v[2:5], v133
	ds_read_b128 v[6:9], v133 offset:1024
	ds_read_b128 v[10:13], v133 offset:2048
	ds_read_b128 v[14:17], v133 offset:3072
	s_nop 0
	v_lshl_add_u64 v[18:19], s[76:77], 0, v[252:253]
	global_load_lds_dwordx4 v[18:19], off
	v_lshl_add_u64 v[18:19], s[74:75], 0, v[252:253]
	s_mov_b32 m0, s45
	s_nop 0
	global_load_lds_dwordx4 v[18:19], off
	s_barrier
	s_waitcnt lgkmcnt(0)
	s_setprio 1
	s_waitcnt lgkmcnt(0)
	v_mfma_scale_f32_16x16x128_f8f6f4 v[224:227], v[2:9], v[84:91], v[36:39], v154, v154 op_sel_hi:[0,0,0]
	v_mfma_scale_f32_16x16x128_f8f6f4 v[84:87], v[10:17], v[84:91], v[40:43], v154, v154 op_sel_hi:[0,0,0]
	v_mfma_scale_f32_16x16x128_f8f6f4 v[88:91], v[2:9], v[92:99], v[44:47], v154, v154 op_sel_hi:[0,0,0]
	v_mfma_scale_f32_16x16x128_f8f6f4 v[52:55], v[2:9], v[100:107], v[52:55], v154, v154 op_sel_hi:[0,0,0]
	v_mfma_scale_f32_16x16x128_f8f6f4 v[56:59], v[10:17], v[100:107], v[56:59], v154, v154 op_sel_hi:[0,0,0]
	v_mfma_scale_f32_16x16x128_f8f6f4 v[60:63], v[2:9], v[108:115], v[60:63], v154, v154 op_sel_hi:[0,0,0]
	v_mfma_scale_f32_16x16x128_f8f6f4 v[64:67], v[10:17], v[108:115], v[64:67], v154, v154 op_sel_hi:[0,0,0]
	v_mfma_scale_f32_16x16x128_f8f6f4 v[228:231], v[10:17], v[92:99], v[48:51], v154, v154 op_sel_hi:[0,0,0]
	s_setprio 0
	v_lshl_add_u32 v34, s2, 10, v156
	s_barrier
	ds_read2st64_b32 v[92:93], v34 offset1:1
	ds_read_b128 v[18:21], v158 offset:16384
	ds_read_b128 v[22:25], v158 offset:17408
	ds_read_b128 v[26:29], v158 offset:18432
	ds_read_b128 v[30:33], v158 offset:19456
	ds_read_b128 v[36:39], v158 offset:20480
	ds_read_b128 v[40:43], v158 offset:21504
	ds_read_b128 v[44:47], v158 offset:22528
	ds_read_b128 v[48:51], v158 offset:23552
	s_mov_b32 m0, s47
	s_waitcnt lgkmcnt(8)
	v_lshl_or_b32 v159, v93, 16, v92
	v_lshl_add_u32 v92, v92, 10, v155
	global_load_lds_dwordx4 v92, s[8:9]
	v_lshl_add_u32 v92, v93, 10, v155
	s_mov_b32 m0, s48
	s_nop 0
	global_load_lds_dwordx4 v92, s[8:9]
	s_barrier
	s_waitcnt lgkmcnt(0)
	s_setprio 1
	s_waitcnt lgkmcnt(0)
	v_mfma_scale_f32_16x16x128_f8f6f4 v[236:239], v[76:83], v[18:25], v[172:175], v154, v154 op_sel_hi:[0,0,0]
	v_mfma_scale_f32_16x16x128_f8f6f4 v[240:243], v[68:75], v[26:33], v[176:179], v154, v154 op_sel_hi:[0,0,0]
	v_mfma_scale_f32_16x16x128_f8f6f4 v[244:247], v[76:83], v[26:33], v[180:183], v154, v154 op_sel_hi:[0,0,0]
	v_mfma_scale_f32_16x16x128_f8f6f4 v[248:251], v[68:75], v[36:43], v[184:187], v154, v154 op_sel_hi:[0,0,0]
	v_mfma_scale_f32_16x16x128_f8f6f4 v[92:95], v[76:83], v[36:43], v[188:191], v154, v154 op_sel_hi:[0,0,0]
	v_mfma_scale_f32_16x16x128_f8f6f4 v[232:235], v[68:75], v[18:25], v[168:171], v154, v154 op_sel_hi:[0,0,0]
	v_mfma_scale_f32_16x16x128_f8f6f4 v[72:75], v[68:75], v[44:51], v[138:141], v154, v154 op_sel_hi:[0,0,0]
	v_mfma_scale_f32_16x16x128_f8f6f4 v[76:79], v[76:83], v[44:51], v[142:145], v154, v154 op_sel_hi:[0,0,0]
	s_setprio 0
	s_barrier
	s_add_u32 s74, s0, 0x20000
	s_addc_u32 s75, s1, 0
	s_add_u32 s76, s0, 0x30000
	s_addc_u32 s77, s1, 0
	s_mov_b32 m0, s50
	s_nop 0
	v_lshl_add_u64 v[68:69], s[74:75], 0, v[252:253]
	global_load_lds_dwordx4 v[68:69], off
	v_lshl_add_u64 v[68:69], s[76:77], 0, v[252:253]
	s_mov_b32 m0, s51
	s_nop 0
	global_load_lds_dwordx4 v[68:69], off
	s_waitcnt vmcnt(6)
	s_barrier
	s_setprio 1
	v_mfma_scale_f32_16x16x128_f8f6f4 v[80:83], v[2:9], v[18:25], v[160:163], v154, v154 op_sel_hi:[0,0,0]
	v_mfma_scale_f32_16x16x128_f8f6f4 v[96:99], v[10:17], v[36:43], v[116:119], v154, v154 op_sel_hi:[0,0,0]
	v_mfma_scale_f32_16x16x128_f8f6f4 v[68:71], v[10:17], v[18:25], v[164:167], v154, v154 op_sel_hi:[0,0,0]
	v_mfma_scale_f32_16x16x128_f8f6f4 v[192:195], v[2:9], v[26:33], v[192:195], v154, v154 op_sel_hi:[0,0,0]
	v_mfma_scale_f32_16x16x128_f8f6f4 v[196:199], v[10:17], v[26:33], v[196:199], v154, v154 op_sel_hi:[0,0,0]
	v_mfma_scale_f32_16x16x128_f8f6f4 v[200:203], v[2:9], v[36:43], v[200:203], v154, v154 op_sel_hi:[0,0,0]
	v_mfma_scale_f32_16x16x128_f8f6f4 v[100:103], v[2:9], v[44:51], v[120:123], v154, v154 op_sel_hi:[0,0,0]
	v_mfma_scale_f32_16x16x128_f8f6f4 v[104:107], v[10:17], v[44:51], v[124:127], v154, v154 op_sel_hi:[0,0,0]
	s_setprio 0
	s_barrier
	ds_read2st64_b32 v[108:109], v34 offset0:2 offset1:3
	ds_read_b128 v[2:5], v135
	ds_read_b128 v[6:9], v135 offset:1024
	ds_read_b128 v[10:13], v135 offset:2048
	ds_read_b128 v[14:17], v135 offset:3072
	ds_read_b128 v[18:21], v158 offset:32768
	ds_read_b128 v[22:25], v158 offset:33792
	ds_read_b128 v[26:29], v158 offset:34816
	ds_read_b128 v[30:33], v158 offset:35840
	ds_read_b128 v[36:39], v158 offset:36864
	ds_read_b128 v[40:43], v158 offset:37888
	ds_read_b128 v[44:47], v158 offset:38912
	ds_read_b128 v[48:51], v158 offset:39936
	s_mov_b32 m0, s52
	s_waitcnt lgkmcnt(12)
	v_lshl_or_b32 v255, v109, 16, v108
	v_lshl_add_u32 v108, v108, 10, v155
	global_load_lds_dwordx4 v108, s[8:9]
	v_lshl_add_u32 v108, v109, 10, v155
	s_mov_b32 m0, s53
	s_nop 0
	global_load_lds_dwordx4 v108, s[8:9]
	s_waitcnt lgkmcnt(8)
	s_barrier
; __device__ __forceinline__ int tid_hidden() { int t = threadIdx.x; asm volatile("" : "+v"(t)); return t; }
; #define lds lds_hidden(lds0)
; template <class Epi, class Src>
; __device__ __forceinline__ void gemm_phase(LAS unsigned char* lds, const Src S, const Epi E) {
;     ...
;         { const int tp = tid_hidden(); E.prefetch(cur, lds, par, tp, __builtin_amdgcn_readfirstlane(tp >> 6)); }
;         if (Src::GATHER && has_next) { const int tp = tid_hidden(); tab_fill(S, nxt, tp, __builtin_amdgcn_readfirstlane(tp >> 6), lds, par ^ 1); }
;         for (int t = 0; t < NKTR - 2; t += 2) {
;             const size_t k1 = (size_t)(t + 1) * kstep, k2 = (size_t)(t + 2) * kstep;
;             const char* b2 = cB + k2; const char* b3 = b2 + kstep;
;             G8_ITER(cA, par, k1, cA, par, k2, b2, b3);
;         }
;         {
;             const int par2 = has_next ? (par ^ 1) : par;
;             const char* b3 = nB + kstep;
;             G8_ITER(cA, par, (size_t)(NKTR - 1) * kstep, nA, par2, (size_t)0, nB, b3);
;         }
	s_waitcnt lgkmcnt(0)
	s_setprio 1
	s_waitcnt lgkmcnt(0)
	v_mfma_scale_f32_16x16x128_f8f6f4 v[128:131], v[2:9], v[18:25], v[128:131], v154, v154 op_sel_hi:[0,0,0]
	v_mfma_scale_f32_16x16x128_f8f6f4 v[124:127], v[10:17], v[18:25], v[204:207], v154, v154 op_sel_hi:[0,0,0]
	v_mfma_scale_f32_16x16x128_f8f6f4 v[120:123], v[2:9], v[26:33], v[208:211], v154, v154 op_sel_hi:[0,0,0]
	v_mfma_scale_f32_16x16x128_f8f6f4 v[116:119], v[10:17], v[26:33], v[212:215], v154, v154 op_sel_hi:[0,0,0]
	v_mfma_scale_f32_16x16x128_f8f6f4 v[112:115], v[2:9], v[36:43], v[146:149], v154, v154 op_sel_hi:[0,0,0]
	v_mfma_scale_f32_16x16x128_f8f6f4 v[108:111], v[10:17], v[36:43], v[150:153], v154, v154 op_sel_hi:[0,0,0]
	v_mfma_scale_f32_16x16x128_f8f6f4 v[204:207], v[2:9], v[44:51], v[216:219], v154, v154 op_sel_hi:[0,0,0]
	v_mfma_scale_f32_16x16x128_f8f6f4 v[208:211], v[10:17], v[44:51], v[220:223], v154, v154 op_sel_hi:[0,0,0]
	s_setprio 0
	s_barrier
	s_add_u32 s74, s0, 0x80
	s_addc_u32 s75, s1, 0
	s_add_u32 s76, s0, 0x10080
	s_addc_u32 s77, s1, 0
	s_mov_b32 m0, s59
	ds_read_b128 v[138:141], v136
	ds_read_b128 v[142:145], v136 offset:1024
	ds_read_b128 v[160:163], v136 offset:2048
	ds_read_b128 v[164:167], v136 offset:3072
	s_nop 0
	v_lshl_add_u64 v[132:133], s[74:75], 0, v[252:253]
	global_load_lds_dwordx4 v[132:133], off
	v_lshl_add_u64 v[132:133], s[76:77], 0, v[252:253]
	s_mov_b32 m0, s60
	s_nop 0
	global_load_lds_dwordx4 v[132:133], off
	s_barrier
	s_waitcnt lgkmcnt(0)
	s_setprio 1
	s_waitcnt lgkmcnt(0)
	v_mfma_scale_f32_16x16x128_f8f6f4 v[84:87], v[160:167], v[18:25], v[84:87], v154, v154 op_sel_hi:[0,0,0]
	v_mfma_scale_f32_16x16x128_f8f6f4 v[88:91], v[138:145], v[26:33], v[88:91], v154, v154 op_sel_hi:[0,0,0]
	v_mfma_scale_f32_16x16x128_f8f6f4 v[26:29], v[160:167], v[26:33], v[228:231], v154, v154 op_sel_hi:[0,0,0]
	v_mfma_scale_f32_16x16x128_f8f6f4 v[52:55], v[138:145], v[36:43], v[52:55], v154, v154 op_sel_hi:[0,0,0]
	v_mfma_scale_f32_16x16x128_f8f6f4 v[36:39], v[160:167], v[36:43], v[56:59], v154, v154 op_sel_hi:[0,0,0]
	v_mfma_scale_f32_16x16x128_f8f6f4 v[30:33], v[138:145], v[44:51], v[60:63], v154, v154 op_sel_hi:[0,0,0]
	v_mfma_scale_f32_16x16x128_f8f6f4 v[40:43], v[160:167], v[44:51], v[64:67], v154, v154 op_sel_hi:[0,0,0]
	v_mfma_scale_f32_16x16x128_f8f6f4 v[132:135], v[138:145], v[18:25], v[224:227], v154, v154 op_sel_hi:[0,0,0]
	s_setprio 0
	s_barrier
	ds_read_b128 v[18:21], v158 offset:49152
	ds_read_b128 v[22:25], v158 offset:50176
	ds_read_b128 v[168:171], v158 offset:51200
	ds_read_b128 v[172:175], v158 offset:52224
	ds_read_b128 v[176:179], v158 offset:53248
	ds_read_b128 v[180:183], v158 offset:54272
	ds_read_b128 v[184:187], v158 offset:55296
	ds_read_b128 v[188:191], v158 offset:56320
	s_add_u32 s94, s8, 0x80
	s_addc_u32 s95, s9, 0
	v_and_b32_e32 v34, 0xffff, v159
	v_lshl_add_u32 v34, v34, 10, v155
	s_mov_b32 m0, s61
	s_nop 0
	global_load_lds_dwordx4 v34, s[94:95]
	v_lshrrev_b32_e32 v34, 16, v159
	v_lshl_add_u32 v34, v34, 10, v155
	s_mov_b32 m0, s62
	s_nop 0
	global_load_lds_dwordx4 v34, s[94:95]
	s_barrier
	s_waitcnt lgkmcnt(0)
	s_setprio 1
	s_waitcnt lgkmcnt(0)
	v_mfma_scale_f32_16x16x128_f8f6f4 v[64:67], v[2:9], v[18:25], v[232:235], v154, v154 op_sel_hi:[0,0,0]
	v_mfma_scale_f32_16x16x128_f8f6f4 v[60:63], v[10:17], v[18:25], v[236:239], v154, v154 op_sel_hi:[0,0,0]
	v_mfma_scale_f32_16x16x128_f8f6f4 v[56:59], v[2:9], v[168:175], v[240:243], v154, v154 op_sel_hi:[0,0,0]
	v_mfma_scale_f32_16x16x128_f8f6f4 v[236:239], v[10:17], v[168:175], v[244:247], v154, v154 op_sel_hi:[0,0,0]
	v_mfma_scale_f32_16x16x128_f8f6f4 v[48:51], v[2:9], v[176:183], v[248:251], v154, v154 op_sel_hi:[0,0,0]
	v_mfma_scale_f32_16x16x128_f8f6f4 v[44:47], v[10:17], v[176:183], v[92:95], v154, v154 op_sel_hi:[0,0,0]
	v_mfma_scale_f32_16x16x128_f8f6f4 v[6:9], v[2:9], v[184:191], v[72:75], v154, v154 op_sel_hi:[0,0,0]
	v_mfma_scale_f32_16x16x128_f8f6f4 v[244:247], v[10:17], v[184:191], v[76:79], v154, v154 op_sel_hi:[0,0,0]
	s_setprio 0
	s_barrier
	s_add_u32 s74, s0, 0x20080
	s_addc_u32 s75, s1, 0
	s_add_u32 s0, s0, 0x30080
	s_addc_u32 s1, s1, 0
	s_mov_b32 m0, s64
	s_nop 0
	v_lshl_add_u64 v[2:3], s[74:75], 0, v[252:253]
	global_load_lds_dwordx4 v[2:3], off
	v_lshl_add_u64 v[2:3], s[0:1], 0, v[252:253]
	s_mov_b32 m0, s65
	s_nop 0
	global_load_lds_dwordx4 v[2:3], off
	s_waitcnt vmcnt(6)
	s_barrier
	s_setprio 1
	v_mfma_scale_f32_16x16x128_f8f6f4 v[240:243], v[138:145], v[18:25], v[80:83], v154, v154 op_sel_hi:[0,0,0]
	v_mfma_scale_f32_16x16x128_f8f6f4 v[248:251], v[160:167], v[18:25], v[68:71], v154, v154 op_sel_hi:[0,0,0]
	v_mfma_scale_f32_16x16x128_f8f6f4 v[22:25], v[138:145], v[168:175], v[192:195], v154, v154 op_sel_hi:[0,0,0]
	v_mfma_scale_f32_16x16x128_f8f6f4 v[18:21], v[160:167], v[168:175], v[196:199], v154, v154 op_sel_hi:[0,0,0]
	v_mfma_scale_f32_16x16x128_f8f6f4 v[14:17], v[138:145], v[176:183], v[200:203], v154, v154 op_sel_hi:[0,0,0]
	v_mfma_scale_f32_16x16x128_f8f6f4 v[10:13], v[160:167], v[176:183], v[96:99], v154, v154 op_sel_hi:[0,0,0]
	v_mfma_scale_f32_16x16x128_f8f6f4 v[92:95], v[138:145], v[184:191], v[100:103], v154, v154 op_sel_hi:[0,0,0]
	s_nop 5
	v_mov_b64_e32 v[96:97], v[132:133]
	v_mov_b64_e32 v[98:99], v[134:135]
	v_mfma_scale_f32_16x16x128_f8f6f4 v[2:5], v[160:167], v[184:191], v[104:107], v154, v154 op_sel_hi:[0,0,0]
	s_setprio 0
	v_mov_b32_e32 v34, v0
	s_barrier
; #define LAS __attribute__((address_space(3)))
; #define lds lds_hidden(lds0)
;     __device__ __forceinline__ void operator()(const f32x4 (&acc)[2][2][4][2], const Unit& u, int wr, int wc, int fr, int fq, LAS unsigned char* lds, int par) const {
;         LAS const float* tb = (LAS const float*)(lds + EPI_OFF + par * 2048);
;         const int colu = wc * 32 + 8 * fq, col = u.pn * 128 + colu;
;         const f32x4 bg0 = *(LAS const f32x4*)(tb + colu), bg1 = *(LAS const f32x4*)(tb + colu + 4), bl0 = *(LAS const f32x4*)(tb + 128 + colu), bl1 = *(LAS const f32x4*)(tb + 128 + colu + 4);
;         const float sc = kf(1.f / (W8_SCALE * H28_SCALE * MX_SCALE)), lim = kf(7.f), ke = kf(-1.702f * 1.4426950408889634f), one = kf(1.f), as = kf(ACT8_SCALE);
;         const f32x2_t sc2 = (f32x2_t){sc, sc}, ke2 = (f32x2_t){ke, ke}, one2 = (f32x2_t){one, one}, as2 = (f32x2_t){as, as};
; #pragma unroll
;         for (int ai = 0; ai < 2; ++ai)
; #pragma unroll
;             for (int m = 0; m < 4; ++m) {
;                 const int r = u.rt * BM + ai * HALF + wr * 64 + m * 16 + fr;
;                 f32x2_t o[4];
; #pragma unroll
;                 for (int n = 0; n < 2; ++n)
; #pragma unroll
;                     for (int h = 0; h < 2; ++h) {
;                         const f32x4 bgv = n ? bg1 : bg0, blv = n ? bl1 : bl0;
;                         f32x2_t glu = (f32x2_t){acc[ai][0][m][n][2 * h], acc[ai][0][m][n][2 * h + 1]} * sc2 + (f32x2_t){bgv[2 * h], bgv[2 * h + 1]};
;                         f32x2_t lin = (f32x2_t){acc[ai][1][m][n][2 * h], acc[ai][1][m][n][2 * h + 1]} * sc2 + (f32x2_t){blv[2 * h], blv[2 * h + 1]};
;                         glu.x = fminf(glu.x, lim); glu.y = fminf(glu.y, lim);
;                         lin.x = __builtin_amdgcn_fmed3f(lin.x, -lim, lim); lin.y = __builtin_amdgcn_fmed3f(lin.y, -lim, lim);
;                         const f32x2_t t = glu * ke2;
;                         const f32x2_t d = (f32x2_t){__builtin_amdgcn_exp2f(t.x), __builtin_amdgcn_exp2f(t.y)} + one2;
;                         const f32x2_t rc = (f32x2_t){__builtin_amdgcn_rcpf(d.x), __builtin_amdgcn_rcpf(d.y)};
;                         o[n * 2 + h] = (glu * rc) * (lin * as2 + as2);
;                     }
;                 const int ro = u.rowbase + r;
;                 u32x2 w; w.x = cvt_pk4_fp8(o[0].x, o[0].y, o[1].x, o[1].y); w.y = cvt_pk4_fp8(o[2].x, o[2].y, o[3].x, o[3].y);
	s_lshl_b32 s0, s68, 11
	v_readfirstlane_b32 s17, v34
	s_lshr_b32 s1, s17, 1
	s_and_b32 s1, s1, 0x60
	v_lshrrev_b32_e32 v68, 1, v34
	s_add_i32 s0, s67, s0
	v_and_or_b32 v69, v68, 24, s1
	v_lshl_or_b32 v68, s18, 7, v69
	v_lshl_add_u32 v69, v69, 2, s0
	ds_read_b128 v[140:143], v69
	ds_read_b128 v[132:135], v69 offset:16
	ds_read_b128 v[144:147], v69 offset:512
	ds_read_b128 v[136:139], v69 offset:528
	s_ashr_i32 s17, s17, 2
	s_mov_b32 s34, 0x3b000000
	s_mov_b32 s1, 0x40e00000
	s_andn2_b32 s17, s17, 63
	v_ashrrev_i32_e32 v69, 31, v68
	v_and_or_b32 v80, v34, 15, s17
	v_lshl_add_u64 v[150:151], s[14:15], 0, v[68:69]
	s_waitcnt lgkmcnt(0)
	v_pk_fma_f32 v[68:69], v[128:129], s[34:35], v[140:141] op_sel_hi:[1,0,1]
	v_max_f32_e64 v34, s1, s1
	s_mov_b32 s30, 0xc01d265f
	v_min_f32_e32 v68, v68, v34
	v_min_f32_e32 v69, v69, v34
	s_mov_b32 s2, 1.0
	v_pk_mul_f32 v[72:73], s[30:31], v[68:69] op_sel_hi:[0,1]
	v_exp_f32_e32 v72, v72
	v_exp_f32_e32 v73, v73
	v_pk_fma_f32 v[70:71], v[96:97], s[34:35], v[144:145] op_sel_hi:[1,0,1]
	s_mov_b32 s0, 4.0
	v_pk_add_f32 v[72:73], s[2:3], v[72:73] op_sel_hi:[0,1]
	v_rcp_f32_e32 v72, v72
	v_rcp_f32_e32 v73, v73
	v_med3_f32 v70, v70, -s1, s1
	v_med3_f32 v71, v71, -s1, s1
	v_pk_mul_f32 v[68:69], v[68:69], v[72:73]
	v_pk_fma_f32 v[70:71], s[0:1], v[70:71], s[0:1] op_sel_hi:[0,1,0]
	v_pk_mul_f32 v[68:69], v[70:71], v[68:69]
	v_pk_fma_f32 v[70:71], v[130:131], s[34:35], v[142:143] op_sel_hi:[1,0,1]
	v_pk_fma_f32 v[72:73], v[98:99], s[34:35], v[146:147] op_sel_hi:[1,0,1]
	v_min_f32_e32 v70, v70, v34
	v_min_f32_e32 v71, v71, v34
	v_pk_mul_f32 v[74:75], s[30:31], v[70:71] op_sel_hi:[0,1]
	v_exp_f32_e32 v74, v74
	v_exp_f32_e32 v75, v75
	v_med3_f32 v72, v72, -s1, s1
	v_med3_f32 v73, v73, -s1, s1
	v_pk_fma_f32 v[72:73], s[0:1], v[72:73], s[0:1] op_sel_hi:[0,1,0]
	v_pk_add_f32 v[74:75], s[2:3], v[74:75] op_sel_hi:[0,1]
	v_rcp_f32_e32 v74, v74
	v_rcp_f32_e32 v75, v75
	s_lshl_b32 s17, s38, 8
	s_add_i32 s17, s17, s39
	v_add_u32_e32 v152, s17, v80
	v_pk_mul_f32 v[70:71], v[70:71], v[74:75]
	v_pk_fma_f32 v[74:75], v[84:85], s[34:35], v[136:137] op_sel_hi:[1,0,1]
	v_pk_mul_f32 v[70:71], v[72:73], v[70:71]
	v_pk_fma_f32 v[72:73], v[124:125], s[34:35], v[132:133] op_sel_hi:[1,0,1]
	v_med3_f32 v74, v74, -s1, s1
	v_min_f32_e32 v72, v72, v34
	v_min_f32_e32 v73, v73, v34
	v_pk_mul_f32 v[76:77], s[30:31], v[72:73] op_sel_hi:[0,1]
	v_exp_f32_e32 v76, v76
	v_exp_f32_e32 v77, v77
	v_med3_f32 v75, v75, -s1, s1
	v_pk_fma_f32 v[74:75], s[0:1], v[74:75], s[0:1] op_sel_hi:[0,1,0]
	v_ashrrev_i32_e32 v153, 31, v152
	v_pk_add_f32 v[76:77], s[2:3], v[76:77] op_sel_hi:[0,1]
	v_rcp_f32_e32 v76, v76
	v_rcp_f32_e32 v77, v77
	v_mov_b64_e32 v[80:81], v[208:209]
	v_mov_b64_e32 v[82:83], v[210:211]
	s_and_b64 vcc, exec, s[4:5]
	v_pk_mul_f32 v[72:73], v[72:73], v[76:77]
	v_pk_fma_f32 v[76:77], v[86:87], s[34:35], v[138:139] op_sel_hi:[1,0,1]
	v_pk_mul_f32 v[72:73], v[74:75], v[72:73]
	v_pk_fma_f32 v[74:75], v[126:127], s[34:35], v[134:135] op_sel_hi:[1,0,1]
	v_med3_f32 v76, v76, -s1, s1
	v_min_f32_e32 v74, v74, v34
	v_min_f32_e32 v75, v75, v34
	v_pk_mul_f32 v[78:79], s[30:31], v[74:75] op_sel_hi:[0,1]
	v_exp_f32_e32 v78, v78
	v_exp_f32_e32 v79, v79
	v_med3_f32 v77, v77, -s1, s1
	v_pk_fma_f32 v[76:77], s[0:1], v[76:77], s[0:1] op_sel_hi:[0,1,0]
	v_pk_add_f32 v[78:79], s[2:3], v[78:79] op_sel_hi:[0,1]
	v_rcp_f32_e32 v78, v78
	v_rcp_f32_e32 v79, v79
	s_nop 0
	v_pk_mul_f32 v[74:75], v[74:75], v[78:79]
	s_nop 0
	v_pk_mul_f32 v[74:75], v[76:77], v[74:75]
	v_mov_b32_e32 v76, v35
	v_mov_b32_e32 v77, v35
	v_cvt_pk_fp8_f32 v76, v68, v69
	v_cvt_pk_fp8_f32 v77, v72, v73
	v_lshlrev_b64 v[68:69], 10, v[152:153]
	v_lshl_add_u64 v[68:69], v[150:151], 0, v[68:69]
	v_cvt_pk_fp8_f32 v76, v70, v71 op_sel:[0,0,1]
	v_cvt_pk_fp8_f32 v77, v74, v75 op_sel:[0,0,1]
	v_pk_fma_f32 v[70:71], v[88:89], s[34:35], v[144:145] op_sel_hi:[1,0,1]
	global_store_dwordx2 v[68:69], v[76:77], off sc1
	v_pk_fma_f32 v[68:69], v[120:121], s[34:35], v[140:141] op_sel_hi:[1,0,1]
	v_med3_f32 v70, v70, -s1, s1
	v_min_f32_e32 v68, v68, v34
	v_min_f32_e32 v69, v69, v34
	v_pk_mul_f32 v[72:73], s[30:31], v[68:69] op_sel_hi:[0,1]
	v_exp_f32_e32 v72, v72
	v_exp_f32_e32 v73, v73
	v_med3_f32 v71, v71, -s1, s1
	v_pk_fma_f32 v[70:71], s[0:1], v[70:71], s[0:1] op_sel_hi:[0,1,0]
	v_pk_add_f32 v[72:73], s[2:3], v[72:73] op_sel_hi:[0,1]
	v_rcp_f32_e32 v72, v72
	v_rcp_f32_e32 v73, v73
	s_nop 0
	v_pk_mul_f32 v[68:69], v[68:69], v[72:73]
	s_nop 0
	v_pk_mul_f32 v[68:69], v[70:71], v[68:69]
	v_pk_fma_f32 v[70:71], v[122:123], s[34:35], v[142:143] op_sel_hi:[1,0,1]
	v_pk_fma_f32 v[72:73], v[90:91], s[34:35], v[146:147] op_sel_hi:[1,0,1]
	v_min_f32_e32 v70, v70, v34
	v_min_f32_e32 v71, v71, v34
	v_pk_mul_f32 v[74:75], s[30:31], v[70:71] op_sel_hi:[0,1]
	v_exp_f32_e32 v74, v74
	v_exp_f32_e32 v75, v75
	v_med3_f32 v72, v72, -s1, s1
	v_med3_f32 v73, v73, -s1, s1
	v_pk_fma_f32 v[72:73], s[0:1], v[72:73], s[0:1] op_sel_hi:[0,1,0]
	v_pk_add_f32 v[74:75], s[2:3], v[74:75] op_sel_hi:[0,1]
	v_rcp_f32_e32 v74, v74
	v_rcp_f32_e32 v75, v75
	s_nop 0
	v_pk_mul_f32 v[70:71], v[70:71], v[74:75]
	s_nop 0
	v_pk_mul_f32 v[70:71], v[72:73], v[70:71]
	v_pk_fma_f32 v[72:73], v[116:117], s[34:35], v[132:133] op_sel_hi:[1,0,1]
	v_pk_fma_f32 v[74:75], v[26:27], s[34:35], v[136:137] op_sel_hi:[1,0,1]
	v_min_f32_e32 v72, v72, v34
	v_min_f32_e32 v73, v73, v34
	v_pk_mul_f32 v[76:77], s[30:31], v[72:73] op_sel_hi:[0,1]
	v_exp_f32_e32 v76, v76
	v_exp_f32_e32 v77, v77
	v_med3_f32 v74, v74, -s1, s1
	v_med3_f32 v75, v75, -s1, s1
	v_pk_fma_f32 v[74:75], s[0:1], v[74:75], s[0:1] op_sel_hi:[0,1,0]
	v_pk_add_f32 v[76:77], s[2:3], v[76:77] op_sel_hi:[0,1]
; __device__ __forceinline__ unsigned cvt_pk4_fp8(float a, float b, float c, float d) { int w = 0; w = __builtin_amdgcn_cvt_pk_fp8_f32(a, b, w, false); w = __builtin_amdgcn_cvt_pk_fp8_f32(c, d, w, true); return (unsigned)w; }
; #define GAS __attribute__((address_space(1)))
;     __device__ __forceinline__ void operator()(const f32x4 (&acc)[2][2][4][2], const Unit& u, int wr, int wc, int fr, int fq, LAS unsigned char* lds, int par) const {
;     ...
;         for (int ai = 0; ai < 2; ++ai)
; #pragma unroll
;             for (int m = 0; m < 4; ++m) {
;                 const int r = u.rt * BM + ai * HALF + wr * 64 + m * 16 + fr;
;                 f32x2_t o[4];
; #pragma unroll
;                 for (int n = 0; n < 2; ++n)
; #pragma unroll
;                     for (int h = 0; h < 2; ++h) {
;                         const f32x4 bgv = n ? bg1 : bg0, blv = n ? bl1 : bl0;
;                         f32x2_t glu = (f32x2_t){acc[ai][0][m][n][2 * h], acc[ai][0][m][n][2 * h + 1]} * sc2 + (f32x2_t){bgv[2 * h], bgv[2 * h + 1]};
;                         f32x2_t lin = (f32x2_t){acc[ai][1][m][n][2 * h], acc[ai][1][m][n][2 * h + 1]} * sc2 + (f32x2_t){blv[2 * h], blv[2 * h + 1]};
;                         glu.x = fminf(glu.x, lim); glu.y = fminf(glu.y, lim);
;                         lin.x = __builtin_amdgcn_fmed3f(lin.x, -lim, lim); lin.y = __builtin_amdgcn_fmed3f(lin.y, -lim, lim);
;                         const f32x2_t t = glu * ke2;
;                         const f32x2_t d = (f32x2_t){__builtin_amdgcn_exp2f(t.x), __builtin_amdgcn_exp2f(t.y)} + one2;
;                         const f32x2_t rc = (f32x2_t){__builtin_amdgcn_rcpf(d.x), __builtin_amdgcn_rcpf(d.y)};
;                         o[n * 2 + h] = (glu * rc) * (lin * as2 + as2);
;                     }
;                 const int ro = u.rowbase + r;
;                 u32x2 w; w.x = cvt_pk4_fp8(o[0].x, o[0].y, o[1].x, o[1].y); w.y = cvt_pk4_fp8(o[2].x, o[2].y, o[3].x, o[3].y);
;                 __hip_atomic_store((unsigned long long GAS*)(act + (size_t)ro * DFF + col), ((unsigned long long)w.y << 32) | w.x, __ATOMIC_RELAXED, __HIP_MEMORY_SCOPE_AGENT);
;             }
	v_rcp_f32_e32 v76, v76
	v_rcp_f32_e32 v77, v77
	s_nop 0
	v_pk_mul_f32 v[72:73], v[72:73], v[76:77]
	s_nop 0
	v_pk_mul_f32 v[72:73], v[74:75], v[72:73]
	v_pk_fma_f32 v[74:75], v[118:119], s[34:35], v[134:135] op_sel_hi:[1,0,1]
	v_pk_fma_f32 v[76:77], v[28:29], s[34:35], v[138:139] op_sel_hi:[1,0,1]
	v_min_f32_e32 v74, v74, v34
	v_min_f32_e32 v75, v75, v34
	v_pk_mul_f32 v[78:79], s[30:31], v[74:75] op_sel_hi:[0,1]
	v_exp_f32_e32 v78, v78
	v_exp_f32_e32 v79, v79
	v_med3_f32 v76, v76, -s1, s1
	v_med3_f32 v77, v77, -s1, s1
	v_pk_fma_f32 v[76:77], s[0:1], v[76:77], s[0:1] op_sel_hi:[0,1,0]
	v_pk_add_f32 v[78:79], s[2:3], v[78:79] op_sel_hi:[0,1]
	v_rcp_f32_e32 v78, v78
	v_rcp_f32_e32 v79, v79
	s_nop 0
	v_pk_mul_f32 v[74:75], v[74:75], v[78:79]
	v_mov_b32_e32 v78, v35
	v_mov_b32_e32 v79, v35
	v_cvt_pk_fp8_f32 v78, v68, v69
	v_cvt_pk_fp8_f32 v79, v72, v73
	v_pk_mul_f32 v[74:75], v[76:77], v[74:75]
	v_add_u32_e32 v76, 16, v152
	v_cvt_pk_fp8_f32 v78, v70, v71 op_sel:[0,0,1]
	v_cvt_pk_fp8_f32 v79, v74, v75 op_sel:[0,0,1]
	v_ashrrev_i32_e32 v77, 31, v76
	v_lshlrev_b64 v[68:69], 10, v[76:77]
	v_lshl_add_u64 v[68:69], v[150:151], 0, v[68:69]
	global_store_dwordx2 v[68:69], v[78:79], off sc1
	v_pk_fma_f32 v[68:69], v[112:113], s[34:35], v[140:141] op_sel_hi:[1,0,1]
	v_pk_fma_f32 v[70:71], v[52:53], s[34:35], v[144:145] op_sel_hi:[1,0,1]
	v_min_f32_e32 v68, v68, v34
	v_min_f32_e32 v69, v69, v34
	v_pk_mul_f32 v[72:73], s[30:31], v[68:69] op_sel_hi:[0,1]
	v_exp_f32_e32 v72, v72
	v_exp_f32_e32 v73, v73
	v_med3_f32 v70, v70, -s1, s1
	v_med3_f32 v71, v71, -s1, s1
	v_pk_fma_f32 v[70:71], s[0:1], v[70:71], s[0:1] op_sel_hi:[0,1,0]
	v_pk_add_f32 v[72:73], s[2:3], v[72:73] op_sel_hi:[0,1]
	v_rcp_f32_e32 v72, v72
	v_rcp_f32_e32 v73, v73
	s_nop 0
	v_pk_mul_f32 v[68:69], v[68:69], v[72:73]
	s_nop 0
	v_pk_mul_f32 v[68:69], v[70:71], v[68:69]
	v_pk_fma_f32 v[70:71], v[114:115], s[34:35], v[142:143] op_sel_hi:[1,0,1]
	v_pk_fma_f32 v[72:73], v[54:55], s[34:35], v[146:147] op_sel_hi:[1,0,1]
	v_min_f32_e32 v70, v70, v34
	v_min_f32_e32 v71, v71, v34
	v_pk_mul_f32 v[74:75], s[30:31], v[70:71] op_sel_hi:[0,1]
	v_exp_f32_e32 v74, v74
	v_exp_f32_e32 v75, v75
	v_med3_f32 v72, v72, -s1, s1
	v_med3_f32 v73, v73, -s1, s1
	v_pk_fma_f32 v[72:73], s[0:1], v[72:73], s[0:1] op_sel_hi:[0,1,0]
	v_pk_add_f32 v[74:75], s[2:3], v[74:75] op_sel_hi:[0,1]
	v_rcp_f32_e32 v74, v74
	v_rcp_f32_e32 v75, v75
	s_nop 0
	v_pk_mul_f32 v[70:71], v[70:71], v[74:75]
	s_nop 0
	v_pk_mul_f32 v[70:71], v[72:73], v[70:71]
	v_pk_fma_f32 v[72:73], v[108:109], s[34:35], v[132:133] op_sel_hi:[1,0,1]
	v_pk_fma_f32 v[74:75], v[36:37], s[34:35], v[136:137] op_sel_hi:[1,0,1]
	v_min_f32_e32 v72, v72, v34
	v_min_f32_e32 v73, v73, v34
	v_pk_mul_f32 v[76:77], s[30:31], v[72:73] op_sel_hi:[0,1]
	v_exp_f32_e32 v76, v76
	v_exp_f32_e32 v77, v77
	v_med3_f32 v74, v74, -s1, s1
	v_med3_f32 v75, v75, -s1, s1
	v_pk_fma_f32 v[74:75], s[0:1], v[74:75], s[0:1] op_sel_hi:[0,1,0]
	v_pk_add_f32 v[76:77], s[2:3], v[76:77] op_sel_hi:[0,1]
	v_rcp_f32_e32 v76, v76
	v_rcp_f32_e32 v77, v77
	s_nop 0
	v_pk_mul_f32 v[72:73], v[72:73], v[76:77]
	s_nop 0
	v_pk_mul_f32 v[72:73], v[74:75], v[72:73]
	v_pk_fma_f32 v[74:75], v[110:111], s[34:35], v[134:135] op_sel_hi:[1,0,1]
	v_pk_fma_f32 v[76:77], v[38:39], s[34:35], v[138:139] op_sel_hi:[1,0,1]
	v_min_f32_e32 v74, v74, v34
	v_min_f32_e32 v75, v75, v34
	v_pk_mul_f32 v[78:79], s[30:31], v[74:75] op_sel_hi:[0,1]
	v_exp_f32_e32 v78, v78
	v_exp_f32_e32 v79, v79
	v_med3_f32 v76, v76, -s1, s1
	v_med3_f32 v77, v77, -s1, s1
	v_pk_fma_f32 v[76:77], s[0:1], v[76:77], s[0:1] op_sel_hi:[0,1,0]
	v_pk_add_f32 v[78:79], s[2:3], v[78:79] op_sel_hi:[0,1]
	v_rcp_f32_e32 v78, v78
	v_rcp_f32_e32 v79, v79
	s_nop 0
	v_pk_mul_f32 v[74:75], v[74:75], v[78:79]
	v_mov_b32_e32 v78, v35
	v_mov_b32_e32 v79, v35
	v_cvt_pk_fp8_f32 v78, v68, v69
	v_cvt_pk_fp8_f32 v79, v72, v73
	v_pk_mul_f32 v[74:75], v[76:77], v[74:75]
	v_add_u32_e32 v76, 32, v152
	v_cvt_pk_fp8_f32 v78, v70, v71 op_sel:[0,0,1]
	v_cvt_pk_fp8_f32 v79, v74, v75 op_sel:[0,0,1]
	v_ashrrev_i32_e32 v77, 31, v76
	v_lshlrev_b64 v[68:69], 10, v[76:77]
	v_lshl_add_u64 v[68:69], v[150:151], 0, v[68:69]
	global_store_dwordx2 v[68:69], v[78:79], off sc1
	v_pk_fma_f32 v[68:69], v[204:205], s[34:35], v[140:141] op_sel_hi:[1,0,1]
	v_pk_fma_f32 v[70:71], v[30:31], s[34:35], v[144:145] op_sel_hi:[1,0,1]
	v_min_f32_e32 v68, v68, v34
	v_min_f32_e32 v69, v69, v34
	v_pk_mul_f32 v[72:73], s[30:31], v[68:69] op_sel_hi:[0,1]
	v_exp_f32_e32 v72, v72
	v_exp_f32_e32 v73, v73
	v_med3_f32 v70, v70, -s1, s1
	v_med3_f32 v71, v71, -s1, s1
	v_pk_fma_f32 v[70:71], s[0:1], v[70:71], s[0:1] op_sel_hi:[0,1,0]
	v_pk_add_f32 v[72:73], s[2:3], v[72:73] op_sel_hi:[0,1]
	v_rcp_f32_e32 v72, v72
	v_rcp_f32_e32 v73, v73
	s_nop 0
	v_pk_mul_f32 v[68:69], v[68:69], v[72:73]
	s_nop 0
	v_pk_mul_f32 v[68:69], v[70:71], v[68:69]
	v_pk_fma_f32 v[70:71], v[206:207], s[34:35], v[142:143] op_sel_hi:[1,0,1]
	v_pk_fma_f32 v[72:73], v[32:33], s[34:35], v[146:147] op_sel_hi:[1,0,1]
	v_min_f32_e32 v70, v70, v34
	v_min_f32_e32 v71, v71, v34
	v_pk_mul_f32 v[74:75], s[30:31], v[70:71] op_sel_hi:[0,1]
	v_exp_f32_e32 v74, v74
	v_exp_f32_e32 v75, v75
	v_med3_f32 v72, v72, -s1, s1
	v_med3_f32 v73, v73, -s1, s1
	v_pk_fma_f32 v[72:73], s[0:1], v[72:73], s[0:1] op_sel_hi:[0,1,0]
	v_pk_add_f32 v[74:75], s[2:3], v[74:75] op_sel_hi:[0,1]
	v_rcp_f32_e32 v74, v74
	v_rcp_f32_e32 v75, v75
	s_nop 0
	v_pk_mul_f32 v[70:71], v[70:71], v[74:75]
	s_nop 0
	v_pk_mul_f32 v[70:71], v[72:73], v[70:71]
	v_pk_fma_f32 v[72:73], v[80:81], s[34:35], v[132:133] op_sel_hi:[1,0,1]
	v_pk_fma_f32 v[74:75], v[40:41], s[34:35], v[136:137] op_sel_hi:[1,0,1]
; __device__ __forceinline__ unsigned cvt_pk4_fp8(float a, float b, float c, float d) { int w = 0; w = __builtin_amdgcn_cvt_pk_fp8_f32(a, b, w, false); w = __builtin_amdgcn_cvt_pk_fp8_f32(c, d, w, true); return (unsigned)w; }
; #define GAS __attribute__((address_space(1)))
;     __device__ __forceinline__ void operator()(const f32x4 (&acc)[2][2][4][2], const Unit& u, int wr, int wc, int fr, int fq, LAS unsigned char* lds, int par) const {
;     ...
;         for (int ai = 0; ai < 2; ++ai)
; #pragma unroll
;             for (int m = 0; m < 4; ++m) {
;                 const int r = u.rt * BM + ai * HALF + wr * 64 + m * 16 + fr;
;                 f32x2_t o[4];
; #pragma unroll
;                 for (int n = 0; n < 2; ++n)
; #pragma unroll
;                     for (int h = 0; h < 2; ++h) {
;                         const f32x4 bgv = n ? bg1 : bg0, blv = n ? bl1 : bl0;
;                         f32x2_t glu = (f32x2_t){acc[ai][0][m][n][2 * h], acc[ai][0][m][n][2 * h + 1]} * sc2 + (f32x2_t){bgv[2 * h], bgv[2 * h + 1]};
;                         f32x2_t lin = (f32x2_t){acc[ai][1][m][n][2 * h], acc[ai][1][m][n][2 * h + 1]} * sc2 + (f32x2_t){blv[2 * h], blv[2 * h + 1]};
;                         glu.x = fminf(glu.x, lim); glu.y = fminf(glu.y, lim);
;                         lin.x = __builtin_amdgcn_fmed3f(lin.x, -lim, lim); lin.y = __builtin_amdgcn_fmed3f(lin.y, -lim, lim);
;                         const f32x2_t t = glu * ke2;
;                         const f32x2_t d = (f32x2_t){__builtin_amdgcn_exp2f(t.x), __builtin_amdgcn_exp2f(t.y)} + one2;
;                         const f32x2_t rc = (f32x2_t){__builtin_amdgcn_rcpf(d.x), __builtin_amdgcn_rcpf(d.y)};
;                         o[n * 2 + h] = (glu * rc) * (lin * as2 + as2);
;                     }
;                 const int ro = u.rowbase + r;
;                 u32x2 w; w.x = cvt_pk4_fp8(o[0].x, o[0].y, o[1].x, o[1].y); w.y = cvt_pk4_fp8(o[2].x, o[2].y, o[3].x, o[3].y);
;                 __hip_atomic_store((unsigned long long GAS*)(act + (size_t)ro * DFF + col), ((unsigned long long)w.y << 32) | w.x, __ATOMIC_RELAXED, __HIP_MEMORY_SCOPE_AGENT);
;             }
	v_min_f32_e32 v72, v72, v34
	v_min_f32_e32 v73, v73, v34
	v_pk_mul_f32 v[76:77], s[30:31], v[72:73] op_sel_hi:[0,1]
	v_exp_f32_e32 v76, v76
	v_exp_f32_e32 v77, v77
	v_med3_f32 v74, v74, -s1, s1
	v_med3_f32 v75, v75, -s1, s1
	v_pk_fma_f32 v[74:75], s[0:1], v[74:75], s[0:1] op_sel_hi:[0,1,0]
	v_pk_add_f32 v[76:77], s[2:3], v[76:77] op_sel_hi:[0,1]
	v_rcp_f32_e32 v76, v76
	v_rcp_f32_e32 v77, v77
	s_nop 0
	v_pk_mul_f32 v[72:73], v[72:73], v[76:77]
	s_nop 0
	v_pk_mul_f32 v[72:73], v[74:75], v[72:73]
	v_pk_fma_f32 v[74:75], v[82:83], s[34:35], v[134:135] op_sel_hi:[1,0,1]
	v_pk_fma_f32 v[76:77], v[42:43], s[34:35], v[138:139] op_sel_hi:[1,0,1]
	v_min_f32_e32 v74, v74, v34
	v_min_f32_e32 v75, v75, v34
	v_pk_mul_f32 v[78:79], s[30:31], v[74:75] op_sel_hi:[0,1]
	v_exp_f32_e32 v78, v78
	v_exp_f32_e32 v79, v79
	v_med3_f32 v76, v76, -s1, s1
	v_med3_f32 v77, v77, -s1, s1
	v_pk_fma_f32 v[76:77], s[0:1], v[76:77], s[0:1] op_sel_hi:[0,1,0]
	v_pk_add_f32 v[78:79], s[2:3], v[78:79] op_sel_hi:[0,1]
	v_rcp_f32_e32 v78, v78
	v_rcp_f32_e32 v79, v79
	s_nop 0
	v_pk_mul_f32 v[74:75], v[74:75], v[78:79]
	v_mov_b32_e32 v78, v35
	v_mov_b32_e32 v79, v35
	v_cvt_pk_fp8_f32 v78, v68, v69
	v_cvt_pk_fp8_f32 v79, v72, v73
	v_pk_mul_f32 v[74:75], v[76:77], v[74:75]
	v_add_u32_e32 v76, 48, v152
	v_cvt_pk_fp8_f32 v78, v70, v71 op_sel:[0,0,1]
	v_cvt_pk_fp8_f32 v79, v74, v75 op_sel:[0,0,1]
	v_ashrrev_i32_e32 v77, 31, v76
	v_lshlrev_b64 v[68:69], 10, v[76:77]
	v_lshl_add_u64 v[68:69], v[150:151], 0, v[68:69]
	global_store_dwordx2 v[68:69], v[78:79], off sc1
	v_pk_fma_f32 v[68:69], v[64:65], s[34:35], v[140:141] op_sel_hi:[1,0,1]
	v_pk_fma_f32 v[70:71], v[240:241], s[34:35], v[144:145] op_sel_hi:[1,0,1]
	v_min_f32_e32 v68, v68, v34
	v_min_f32_e32 v69, v69, v34
	v_pk_mul_f32 v[72:73], s[30:31], v[68:69] op_sel_hi:[0,1]
	v_exp_f32_e32 v72, v72
	v_exp_f32_e32 v73, v73
	v_med3_f32 v70, v70, -s1, s1
	v_med3_f32 v71, v71, -s1, s1
	v_pk_fma_f32 v[70:71], s[0:1], v[70:71], s[0:1] op_sel_hi:[0,1,0]
	v_pk_add_f32 v[72:73], s[2:3], v[72:73] op_sel_hi:[0,1]
	v_rcp_f32_e32 v72, v72
	v_rcp_f32_e32 v73, v73
	s_nop 0
	v_pk_mul_f32 v[68:69], v[68:69], v[72:73]
	s_nop 0
	v_pk_mul_f32 v[68:69], v[70:71], v[68:69]
	v_pk_fma_f32 v[70:71], v[66:67], s[34:35], v[142:143] op_sel_hi:[1,0,1]
	v_pk_fma_f32 v[72:73], v[242:243], s[34:35], v[146:147] op_sel_hi:[1,0,1]
	v_min_f32_e32 v70, v70, v34
	v_min_f32_e32 v71, v71, v34
	v_pk_mul_f32 v[74:75], s[30:31], v[70:71] op_sel_hi:[0,1]
	v_exp_f32_e32 v74, v74
	v_exp_f32_e32 v75, v75
	v_med3_f32 v72, v72, -s1, s1
	v_med3_f32 v73, v73, -s1, s1
	v_pk_fma_f32 v[72:73], s[0:1], v[72:73], s[0:1] op_sel_hi:[0,1,0]
	v_pk_add_f32 v[74:75], s[2:3], v[74:75] op_sel_hi:[0,1]
	v_rcp_f32_e32 v74, v74
	v_rcp_f32_e32 v75, v75
	s_nop 0
	v_pk_mul_f32 v[70:71], v[70:71], v[74:75]
	s_nop 0
	v_pk_mul_f32 v[70:71], v[72:73], v[70:71]
	v_pk_fma_f32 v[72:73], v[60:61], s[34:35], v[132:133] op_sel_hi:[1,0,1]
	v_pk_fma_f32 v[74:75], v[248:249], s[34:35], v[136:137] op_sel_hi:[1,0,1]
	v_min_f32_e32 v72, v72, v34
	v_min_f32_e32 v73, v73, v34
	v_pk_mul_f32 v[76:77], s[30:31], v[72:73] op_sel_hi:[0,1]
	v_exp_f32_e32 v76, v76
	v_exp_f32_e32 v77, v77
	v_med3_f32 v74, v74, -s1, s1
	v_med3_f32 v75, v75, -s1, s1
	v_pk_fma_f32 v[74:75], s[0:1], v[74:75], s[0:1] op_sel_hi:[0,1,0]
	v_pk_add_f32 v[76:77], s[2:3], v[76:77] op_sel_hi:[0,1]
	v_rcp_f32_e32 v76, v76
	v_rcp_f32_e32 v77, v77
	s_nop 0
	v_pk_mul_f32 v[72:73], v[72:73], v[76:77]
	s_nop 0
	v_pk_mul_f32 v[72:73], v[74:75], v[72:73]
	v_pk_fma_f32 v[74:75], v[62:63], s[34:35], v[134:135] op_sel_hi:[1,0,1]
	v_pk_fma_f32 v[76:77], v[250:251], s[34:35], v[138:139] op_sel_hi:[1,0,1]
	v_min_f32_e32 v74, v74, v34
	v_min_f32_e32 v75, v75, v34
	v_pk_mul_f32 v[78:79], s[30:31], v[74:75] op_sel_hi:[0,1]
	v_exp_f32_e32 v78, v78
	v_exp_f32_e32 v79, v79
	v_med3_f32 v76, v76, -s1, s1
	v_med3_f32 v77, v77, -s1, s1
	v_pk_fma_f32 v[76:77], s[0:1], v[76:77], s[0:1] op_sel_hi:[0,1,0]
	v_pk_add_f32 v[78:79], s[2:3], v[78:79] op_sel_hi:[0,1]
	v_rcp_f32_e32 v78, v78
	v_rcp_f32_e32 v79, v79
	s_nop 0
	v_pk_mul_f32 v[74:75], v[74:75], v[78:79]
	v_mov_b32_e32 v78, v35
	v_mov_b32_e32 v79, v35
	v_cvt_pk_fp8_f32 v78, v68, v69
	v_cvt_pk_fp8_f32 v79, v72, v73
	v_pk_mul_f32 v[74:75], v[76:77], v[74:75]
	v_add_u32_e32 v76, 0x80, v152
	v_cvt_pk_fp8_f32 v78, v70, v71 op_sel:[0,0,1]
	v_cvt_pk_fp8_f32 v79, v74, v75 op_sel:[0,0,1]
	v_ashrrev_i32_e32 v77, 31, v76
	v_lshlrev_b64 v[68:69], 10, v[76:77]
	v_lshl_add_u64 v[68:69], v[150:151], 0, v[68:69]
	global_store_dwordx2 v[68:69], v[78:79], off sc1
	v_pk_fma_f32 v[68:69], v[56:57], s[34:35], v[140:141] op_sel_hi:[1,0,1]
	v_pk_fma_f32 v[70:71], v[22:23], s[34:35], v[144:145] op_sel_hi:[1,0,1]
	v_min_f32_e32 v68, v68, v34
	v_min_f32_e32 v69, v69, v34
	v_pk_mul_f32 v[72:73], s[30:31], v[68:69] op_sel_hi:[0,1]
	v_exp_f32_e32 v72, v72
	v_exp_f32_e32 v73, v73
	v_med3_f32 v70, v70, -s1, s1
	v_med3_f32 v71, v71, -s1, s1
	v_pk_fma_f32 v[70:71], s[0:1], v[70:71], s[0:1] op_sel_hi:[0,1,0]
	v_pk_add_f32 v[72:73], s[2:3], v[72:73] op_sel_hi:[0,1]
	v_rcp_f32_e32 v72, v72
	v_rcp_f32_e32 v73, v73
	s_nop 0
	v_pk_mul_f32 v[68:69], v[68:69], v[72:73]
	s_nop 0
	v_pk_mul_f32 v[68:69], v[70:71], v[68:69]
	v_pk_fma_f32 v[70:71], v[58:59], s[34:35], v[142:143] op_sel_hi:[1,0,1]
	v_pk_fma_f32 v[72:73], v[24:25], s[34:35], v[146:147] op_sel_hi:[1,0,1]
	v_min_f32_e32 v70, v70, v34
	v_min_f32_e32 v71, v71, v34
	v_pk_mul_f32 v[74:75], s[30:31], v[70:71] op_sel_hi:[0,1]
	v_exp_f32_e32 v74, v74
	v_exp_f32_e32 v75, v75
	v_med3_f32 v72, v72, -s1, s1
	v_med3_f32 v73, v73, -s1, s1
	v_pk_fma_f32 v[72:73], s[0:1], v[72:73], s[0:1] op_sel_hi:[0,1,0]
; __device__ __forceinline__ unsigned cvt_pk4_fp8(float a, float b, float c, float d) { int w = 0; w = __builtin_amdgcn_cvt_pk_fp8_f32(a, b, w, false); w = __builtin_amdgcn_cvt_pk_fp8_f32(c, d, w, true); return (unsigned)w; }
; #define GAS __attribute__((address_space(1)))
;     __device__ __forceinline__ void operator()(const f32x4 (&acc)[2][2][4][2], const Unit& u, int wr, int wc, int fr, int fq, LAS unsigned char* lds, int par) const {
;     ...
;         for (int ai = 0; ai < 2; ++ai)
; #pragma unroll
;             for (int m = 0; m < 4; ++m) {
;                 const int r = u.rt * BM + ai * HALF + wr * 64 + m * 16 + fr;
;                 f32x2_t o[4];
; #pragma unroll
;                 for (int n = 0; n < 2; ++n)
; #pragma unroll
;                     for (int h = 0; h < 2; ++h) {
;                         const f32x4 bgv = n ? bg1 : bg0, blv = n ? bl1 : bl0;
;                         f32x2_t glu = (f32x2_t){acc[ai][0][m][n][2 * h], acc[ai][0][m][n][2 * h + 1]} * sc2 + (f32x2_t){bgv[2 * h], bgv[2 * h + 1]};
;                         f32x2_t lin = (f32x2_t){acc[ai][1][m][n][2 * h], acc[ai][1][m][n][2 * h + 1]} * sc2 + (f32x2_t){blv[2 * h], blv[2 * h + 1]};
;                         glu.x = fminf(glu.x, lim); glu.y = fminf(glu.y, lim);
;                         lin.x = __builtin_amdgcn_fmed3f(lin.x, -lim, lim); lin.y = __builtin_amdgcn_fmed3f(lin.y, -lim, lim);
;                         const f32x2_t t = glu * ke2;
;                         const f32x2_t d = (f32x2_t){__builtin_amdgcn_exp2f(t.x), __builtin_amdgcn_exp2f(t.y)} + one2;
;                         const f32x2_t rc = (f32x2_t){__builtin_amdgcn_rcpf(d.x), __builtin_amdgcn_rcpf(d.y)};
;                         o[n * 2 + h] = (glu * rc) * (lin * as2 + as2);
;                     }
;                 const int ro = u.rowbase + r;
;                 u32x2 w; w.x = cvt_pk4_fp8(o[0].x, o[0].y, o[1].x, o[1].y); w.y = cvt_pk4_fp8(o[2].x, o[2].y, o[3].x, o[3].y);
;                 __hip_atomic_store((unsigned long long GAS*)(act + (size_t)ro * DFF + col), ((unsigned long long)w.y << 32) | w.x, __ATOMIC_RELAXED, __HIP_MEMORY_SCOPE_AGENT);
;             }
	v_pk_add_f32 v[74:75], s[2:3], v[74:75] op_sel_hi:[0,1]
	v_rcp_f32_e32 v74, v74
	v_rcp_f32_e32 v75, v75
	s_nop 0
	v_pk_mul_f32 v[70:71], v[70:71], v[74:75]
	s_nop 0
	v_pk_mul_f32 v[70:71], v[72:73], v[70:71]
	v_pk_fma_f32 v[72:73], v[236:237], s[34:35], v[132:133] op_sel_hi:[1,0,1]
	v_pk_fma_f32 v[74:75], v[18:19], s[34:35], v[136:137] op_sel_hi:[1,0,1]
	v_min_f32_e32 v72, v72, v34
	v_min_f32_e32 v73, v73, v34
	v_pk_mul_f32 v[76:77], s[30:31], v[72:73] op_sel_hi:[0,1]
	v_exp_f32_e32 v76, v76
	v_exp_f32_e32 v77, v77
	v_med3_f32 v74, v74, -s1, s1
	v_med3_f32 v75, v75, -s1, s1
	v_pk_fma_f32 v[74:75], s[0:1], v[74:75], s[0:1] op_sel_hi:[0,1,0]
	v_pk_add_f32 v[76:77], s[2:3], v[76:77] op_sel_hi:[0,1]
	v_rcp_f32_e32 v76, v76
	v_rcp_f32_e32 v77, v77
	s_nop 0
	v_pk_mul_f32 v[72:73], v[72:73], v[76:77]
	s_nop 0
	v_pk_mul_f32 v[72:73], v[74:75], v[72:73]
	v_pk_fma_f32 v[74:75], v[238:239], s[34:35], v[134:135] op_sel_hi:[1,0,1]
	v_pk_fma_f32 v[76:77], v[20:21], s[34:35], v[138:139] op_sel_hi:[1,0,1]
	v_min_f32_e32 v74, v74, v34
	v_min_f32_e32 v75, v75, v34
	v_pk_mul_f32 v[78:79], s[30:31], v[74:75] op_sel_hi:[0,1]
	v_exp_f32_e32 v78, v78
	v_exp_f32_e32 v79, v79
	v_med3_f32 v76, v76, -s1, s1
	v_med3_f32 v77, v77, -s1, s1
	v_pk_fma_f32 v[76:77], s[0:1], v[76:77], s[0:1] op_sel_hi:[0,1,0]
	v_pk_add_f32 v[78:79], s[2:3], v[78:79] op_sel_hi:[0,1]
	v_rcp_f32_e32 v78, v78
	v_rcp_f32_e32 v79, v79
	s_nop 0
	v_pk_mul_f32 v[74:75], v[74:75], v[78:79]
	v_mov_b32_e32 v78, v35
	v_mov_b32_e32 v79, v35
	v_cvt_pk_fp8_f32 v78, v68, v69
	v_cvt_pk_fp8_f32 v79, v72, v73
	v_pk_mul_f32 v[74:75], v[76:77], v[74:75]
	v_add_u32_e32 v76, 0x90, v152
	v_cvt_pk_fp8_f32 v78, v70, v71 op_sel:[0,0,1]
	v_cvt_pk_fp8_f32 v79, v74, v75 op_sel:[0,0,1]
	v_ashrrev_i32_e32 v77, 31, v76
	v_lshlrev_b64 v[68:69], 10, v[76:77]
	v_lshl_add_u64 v[68:69], v[150:151], 0, v[68:69]
	global_store_dwordx2 v[68:69], v[78:79], off sc1
	v_pk_fma_f32 v[68:69], v[48:49], s[34:35], v[140:141] op_sel_hi:[1,0,1]
	v_pk_fma_f32 v[70:71], v[14:15], s[34:35], v[144:145] op_sel_hi:[1,0,1]
	v_min_f32_e32 v68, v68, v34
	v_min_f32_e32 v69, v69, v34
	v_pk_mul_f32 v[72:73], s[30:31], v[68:69] op_sel_hi:[0,1]
	v_exp_f32_e32 v72, v72
	v_exp_f32_e32 v73, v73
	v_med3_f32 v70, v70, -s1, s1
	v_med3_f32 v71, v71, -s1, s1
	v_pk_fma_f32 v[70:71], s[0:1], v[70:71], s[0:1] op_sel_hi:[0,1,0]
	v_pk_add_f32 v[72:73], s[2:3], v[72:73] op_sel_hi:[0,1]
	v_rcp_f32_e32 v72, v72
	v_rcp_f32_e32 v73, v73
	s_nop 0
	v_pk_mul_f32 v[68:69], v[68:69], v[72:73]
	s_nop 0
	v_pk_mul_f32 v[68:69], v[70:71], v[68:69]
	v_pk_fma_f32 v[70:71], v[50:51], s[34:35], v[142:143] op_sel_hi:[1,0,1]
	v_pk_fma_f32 v[72:73], v[16:17], s[34:35], v[146:147] op_sel_hi:[1,0,1]
	v_min_f32_e32 v70, v70, v34
	v_min_f32_e32 v71, v71, v34
	v_pk_mul_f32 v[74:75], s[30:31], v[70:71] op_sel_hi:[0,1]
	v_exp_f32_e32 v74, v74
	v_exp_f32_e32 v75, v75
	v_med3_f32 v72, v72, -s1, s1
	v_med3_f32 v73, v73, -s1, s1
	v_pk_fma_f32 v[72:73], s[0:1], v[72:73], s[0:1] op_sel_hi:[0,1,0]
	v_pk_add_f32 v[74:75], s[2:3], v[74:75] op_sel_hi:[0,1]
	v_rcp_f32_e32 v74, v74
	v_rcp_f32_e32 v75, v75
	s_nop 0
	v_pk_mul_f32 v[70:71], v[70:71], v[74:75]
	s_nop 0
	v_pk_mul_f32 v[70:71], v[72:73], v[70:71]
	v_pk_fma_f32 v[72:73], v[44:45], s[34:35], v[132:133] op_sel_hi:[1,0,1]
	v_pk_fma_f32 v[74:75], v[10:11], s[34:35], v[136:137] op_sel_hi:[1,0,1]
	v_min_f32_e32 v72, v72, v34
	v_min_f32_e32 v73, v73, v34
	v_pk_mul_f32 v[76:77], s[30:31], v[72:73] op_sel_hi:[0,1]
	v_exp_f32_e32 v76, v76
	v_exp_f32_e32 v77, v77
	v_med3_f32 v74, v74, -s1, s1
	v_med3_f32 v75, v75, -s1, s1
	v_pk_fma_f32 v[74:75], s[0:1], v[74:75], s[0:1] op_sel_hi:[0,1,0]
	v_pk_add_f32 v[76:77], s[2:3], v[76:77] op_sel_hi:[0,1]
	v_rcp_f32_e32 v76, v76
	v_rcp_f32_e32 v77, v77
	s_nop 0
	v_pk_mul_f32 v[72:73], v[72:73], v[76:77]
	s_nop 0
	v_pk_mul_f32 v[72:73], v[74:75], v[72:73]
	v_pk_fma_f32 v[74:75], v[46:47], s[34:35], v[134:135] op_sel_hi:[1,0,1]
	v_pk_fma_f32 v[76:77], v[12:13], s[34:35], v[138:139] op_sel_hi:[1,0,1]
	v_min_f32_e32 v74, v74, v34
	v_min_f32_e32 v75, v75, v34
	v_pk_mul_f32 v[78:79], s[30:31], v[74:75] op_sel_hi:[0,1]
; #define GAS __attribute__((address_space(1)))
; template <class Epi, class Src>
; __device__ __forceinline__ void gemm_phase(LAS unsigned char* lds, const Src S, const Epi E) {
;     ...
; #pragma unroll
;         for (int a = 0; a < 2; ++a)
; #pragma unroll
;             for (int b = 0; b < 2; ++b)
; #pragma unroll
;                 for (int m = 0; m < 4; ++m)
; #pragma unroll
;                     for (int n = 0; n < 2; ++n) acc[a][b][m][n] = (f32x4){0.f, 0.f, 0.f, 0.f};
;         cur = nxt; cB = nB; cA = nA; ++ui; par ^= 1;
;     __device__ __forceinline__ void operator()(const f32x4 (&acc)[2][2][4][2], const Unit& u, int wr, int wc, int fr, int fq, LAS unsigned char* lds, int par) const {
;     ...
;         for (int ai = 0; ai < 2; ++ai)
; #pragma unroll
;             for (int m = 0; m < 4; ++m) {
;                 const int r = u.rt * BM + ai * HALF + wr * 64 + m * 16 + fr;
;                 f32x2_t o[4];
; #pragma unroll
;                 for (int n = 0; n < 2; ++n)
; #pragma unroll
;                     for (int h = 0; h < 2; ++h) {
;                         const f32x4 bgv = n ? bg1 : bg0, blv = n ? bl1 : bl0;
;                         f32x2_t glu = (f32x2_t){acc[ai][0][m][n][2 * h], acc[ai][0][m][n][2 * h + 1]} * sc2 + (f32x2_t){bgv[2 * h], bgv[2 * h + 1]};
;                         f32x2_t lin = (f32x2_t){acc[ai][1][m][n][2 * h], acc[ai][1][m][n][2 * h + 1]} * sc2 + (f32x2_t){blv[2 * h], blv[2 * h + 1]};
;                         glu.x = fminf(glu.x, lim); glu.y = fminf(glu.y, lim);
;                         lin.x = __builtin_amdgcn_fmed3f(lin.x, -lim, lim); lin.y = __builtin_amdgcn_fmed3f(lin.y, -lim, lim);
;                         const f32x2_t t = glu * ke2;
;                         const f32x2_t d = (f32x2_t){__builtin_amdgcn_exp2f(t.x), __builtin_amdgcn_exp2f(t.y)} + one2;
;                         const f32x2_t rc = (f32x2_t){__builtin_amdgcn_rcpf(d.x), __builtin_amdgcn_rcpf(d.y)};
;                         o[n * 2 + h] = (glu * rc) * (lin * as2 + as2);
;                     }
;                 const int ro = u.rowbase + r;
;                 u32x2 w; w.x = cvt_pk4_fp8(o[0].x, o[0].y, o[1].x, o[1].y); w.y = cvt_pk4_fp8(o[2].x, o[2].y, o[3].x, o[3].y);
;                 __hip_atomic_store((unsigned long long GAS*)(act + (size_t)ro * DFF + col), ((unsigned long long)w.y << 32) | w.x, __ATOMIC_RELAXED, __HIP_MEMORY_SCOPE_AGENT);
;             }
	v_exp_f32_e32 v78, v78
	v_exp_f32_e32 v79, v79
	v_med3_f32 v76, v76, -s1, s1
	v_med3_f32 v77, v77, -s1, s1
	v_pk_fma_f32 v[76:77], s[0:1], v[76:77], s[0:1] op_sel_hi:[0,1,0]
	v_pk_add_f32 v[78:79], s[2:3], v[78:79] op_sel_hi:[0,1]
	v_rcp_f32_e32 v78, v78
	v_rcp_f32_e32 v79, v79
	s_nop 0
	v_pk_mul_f32 v[74:75], v[74:75], v[78:79]
	v_mov_b32_e32 v78, v35
	v_mov_b32_e32 v79, v35
	v_cvt_pk_fp8_f32 v78, v68, v69
	v_cvt_pk_fp8_f32 v79, v72, v73
	v_pk_mul_f32 v[74:75], v[76:77], v[74:75]
	v_add_u32_e32 v76, 0xa0, v152
	v_cvt_pk_fp8_f32 v78, v70, v71 op_sel:[0,0,1]
	v_cvt_pk_fp8_f32 v79, v74, v75 op_sel:[0,0,1]
	v_ashrrev_i32_e32 v77, 31, v76
	v_lshlrev_b64 v[68:69], 10, v[76:77]
	v_lshl_add_u64 v[68:69], v[150:151], 0, v[68:69]
	global_store_dwordx2 v[68:69], v[78:79], off sc1
	v_pk_fma_f32 v[68:69], v[6:7], s[34:35], v[140:141] op_sel_hi:[1,0,1]
	v_pk_fma_f32 v[70:71], v[92:93], s[34:35], v[144:145] op_sel_hi:[1,0,1]
	v_min_f32_e32 v68, v68, v34
	v_min_f32_e32 v69, v69, v34
	v_pk_mul_f32 v[72:73], s[30:31], v[68:69] op_sel_hi:[0,1]
	v_exp_f32_e32 v72, v72
	v_exp_f32_e32 v73, v73
	v_med3_f32 v70, v70, -s1, s1
	v_med3_f32 v71, v71, -s1, s1
	v_pk_fma_f32 v[70:71], s[0:1], v[70:71], s[0:1] op_sel_hi:[0,1,0]
	v_pk_add_f32 v[72:73], s[2:3], v[72:73] op_sel_hi:[0,1]
	v_rcp_f32_e32 v72, v72
	v_rcp_f32_e32 v73, v73
	s_nop 0
	v_pk_mul_f32 v[68:69], v[68:69], v[72:73]
	s_nop 0
	v_pk_mul_f32 v[68:69], v[70:71], v[68:69]
	v_pk_fma_f32 v[70:71], v[8:9], s[34:35], v[142:143] op_sel_hi:[1,0,1]
	v_pk_fma_f32 v[72:73], v[94:95], s[34:35], v[146:147] op_sel_hi:[1,0,1]
	v_min_f32_e32 v70, v70, v34
	v_min_f32_e32 v71, v71, v34
	v_pk_mul_f32 v[74:75], s[30:31], v[70:71] op_sel_hi:[0,1]
	v_exp_f32_e32 v74, v74
	v_exp_f32_e32 v75, v75
	v_med3_f32 v72, v72, -s1, s1
	v_med3_f32 v73, v73, -s1, s1
	v_pk_fma_f32 v[72:73], s[0:1], v[72:73], s[0:1] op_sel_hi:[0,1,0]
	v_pk_add_f32 v[74:75], s[2:3], v[74:75] op_sel_hi:[0,1]
	v_rcp_f32_e32 v74, v74
	v_rcp_f32_e32 v75, v75
	s_nop 0
	v_pk_mul_f32 v[70:71], v[70:71], v[74:75]
	s_nop 0
	v_pk_mul_f32 v[70:71], v[72:73], v[70:71]
	v_pk_fma_f32 v[72:73], v[244:245], s[34:35], v[132:133] op_sel_hi:[1,0,1]
	v_pk_fma_f32 v[74:75], v[2:3], s[34:35], v[136:137] op_sel_hi:[1,0,1]
	v_min_f32_e32 v72, v72, v34
	v_min_f32_e32 v73, v73, v34
	v_pk_mul_f32 v[76:77], s[30:31], v[72:73] op_sel_hi:[0,1]
	v_exp_f32_e32 v76, v76
	v_exp_f32_e32 v77, v77
	v_med3_f32 v74, v74, -s1, s1
	v_med3_f32 v75, v75, -s1, s1
	v_pk_fma_f32 v[74:75], s[0:1], v[74:75], s[0:1] op_sel_hi:[0,1,0]
	v_pk_add_f32 v[76:77], s[2:3], v[76:77] op_sel_hi:[0,1]
	v_rcp_f32_e32 v76, v76
	v_rcp_f32_e32 v77, v77
	s_nop 0
	v_pk_mul_f32 v[72:73], v[72:73], v[76:77]
	s_nop 0
	v_pk_mul_f32 v[72:73], v[74:75], v[72:73]
	v_pk_fma_f32 v[74:75], v[246:247], s[34:35], v[134:135] op_sel_hi:[1,0,1]
	v_pk_fma_f32 v[76:77], v[4:5], s[34:35], v[138:139] op_sel_hi:[1,0,1]
	v_min_f32_e32 v74, v74, v34
	v_min_f32_e32 v75, v75, v34
	v_pk_mul_f32 v[78:79], s[30:31], v[74:75] op_sel_hi:[0,1]
	v_exp_f32_e32 v78, v78
	v_exp_f32_e32 v79, v79
	v_med3_f32 v76, v76, -s1, s1
	v_med3_f32 v77, v77, -s1, s1
	v_pk_fma_f32 v[76:77], s[0:1], v[76:77], s[0:1] op_sel_hi:[0,1,0]
	v_pk_add_f32 v[78:79], s[2:3], v[78:79] op_sel_hi:[0,1]
	v_rcp_f32_e32 v78, v78
	v_rcp_f32_e32 v79, v79
	s_nop 0
	v_pk_mul_f32 v[74:75], v[74:75], v[78:79]
	v_mov_b32_e32 v78, v35
	v_mov_b32_e32 v79, v35
	v_cvt_pk_fp8_f32 v78, v68, v69
	v_cvt_pk_fp8_f32 v79, v72, v73
	v_pk_mul_f32 v[74:75], v[76:77], v[74:75]
	v_add_u32_e32 v76, 0xb0, v152
	v_cvt_pk_fp8_f32 v78, v70, v71 op_sel:[0,0,1]
	v_cvt_pk_fp8_f32 v79, v74, v75 op_sel:[0,0,1]
	v_ashrrev_i32_e32 v77, 31, v76
	v_lshlrev_b64 v[68:69], 10, v[76:77]
	v_lshl_add_u64 v[68:69], v[150:151], 0, v[68:69]
	global_store_dwordx2 v[68:69], v[78:79], off sc1
	s_cbranch_vccnz .LBB0_1371
	s_mov_b32 s39, s71
	s_mov_b32 s18, s26
	s_mov_b32 s38, s70
	s_mov_b32 s16, s22
	s_mov_b32 s68, s3
	s_mov_b64 s[20:21], s[28:29]
	s_mov_b32 s57, s72
	s_xor_b64 s[0:1], s[24:25], -1
	s_andn2_b64 vcc, exec, s[0:1]
	s_cbranch_vccnz .LBB0_1372
	s_branch .LBB0_1373

; __global__ void __launch_bounds__(512, 2) fwd(Args a) {
;     extern __shared__ __attribute__((aligned(16))) unsigned char lds_raw[];
	.amdhsa_kernel _ZN12_GLOBAL__N_13fwdENS_4ArgsE
		.amdhsa_group_segment_fixed_size 0
		.amdhsa_private_segment_fixed_size 0
		.amdhsa_kernarg_size 440
		.amdhsa_user_sgpr_count 2
		.amdhsa_user_sgpr_dispatch_ptr 0
		.amdhsa_user_sgpr_queue_ptr 0
		.amdhsa_user_sgpr_kernarg_segment_ptr 1
		.amdhsa_user_sgpr_dispatch_id 0
		.amdhsa_user_sgpr_kernarg_preload_length 0
		.amdhsa_user_sgpr_kernarg_preload_offset 0
		.amdhsa_user_sgpr_private_segment_size 0
		.amdhsa_uses_dynamic_stack 0
		.amdhsa_enable_private_segment 0
		.amdhsa_system_sgpr_workgroup_id_x 1
		.amdhsa_system_sgpr_workgroup_id_y 0
		.amdhsa_system_sgpr_workgroup_id_z 0
		.amdhsa_system_sgpr_workgroup_info 0
		.amdhsa_system_vgpr_workitem_id 0
		.amdhsa_next_free_vgpr 256
		.amdhsa_next_free_sgpr 100
		.amdhsa_accum_offset 256
		.amdhsa_reserve_vcc 1
		.amdhsa_float_round_mode_32 0
		.amdhsa_float_round_mode_16_64 0
		.amdhsa_float_denorm_mode_32 3
		.amdhsa_float_denorm_mode_16_64 3
		.amdhsa_dx10_clamp 1
		.amdhsa_ieee_mode 1
		.amdhsa_fp16_overflow 0
		.amdhsa_tg_split 0
		.amdhsa_exception_fp_ieee_invalid_op 0
		.amdhsa_exception_fp_denorm_src 0
		.amdhsa_exception_fp_ieee_div_zero 0
		.amdhsa_exception_fp_ieee_overflow 0
		.amdhsa_exception_fp_ieee_underflow 0
		.amdhsa_exception_fp_ieee_inexact 0
		.amdhsa_exception_int_div_zero 0
	.end_amdhsa_kernel

; __global__ void __launch_bounds__(512, 2) fwd(Args a) {
;     extern __shared__ __attribute__((aligned(16))) unsigned char lds_raw[];
amdhsa.kernels:
  - .agpr_count:     0
    .args:
      - .offset:         0
        .size:           184
        .value_kind:     by_value
      - .offset:         184
        .size:           4
        .value_kind:     hidden_block_count_x
      - .offset:         188
        .size:           4
        .value_kind:     hidden_block_count_y
      - .offset:         192
        .size:           4
        .value_kind:     hidden_block_count_z
      - .offset:         196
        .size:           2
        .value_kind:     hidden_group_size_x
      - .offset:         198
        .size:           2
        .value_kind:     hidden_group_size_y
      - .offset:         200
        .size:           2
        .value_kind:     hidden_group_size_z
      - .offset:         202
        .size:           2
        .value_kind:     hidden_remainder_x
      - .offset:         204
        .size:           2
        .value_kind:     hidden_remainder_y
      - .offset:         206
        .size:           2
        .value_kind:     hidden_remainder_z
      - .offset:         224
        .size:           8
        .value_kind:     hidden_global_offset_x
      - .offset:         232
        .size:           8
        .value_kind:     hidden_global_offset_y
      - .offset:         240
        .size:           8
        .value_kind:     hidden_global_offset_z
      - .offset:         248
        .size:           2
        .value_kind:     hidden_grid_dims
      - .offset:         304
        .size:           4
        .value_kind:     hidden_dynamic_lds_size
    .group_segment_fixed_size: 0
    .kernarg_segment_align: 8
    .kernarg_segment_size: 440
    .language:       OpenCL C
    .language_version:
      - 2
      - 0
    .max_flat_workgroup_size: 512
    .name:           _ZN12_GLOBAL__N_13fwdENS_4ArgsE
    .private_segment_fixed_size: 0
    .sgpr_count:     106
    .sgpr_spill_count: 36
    .symbol:         _ZN12_GLOBAL__N_13fwdENS_4ArgsE.kd
    .uniform_work_group_size: 1
    .uses_dynamic_stack: false
    .vgpr_count:     256
    .vgpr_spill_count: 0
    .wavefront_size: 64
